# routing: per-token expert rank loop visits only the 32 experts of the four kept groups (group bases from s_ff1 on group rank == r)
# speedup vs baseline: 1.0070x; 1.0004x over previous
; #define LAS __attribute__((address_space(3)))
; __device__ __forceinline__ void phase_nrr(const Frame& F, const Args& a, int l, const bf16_t* XA, const float* g, const float* modl, unsigned char* XN8) {
;     ...
;         __syncthreads();
; #pragma unroll
;         for (int rb = 0; rb < 4; ++rb) *(LAS f32x4*)(Pl + (size_t)((kq * 64 + 16 * rb + fr) * NE + 16 * eb + 4 * fq)) = acc[rb];
;         __syncthreads();
;         const float bias = rbias[lane];
; #pragma unroll
;         for (int i = 0; i < 8; ++i) { const int t = tb + i;
;             const float lg = Pl[(w * 8 + i) * NE + lane] + Pl[(64 + w * 8 + i) * NE + lane]; const float sc = 1.f / (1.f + __expf(-lg)); const float bb = sc + bias;
;             float m1 = bb; m1 = fmaxf(m1, __shfl_xor(m1, 1)); m1 = fmaxf(m1, __shfl_xor(m1, 2)); m1 = fmaxf(m1, __shfl_xor(m1, 4));
;             const unsigned long long eq = __ballot(bb == m1); const int gbase = lane & ~7; const unsigned grpmask = (unsigned)((eq >> gbase) & 0xffull);
;             const int first = gbase + __builtin_ctz(grpmask);
;             float m2 = (lane == first) ? -INFINITY : bb; m2 = fmaxf(m2, __shfl_xor(m2, 1)); m2 = fmaxf(m2, __shfl_xor(m2, 2)); m2 = fmaxf(m2, __shfl_xor(m2, 4));
;             const float gsum = m1 + m2; const int gq = lane >> 3;
;             int grank = 0;
; #pragma unroll
;             for (int g2 = 0; g2 < 8; ++g2) { const float v = __int_as_float(__builtin_amdgcn_readlane(__float_as_int(gsum), g2 * 8)); grank += (v > gsum || (v == gsum && g2 < gq)) ? 1 : 0; }
;             const bool keep = grank < 4; const float val = keep ? bb : -INFINITY;
;             int rank = 0;
; #pragma unroll 8
;             for (int e2 = 0; e2 < 64; ++e2) { const float v = __int_as_float(__builtin_amdgcn_readlane(__float_as_int(val), e2)); rank += (v > val || (v == val && e2 < lane)) ? 1 : 0; }
.LBB0_535:
	s_barrier
	ds_write_b128 v242, v[110:113]
	ds_write_b128 v242, v[118:121] offset:4096
	s_nop 0
	ds_write_b128 v242, v[126:129] offset:8192
	s_nop 1
	ds_write_b128 v242, v[130:133] offset:12288
	s_waitcnt lgkmcnt(0)
	s_barrier
	global_load_dword v3, v[198:199], off
	s_waitcnt vmcnt(15)
	v_add_u32_e32 v4, s76, v226
	ds_read2st64_b32 v[6:7], v4 offset1:64
	s_mov_b32 s3, 0
	s_waitcnt lgkmcnt(0)
	v_add_f32_e32 v2, v6, v7
	v_mul_f32_e32 v2, 0xbfb8aa3b, v2
	v_exp_f32_e32 v2, v2
	s_nop 0
	v_add_f32_e32 v2, 1.0, v2
	v_div_scale_f32 v5, s[22:23], v2, v2, 1.0
	v_rcp_f32_e32 v6, v5
	s_nop 0
	v_fma_f32 v7, -v5, v6, 1.0
	v_fmac_f32_e32 v6, v7, v6
	v_div_scale_f32 v7, vcc, 1.0, v2, 1.0
	v_mul_f32_e32 v8, v7, v6
	v_fma_f32 v9, -v5, v8, v7
	v_fmac_f32_e32 v8, v9, v6
	v_fma_f32 v5, -v5, v8, v7
	v_div_fmas_f32 v5, v5, v6, v8
	v_div_fixup_f32 v2, v5, v2, 1.0
	s_waitcnt vmcnt(0)
	v_add_f32_e32 v5, v3, v2
	s_nop 1
	s_waitcnt lgkmcnt(0)
	v_max_f32_dpp v6, v5, v5 quad_perm:[1,0,3,2] row_mask:0xf bank_mask:0xf
	s_nop 1
	s_waitcnt lgkmcnt(0)
	v_max_f32_dpp v6, v6, v6 quad_perm:[2,3,0,1] row_mask:0xf bank_mask:0xf
	s_nop 1
	s_waitcnt lgkmcnt(0)
	v_max_f32_dpp v8, v6, v6 row_half_mirror row_mask:0xf bank_mask:0xf
	v_cmp_eq_f32_e32 vcc, v5, v8
	s_nop 1
	v_lshrrev_b64 v[6:7], v200, vcc
	v_ffbl_b32_sdwa v6, v6 dst_sel:DWORD dst_unused:UNUSED_PAD src0_sel:BYTE_0
	v_add_u32_e32 v6, v6, v200
	v_cmp_ne_u32_e32 vcc, v230, v6
	s_nop 1
	v_cndmask_b32_e32 v6, v245, v5, vcc
	s_nop 1
	s_waitcnt lgkmcnt(0)
	v_max_f32_dpp v6, v6, v6 quad_perm:[1,0,3,2] row_mask:0xf bank_mask:0xf
	s_nop 1
	s_waitcnt lgkmcnt(0)
	v_max_f32_dpp v6, v6, v6 quad_perm:[2,3,0,1] row_mask:0xf bank_mask:0xf
	s_nop 1
	s_waitcnt lgkmcnt(0)
	v_max_f32_dpp v6, v6, v6 row_half_mirror row_mask:0xf bank_mask:0xf
	v_add_f32_e32 v6, v8, v6
	s_nop 0
	v_readlane_b32 s5, v6, 0
	s_nop 1
	v_cmp_eq_f32_e64 s[22:23], s5, v6
	v_cmp_gt_f32_e32 vcc, s5, v6
	s_and_b64 s[22:23], s[6:7], s[22:23]
	s_or_b64 s[22:23], vcc, s[22:23]
	v_readlane_b32 s5, v6, 8
	v_cndmask_b32_e64 v7, 0, 1, s[22:23]
	s_nop 0
	v_cmp_eq_f32_e64 s[22:23], s5, v6
	v_cmp_gt_f32_e32 vcc, s5, v6
	s_and_b64 s[22:23], s[8:9], s[22:23]
	s_or_b64 s[22:23], vcc, s[22:23]
	v_readlane_b32 s5, v6, 16
	v_cndmask_b32_e64 v8, 0, 1, s[22:23]
	s_nop 0
	v_cmp_eq_f32_e64 s[22:23], s5, v6
	v_cmp_gt_f32_e32 vcc, s5, v6
	s_and_b64 s[22:23], s[10:11], s[22:23]
	s_or_b64 s[22:23], vcc, s[22:23]
	v_readlane_b32 s5, v6, 24
	v_cndmask_b32_e64 v9, 0, 1, s[22:23]
	s_nop 0
	v_cmp_eq_f32_e64 s[22:23], s5, v6
	v_cmp_gt_f32_e32 vcc, s5, v6
	s_and_b64 s[22:23], s[12:13], s[22:23]
	s_or_b64 s[22:23], vcc, s[22:23]
	v_readlane_b32 s5, v6, 32
	v_cndmask_b32_e64 v10, 0, 1, s[22:23]
	s_nop 0
	v_cmp_eq_f32_e64 s[22:23], s5, v6
	v_cmp_gt_f32_e32 vcc, s5, v6
	s_and_b64 s[22:23], s[14:15], s[22:23]
	s_or_b64 s[22:23], vcc, s[22:23]
	v_readlane_b32 s5, v6, 40
	v_cndmask_b32_e64 v11, 0, 1, s[22:23]
	s_nop 0
	v_cmp_eq_f32_e64 s[22:23], s5, v6
	v_cmp_gt_f32_e32 vcc, s5, v6
	s_and_b64 s[22:23], s[16:17], s[22:23]
	s_or_b64 s[22:23], vcc, s[22:23]
	v_readlane_b32 s5, v6, 48
	v_cndmask_b32_e64 v12, 0, 1, s[22:23]
	s_nop 0
	v_cmp_eq_f32_e64 s[22:23], s5, v6
	v_cmp_gt_f32_e32 vcc, s5, v6
	s_and_b64 s[22:23], s[18:19], s[22:23]
	v_readlane_b32 s5, v6, 56
	s_or_b64 s[22:23], vcc, s[22:23]
	v_cndmask_b32_e64 v13, 0, 1, s[22:23]
	v_cmp_gt_f32_e32 vcc, s5, v6
	s_nop 1
	v_cndmask_b32_e64 v6, 0, 1, vcc
	v_add_u32_e32 v6, v8, v6
	v_add3_u32 v6, v6, v7, v9
	v_add3_u32 v6, v6, v10, v11
	v_add3_u32 v6, v6, v12, v13
	v_cmp_eq_u32_e32 vcc, 0, v6
	s_ff1_i32_b64 s98, vcc
	v_cmp_eq_u32_e32 vcc, 1, v6
	s_ff1_i32_b64 s99, vcc
	v_cmp_eq_u32_e32 vcc, 2, v6
	s_ff1_i32_b64 s100, vcc
	v_cmp_eq_u32_e32 vcc, 3, v6
	s_ff1_i32_b64 s101, vcc
	v_cmp_gt_u32_e32 vcc, 4, v6
	v_mov_b32_e32 v6, 0
	s_nop 0
	v_cndmask_b32_e32 v5, v245, v5, vcc
	v_ashrrev_i32_e32 v9, 31, v5
	v_sub_u32_e32 v8, 63, v230
	v_and_b32_e32 v9, 0x7fffffff, v9
	v_xor_b32_e32 v9, v5, v9
	s_nop 0
	v_readlane_b32 s25, v9, s98
	s_sub_i32 s24, 63, s98
	s_add_i32 s98, s98, 1
	v_readlane_b32 s23, v9, s98
	s_sub_i32 s22, 63, s98
	s_add_i32 s98, s98, 1
	v_cmp_gt_i64_e32 vcc, s[24:25], v[8:9]
	v_readlane_b32 s25, v9, s98
	s_sub_i32 s24, 63, s98
	s_add_i32 s98, s98, 1
	v_addc_co_u32_e32 v6, vcc, 0, v6, vcc
	v_cmp_gt_i64_e32 vcc, s[22:23], v[8:9]
	v_readlane_b32 s23, v9, s98
	s_sub_i32 s22, 63, s98
	s_add_i32 s98, s98, 1
	v_addc_co_u32_e32 v6, vcc, 0, v6, vcc
	v_cmp_gt_i64_e32 vcc, s[24:25], v[8:9]
	v_readlane_b32 s25, v9, s98
	s_sub_i32 s24, 63, s98
	s_add_i32 s98, s98, 1
	v_addc_co_u32_e32 v6, vcc, 0, v6, vcc
	v_cmp_gt_i64_e32 vcc, s[22:23], v[8:9]
	v_readlane_b32 s23, v9, s98
	s_sub_i32 s22, 63, s98
	s_add_i32 s98, s98, 1
	v_addc_co_u32_e32 v6, vcc, 0, v6, vcc
	v_cmp_gt_i64_e32 vcc, s[24:25], v[8:9]
	v_readlane_b32 s25, v9, s98
	s_sub_i32 s24, 63, s98
	s_add_i32 s98, s98, 1
	v_addc_co_u32_e32 v6, vcc, 0, v6, vcc
	v_cmp_gt_i64_e32 vcc, s[22:23], v[8:9]
	v_readlane_b32 s23, v9, s98
	s_sub_i32 s22, 63, s98
	s_nop 0
	v_addc_co_u32_e32 v6, vcc, 0, v6, vcc
	v_cmp_gt_i64_e32 vcc, s[24:25], v[8:9]
	v_readlane_b32 s25, v9, s99
	s_sub_i32 s24, 63, s99
	s_add_i32 s99, s99, 1
	v_addc_co_u32_e32 v6, vcc, 0, v6, vcc
	v_cmp_gt_i64_e32 vcc, s[22:23], v[8:9]
	v_readlane_b32 s23, v9, s99
	s_sub_i32 s22, 63, s99
	s_add_i32 s99, s99, 1
	v_addc_co_u32_e32 v6, vcc, 0, v6, vcc
	v_cmp_gt_i64_e32 vcc, s[24:25], v[8:9]
	v_readlane_b32 s25, v9, s99
	s_sub_i32 s24, 63, s99
	s_add_i32 s99, s99, 1
	v_addc_co_u32_e32 v6, vcc, 0, v6, vcc
	v_cmp_gt_i64_e32 vcc, s[22:23], v[8:9]
	v_readlane_b32 s23, v9, s99
	s_sub_i32 s22, 63, s99
	s_add_i32 s99, s99, 1
	v_addc_co_u32_e32 v6, vcc, 0, v6, vcc
; __device__ __forceinline__ void phase_nrr(const Frame& F, const Args& a, int l, const bf16_t* XA, const float* g, const float* modl, unsigned char* XN8) {
;     ...
;             int rank = 0;
; #pragma unroll 8
;             for (int e2 = 0; e2 < 64; ++e2) { const float v = __int_as_float(__builtin_amdgcn_readlane(__float_as_int(val), e2)); rank += (v > val || (v == val && e2 < lane)) ? 1 : 0; }
;             const bool sel = rank < TOPK;
;             const float ssum = wave_sum(sel ? sc : 0.f);
;             if (sel) { const int p = atomicAdd((int*)(hist + lane), 1); top_e[t * TOPK + rank] = lane; gate[t * TOPK + rank] = sc / ssum * 2.5f; lpos[t * TOPK + rank] = p; }
	v_cmp_gt_i64_e32 vcc, s[24:25], v[8:9]
	v_readlane_b32 s25, v9, s99
	s_sub_i32 s24, 63, s99
	s_add_i32 s99, s99, 1
	v_addc_co_u32_e32 v6, vcc, 0, v6, vcc
	v_cmp_gt_i64_e32 vcc, s[22:23], v[8:9]
	v_readlane_b32 s23, v9, s99
	s_sub_i32 s22, 63, s99
	s_add_i32 s99, s99, 1
	v_addc_co_u32_e32 v6, vcc, 0, v6, vcc
	v_cmp_gt_i64_e32 vcc, s[24:25], v[8:9]
	v_readlane_b32 s25, v9, s99
	s_sub_i32 s24, 63, s99
	s_add_i32 s99, s99, 1
	v_addc_co_u32_e32 v6, vcc, 0, v6, vcc
	v_cmp_gt_i64_e32 vcc, s[22:23], v[8:9]
	v_readlane_b32 s23, v9, s99
	s_sub_i32 s22, 63, s99
	s_nop 0
	v_addc_co_u32_e32 v6, vcc, 0, v6, vcc
	v_cmp_gt_i64_e32 vcc, s[24:25], v[8:9]
	v_readlane_b32 s25, v9, s100
	s_sub_i32 s24, 63, s100
	s_add_i32 s100, s100, 1
	v_addc_co_u32_e32 v6, vcc, 0, v6, vcc
	v_cmp_gt_i64_e32 vcc, s[22:23], v[8:9]
	v_readlane_b32 s23, v9, s100
	s_sub_i32 s22, 63, s100
	s_add_i32 s100, s100, 1
	v_addc_co_u32_e32 v6, vcc, 0, v6, vcc
	v_cmp_gt_i64_e32 vcc, s[24:25], v[8:9]
	v_readlane_b32 s25, v9, s100
	s_sub_i32 s24, 63, s100
	s_add_i32 s100, s100, 1
	v_addc_co_u32_e32 v6, vcc, 0, v6, vcc
	v_cmp_gt_i64_e32 vcc, s[22:23], v[8:9]
	v_readlane_b32 s23, v9, s100
	s_sub_i32 s22, 63, s100
	s_add_i32 s100, s100, 1
	v_addc_co_u32_e32 v6, vcc, 0, v6, vcc
	v_cmp_gt_i64_e32 vcc, s[24:25], v[8:9]
	v_readlane_b32 s25, v9, s100
	s_sub_i32 s24, 63, s100
	s_add_i32 s100, s100, 1
	v_addc_co_u32_e32 v6, vcc, 0, v6, vcc
	v_cmp_gt_i64_e32 vcc, s[22:23], v[8:9]
	v_readlane_b32 s23, v9, s100
	s_sub_i32 s22, 63, s100
	s_add_i32 s100, s100, 1
	v_addc_co_u32_e32 v6, vcc, 0, v6, vcc
	v_cmp_gt_i64_e32 vcc, s[24:25], v[8:9]
	v_readlane_b32 s25, v9, s100
	s_sub_i32 s24, 63, s100
	s_add_i32 s100, s100, 1
	v_addc_co_u32_e32 v6, vcc, 0, v6, vcc
	v_cmp_gt_i64_e32 vcc, s[22:23], v[8:9]
	v_readlane_b32 s23, v9, s100
	s_sub_i32 s22, 63, s100
	s_nop 0
	v_addc_co_u32_e32 v6, vcc, 0, v6, vcc
	v_cmp_gt_i64_e32 vcc, s[24:25], v[8:9]
	v_readlane_b32 s25, v9, s101
	s_sub_i32 s24, 63, s101
	s_add_i32 s101, s101, 1
	v_addc_co_u32_e32 v6, vcc, 0, v6, vcc
	v_cmp_gt_i64_e32 vcc, s[22:23], v[8:9]
	v_readlane_b32 s23, v9, s101
	s_sub_i32 s22, 63, s101
	s_add_i32 s101, s101, 1
	v_addc_co_u32_e32 v6, vcc, 0, v6, vcc
	v_cmp_gt_i64_e32 vcc, s[24:25], v[8:9]
	v_readlane_b32 s25, v9, s101
	s_sub_i32 s24, 63, s101
	s_add_i32 s101, s101, 1
	v_addc_co_u32_e32 v6, vcc, 0, v6, vcc
	v_cmp_gt_i64_e32 vcc, s[22:23], v[8:9]
	v_readlane_b32 s23, v9, s101
	s_sub_i32 s22, 63, s101
	s_add_i32 s101, s101, 1
	v_addc_co_u32_e32 v6, vcc, 0, v6, vcc
	v_cmp_gt_i64_e32 vcc, s[24:25], v[8:9]
	v_readlane_b32 s25, v9, s101
	s_sub_i32 s24, 63, s101
	s_add_i32 s101, s101, 1
	v_addc_co_u32_e32 v6, vcc, 0, v6, vcc
	v_cmp_gt_i64_e32 vcc, s[22:23], v[8:9]
	v_readlane_b32 s23, v9, s101
	s_sub_i32 s22, 63, s101
	s_add_i32 s101, s101, 1
	v_addc_co_u32_e32 v6, vcc, 0, v6, vcc
	v_cmp_gt_i64_e32 vcc, s[24:25], v[8:9]
	v_readlane_b32 s25, v9, s101
	s_sub_i32 s24, 63, s101
	s_add_i32 s101, s101, 1
	v_addc_co_u32_e32 v6, vcc, 0, v6, vcc
	v_cmp_gt_i64_e32 vcc, s[22:23], v[8:9]
	v_readlane_b32 s23, v9, s101
	s_sub_i32 s22, 63, s101
	s_nop 0
	v_addc_co_u32_e32 v6, vcc, 0, v6, vcc
	v_cmp_gt_i64_e32 vcc, s[24:25], v[8:9]
	s_nop 1
	v_addc_co_u32_e32 v6, vcc, 0, v6, vcc
	v_cmp_gt_i64_e32 vcc, s[22:23], v[8:9]
	s_nop 1
	v_addc_co_u32_e32 v6, vcc, 0, v6, vcc
	v_cmp_gt_u32_e32 vcc, 6, v6
	s_mul_i32 s36, s44, 6
	s_nop 0
	v_cndmask_b32_e32 v5, 0, v2, vcc
	s_nop 1
	v_add_f32_dpp v5, v5, v5 quad_perm:[1,0,3,2] row_mask:0xf bank_mask:0xf
	s_nop 1
	v_add_f32_dpp v5, v5, v5 quad_perm:[2,3,0,1] row_mask:0xf bank_mask:0xf
	s_nop 1
	v_add_f32_dpp v5, v5, v5 row_half_mirror row_mask:0xf bank_mask:0xf
	s_nop 1
	v_add_f32_dpp v5, v5, v5 row_mirror row_mask:0xf bank_mask:0xf
	s_nop 0
	ds_bpermute_b32 v7, v222, v5
	s_waitcnt lgkmcnt(0)
	v_add_f32_e32 v5, v5, v7
	v_mov_b32_e32 v7, v5
	s_nop 1
	v_permlane32_swap_b32_e32 v7, v5
	s_and_saveexec_b64 s[22:23], vcc
	s_cbranch_execz .LBB0_539
	s_waitcnt lgkmcnt(0)
	v_add_f32_e32 v5, v5, v7
	v_div_scale_f32 v11, s[24:25], v5, v5, v2
	v_or_b32_e32 v6, s36, v6
	v_rcp_f32_e32 v12, v11
	v_ashrrev_i32_e32 v7, 31, v6
	v_lshlrev_b64 v[6:7], 2, v[6:7]
	v_lshl_add_u64 v[8:9], s[26:27], 0, v[6:7]
	ds_add_rtn_u32 v10, v227, v243
	global_store_dword v[8:9], v230, off
	v_fma_f32 v8, -v11, v12, 1.0
	v_fmac_f32_e32 v12, v8, v12
	v_div_scale_f32 v8, vcc, v2, v5, v2
	v_mul_f32_e32 v9, v8, v12
	v_fma_f32 v13, -v11, v9, v8
	v_fmac_f32_e32 v9, v13, v12
	v_fma_f32 v8, -v11, v9, v8
	v_div_fmas_f32 v8, v8, v12, v9
	v_div_fixup_f32 v2, v8, v5, v2
	v_mul_f32_e32 v2, 0x40200000, v2
	v_lshl_add_u64 v[8:9], s[28:29], 0, v[6:7]
	v_lshl_add_u64 v[6:7], s[30:31], 0, v[6:7]
	global_store_dword v[8:9], v2, off
	s_waitcnt lgkmcnt(0)
	global_store_dword v[6:7], v10, off
; __device__ __forceinline__ void phase_nrr(const Frame& F, const Args& a, int l, const bf16_t* XA, const float* g, const float* modl, unsigned char* XN8) {
;     ...
;         for (int i = 0; i < 8; ++i) { const int t = tb + i;
;             const float lg = Pl[(w * 8 + i) * NE + lane] + Pl[(64 + w * 8 + i) * NE + lane]; const float sc = 1.f / (1.f + __expf(-lg)); const float bb = sc + bias;
;             float m1 = bb; m1 = fmaxf(m1, __shfl_xor(m1, 1)); m1 = fmaxf(m1, __shfl_xor(m1, 2)); m1 = fmaxf(m1, __shfl_xor(m1, 4));
;             const unsigned long long eq = __ballot(bb == m1); const int gbase = lane & ~7; const unsigned grpmask = (unsigned)((eq >> gbase) & 0xffull);
;             const int first = gbase + __builtin_ctz(grpmask);
;             float m2 = (lane == first) ? -INFINITY : bb; m2 = fmaxf(m2, __shfl_xor(m2, 1)); m2 = fmaxf(m2, __shfl_xor(m2, 2)); m2 = fmaxf(m2, __shfl_xor(m2, 4));
;             const float gsum = m1 + m2; const int gq = lane >> 3;
;             int grank = 0;
; #pragma unroll
;             for (int g2 = 0; g2 < 8; ++g2) { const float v = __int_as_float(__builtin_amdgcn_readlane(__float_as_int(gsum), g2 * 8)); grank += (v > gsum || (v == gsum && g2 < gq)) ? 1 : 0; }
;             const bool keep = grank < 4; const float val = keep ? bb : -INFINITY;
;             int rank = 0;
; #pragma unroll 8
;             for (int e2 = 0; e2 < 64; ++e2) { const float v = __int_as_float(__builtin_amdgcn_readlane(__float_as_int(val), e2)); rank += (v > val || (v == val && e2 < lane)) ? 1 : 0; }
.LBB0_539:
	s_or_b64 exec, exec, s[22:23]
	v_add_u32_e32 v2, s77, v226
	ds_read_b32 v2, v2
	ds_read_b32 v5, v4 offset:16640
	s_mov_b32 s3, 0
	s_waitcnt lgkmcnt(0)
	v_add_f32_e32 v2, v2, v5
	v_mul_f32_e32 v2, 0xbfb8aa3b, v2
	v_exp_f32_e32 v2, v2
	s_nop 0
	v_add_f32_e32 v2, 1.0, v2
	v_div_scale_f32 v5, s[22:23], v2, v2, 1.0
	v_rcp_f32_e32 v6, v5
	s_nop 0
	v_fma_f32 v7, -v5, v6, 1.0
	v_fmac_f32_e32 v6, v7, v6
	v_div_scale_f32 v7, vcc, 1.0, v2, 1.0
	v_mul_f32_e32 v8, v7, v6
	v_fma_f32 v9, -v5, v8, v7
	v_fmac_f32_e32 v8, v9, v6
	v_fma_f32 v5, -v5, v8, v7
	v_div_fmas_f32 v5, v5, v6, v8
	v_div_fixup_f32 v5, v5, v2, 1.0
	v_add_f32_e32 v2, v3, v5
	s_nop 1
	s_waitcnt lgkmcnt(0)
	v_max_f32_dpp v6, v2, v2 quad_perm:[1,0,3,2] row_mask:0xf bank_mask:0xf
	s_nop 1
	s_waitcnt lgkmcnt(0)
	v_max_f32_dpp v6, v6, v6 quad_perm:[2,3,0,1] row_mask:0xf bank_mask:0xf
	s_nop 1
	s_waitcnt lgkmcnt(0)
	v_max_f32_dpp v8, v6, v6 row_half_mirror row_mask:0xf bank_mask:0xf
	v_cmp_eq_f32_e32 vcc, v2, v8
	s_nop 1
	v_lshrrev_b64 v[6:7], v200, vcc
	v_ffbl_b32_sdwa v6, v6 dst_sel:DWORD dst_unused:UNUSED_PAD src0_sel:BYTE_0
	v_add_u32_e32 v6, v6, v200
	v_cmp_ne_u32_e32 vcc, v230, v6
	s_nop 1
	v_cndmask_b32_e32 v6, v245, v2, vcc
	s_nop 1
	s_waitcnt lgkmcnt(0)
	v_max_f32_dpp v6, v6, v6 quad_perm:[1,0,3,2] row_mask:0xf bank_mask:0xf
	s_nop 1
	s_waitcnt lgkmcnt(0)
	v_max_f32_dpp v6, v6, v6 quad_perm:[2,3,0,1] row_mask:0xf bank_mask:0xf
	s_nop 1
	s_waitcnt lgkmcnt(0)
	v_max_f32_dpp v6, v6, v6 row_half_mirror row_mask:0xf bank_mask:0xf
	v_add_f32_e32 v6, v8, v6
	s_nop 0
	v_readlane_b32 s5, v6, 0
	s_nop 1
	v_cmp_eq_f32_e64 s[22:23], s5, v6
	v_cmp_gt_f32_e32 vcc, s5, v6
	s_and_b64 s[22:23], s[6:7], s[22:23]
	s_or_b64 s[22:23], vcc, s[22:23]
	v_readlane_b32 s5, v6, 8
	v_cndmask_b32_e64 v7, 0, 1, s[22:23]
	s_nop 0
	v_cmp_eq_f32_e64 s[22:23], s5, v6
	v_cmp_gt_f32_e32 vcc, s5, v6
	s_and_b64 s[22:23], s[8:9], s[22:23]
	s_or_b64 s[22:23], vcc, s[22:23]
	v_readlane_b32 s5, v6, 16
	v_cndmask_b32_e64 v8, 0, 1, s[22:23]
	s_nop 0
	v_cmp_eq_f32_e64 s[22:23], s5, v6
	v_cmp_gt_f32_e32 vcc, s5, v6
	s_and_b64 s[22:23], s[10:11], s[22:23]
	s_or_b64 s[22:23], vcc, s[22:23]
	v_readlane_b32 s5, v6, 24
	v_cndmask_b32_e64 v9, 0, 1, s[22:23]
	s_nop 0
	v_cmp_eq_f32_e64 s[22:23], s5, v6
	v_cmp_gt_f32_e32 vcc, s5, v6
	s_and_b64 s[22:23], s[12:13], s[22:23]
	s_or_b64 s[22:23], vcc, s[22:23]
	v_readlane_b32 s5, v6, 32
	v_cndmask_b32_e64 v10, 0, 1, s[22:23]
	s_nop 0
	v_cmp_eq_f32_e64 s[22:23], s5, v6
	v_cmp_gt_f32_e32 vcc, s5, v6
	s_and_b64 s[22:23], s[14:15], s[22:23]
	s_or_b64 s[22:23], vcc, s[22:23]
	v_readlane_b32 s5, v6, 40
	v_cndmask_b32_e64 v11, 0, 1, s[22:23]
	s_nop 0
	v_cmp_eq_f32_e64 s[22:23], s5, v6
	v_cmp_gt_f32_e32 vcc, s5, v6
	s_and_b64 s[22:23], s[16:17], s[22:23]
	s_or_b64 s[22:23], vcc, s[22:23]
	v_readlane_b32 s5, v6, 48
	v_cndmask_b32_e64 v12, 0, 1, s[22:23]
	s_nop 0
	v_cmp_eq_f32_e64 s[22:23], s5, v6
	v_cmp_gt_f32_e32 vcc, s5, v6
	s_and_b64 s[22:23], s[18:19], s[22:23]
	v_readlane_b32 s5, v6, 56
	s_or_b64 s[22:23], vcc, s[22:23]
	v_cndmask_b32_e64 v13, 0, 1, s[22:23]
	v_cmp_gt_f32_e32 vcc, s5, v6
	s_nop 1
	v_cndmask_b32_e64 v6, 0, 1, vcc
	v_add_u32_e32 v6, v8, v6
	v_add3_u32 v6, v6, v7, v9
	v_add3_u32 v6, v6, v10, v11
	v_add3_u32 v6, v6, v12, v13
	v_cmp_eq_u32_e32 vcc, 0, v6
	s_ff1_i32_b64 s98, vcc
	v_cmp_eq_u32_e32 vcc, 1, v6
	s_ff1_i32_b64 s99, vcc
	v_cmp_eq_u32_e32 vcc, 2, v6
	s_ff1_i32_b64 s100, vcc
	v_cmp_eq_u32_e32 vcc, 3, v6
	s_ff1_i32_b64 s101, vcc
	v_cmp_gt_u32_e32 vcc, 4, v6
	s_nop 1
	v_cndmask_b32_e32 v6, v245, v2, vcc
	v_mov_b32_e32 v2, 0
	v_ashrrev_i32_e32 v9, 31, v6
	v_sub_u32_e32 v8, 63, v230
	v_and_b32_e32 v9, 0x7fffffff, v9
	v_xor_b32_e32 v9, v6, v9
	s_nop 0
	v_readlane_b32 s25, v9, s98
	s_sub_i32 s24, 63, s98
	s_add_i32 s98, s98, 1
	v_readlane_b32 s23, v9, s98
	s_sub_i32 s22, 63, s98
	s_add_i32 s98, s98, 1
	v_cmp_gt_i64_e32 vcc, s[24:25], v[8:9]
	v_readlane_b32 s25, v9, s98
	s_sub_i32 s24, 63, s98
	s_add_i32 s98, s98, 1
	v_addc_co_u32_e32 v2, vcc, 0, v2, vcc
	v_cmp_gt_i64_e32 vcc, s[22:23], v[8:9]
	v_readlane_b32 s23, v9, s98
	s_sub_i32 s22, 63, s98
	s_add_i32 s98, s98, 1
	v_addc_co_u32_e32 v2, vcc, 0, v2, vcc
	v_cmp_gt_i64_e32 vcc, s[24:25], v[8:9]
	v_readlane_b32 s25, v9, s98
	s_sub_i32 s24, 63, s98
	s_add_i32 s98, s98, 1
	v_addc_co_u32_e32 v2, vcc, 0, v2, vcc
	v_cmp_gt_i64_e32 vcc, s[22:23], v[8:9]
	v_readlane_b32 s23, v9, s98
	s_sub_i32 s22, 63, s98
	s_add_i32 s98, s98, 1
	v_addc_co_u32_e32 v2, vcc, 0, v2, vcc
	v_cmp_gt_i64_e32 vcc, s[24:25], v[8:9]
	v_readlane_b32 s25, v9, s98
	s_sub_i32 s24, 63, s98
	s_add_i32 s98, s98, 1
	v_addc_co_u32_e32 v2, vcc, 0, v2, vcc
	v_cmp_gt_i64_e32 vcc, s[22:23], v[8:9]
	v_readlane_b32 s23, v9, s98
	s_sub_i32 s22, 63, s98
	s_nop 0
	v_addc_co_u32_e32 v2, vcc, 0, v2, vcc
	v_cmp_gt_i64_e32 vcc, s[24:25], v[8:9]
	v_readlane_b32 s25, v9, s99
	s_sub_i32 s24, 63, s99
	s_add_i32 s99, s99, 1
	v_addc_co_u32_e32 v2, vcc, 0, v2, vcc
	v_cmp_gt_i64_e32 vcc, s[22:23], v[8:9]
	v_readlane_b32 s23, v9, s99
	s_sub_i32 s22, 63, s99
	s_add_i32 s99, s99, 1
	v_addc_co_u32_e32 v2, vcc, 0, v2, vcc
	v_cmp_gt_i64_e32 vcc, s[24:25], v[8:9]
	v_readlane_b32 s25, v9, s99
	s_sub_i32 s24, 63, s99
	s_add_i32 s99, s99, 1
	v_addc_co_u32_e32 v2, vcc, 0, v2, vcc
	v_cmp_gt_i64_e32 vcc, s[22:23], v[8:9]
	v_readlane_b32 s23, v9, s99
	s_sub_i32 s22, 63, s99
	s_add_i32 s99, s99, 1
	v_addc_co_u32_e32 v2, vcc, 0, v2, vcc
	v_cmp_gt_i64_e32 vcc, s[24:25], v[8:9]
	v_readlane_b32 s25, v9, s99
	s_sub_i32 s24, 63, s99
	s_add_i32 s99, s99, 1
	v_addc_co_u32_e32 v2, vcc, 0, v2, vcc
	v_cmp_gt_i64_e32 vcc, s[22:23], v[8:9]
	v_readlane_b32 s23, v9, s99
	s_sub_i32 s22, 63, s99
	s_add_i32 s99, s99, 1
; __device__ __forceinline__ void phase_nrr(const Frame& F, const Args& a, int l, const bf16_t* XA, const float* g, const float* modl, unsigned char* XN8) {
;     ...
;             int rank = 0;
; #pragma unroll 8
;             for (int e2 = 0; e2 < 64; ++e2) { const float v = __int_as_float(__builtin_amdgcn_readlane(__float_as_int(val), e2)); rank += (v > val || (v == val && e2 < lane)) ? 1 : 0; }
;             const bool sel = rank < TOPK;
;             const float ssum = wave_sum(sel ? sc : 0.f);
;             if (sel) { const int p = atomicAdd((int*)(hist + lane), 1); top_e[t * TOPK + rank] = lane; gate[t * TOPK + rank] = sc / ssum * 2.5f; lpos[t * TOPK + rank] = p; }
	v_addc_co_u32_e32 v2, vcc, 0, v2, vcc
	v_cmp_gt_i64_e32 vcc, s[24:25], v[8:9]
	v_readlane_b32 s25, v9, s99
	s_sub_i32 s24, 63, s99
	s_add_i32 s99, s99, 1
	v_addc_co_u32_e32 v2, vcc, 0, v2, vcc
	v_cmp_gt_i64_e32 vcc, s[22:23], v[8:9]
	v_readlane_b32 s23, v9, s99
	s_sub_i32 s22, 63, s99
	s_nop 0
	v_addc_co_u32_e32 v2, vcc, 0, v2, vcc
	v_cmp_gt_i64_e32 vcc, s[24:25], v[8:9]
	v_readlane_b32 s25, v9, s100
	s_sub_i32 s24, 63, s100
	s_add_i32 s100, s100, 1
	v_addc_co_u32_e32 v2, vcc, 0, v2, vcc
	v_cmp_gt_i64_e32 vcc, s[22:23], v[8:9]
	v_readlane_b32 s23, v9, s100
	s_sub_i32 s22, 63, s100
	s_add_i32 s100, s100, 1
	v_addc_co_u32_e32 v2, vcc, 0, v2, vcc
	v_cmp_gt_i64_e32 vcc, s[24:25], v[8:9]
	v_readlane_b32 s25, v9, s100
	s_sub_i32 s24, 63, s100
	s_add_i32 s100, s100, 1
	v_addc_co_u32_e32 v2, vcc, 0, v2, vcc
	v_cmp_gt_i64_e32 vcc, s[22:23], v[8:9]
	v_readlane_b32 s23, v9, s100
	s_sub_i32 s22, 63, s100
	s_add_i32 s100, s100, 1
	v_addc_co_u32_e32 v2, vcc, 0, v2, vcc
	v_cmp_gt_i64_e32 vcc, s[24:25], v[8:9]
	v_readlane_b32 s25, v9, s100
	s_sub_i32 s24, 63, s100
	s_add_i32 s100, s100, 1
	v_addc_co_u32_e32 v2, vcc, 0, v2, vcc
	v_cmp_gt_i64_e32 vcc, s[22:23], v[8:9]
	v_readlane_b32 s23, v9, s100
	s_sub_i32 s22, 63, s100
	s_add_i32 s100, s100, 1
	v_addc_co_u32_e32 v2, vcc, 0, v2, vcc
	v_cmp_gt_i64_e32 vcc, s[24:25], v[8:9]
	v_readlane_b32 s25, v9, s100
	s_sub_i32 s24, 63, s100
	s_add_i32 s100, s100, 1
	v_addc_co_u32_e32 v2, vcc, 0, v2, vcc
	v_cmp_gt_i64_e32 vcc, s[22:23], v[8:9]
	v_readlane_b32 s23, v9, s100
	s_sub_i32 s22, 63, s100
	s_nop 0
	v_addc_co_u32_e32 v2, vcc, 0, v2, vcc
	v_cmp_gt_i64_e32 vcc, s[24:25], v[8:9]
	v_readlane_b32 s25, v9, s101
	s_sub_i32 s24, 63, s101
	s_add_i32 s101, s101, 1
	v_addc_co_u32_e32 v2, vcc, 0, v2, vcc
	v_cmp_gt_i64_e32 vcc, s[22:23], v[8:9]
	v_readlane_b32 s23, v9, s101
	s_sub_i32 s22, 63, s101
	s_add_i32 s101, s101, 1
	v_addc_co_u32_e32 v2, vcc, 0, v2, vcc
	v_cmp_gt_i64_e32 vcc, s[24:25], v[8:9]
	v_readlane_b32 s25, v9, s101
	s_sub_i32 s24, 63, s101
	s_add_i32 s101, s101, 1
	v_addc_co_u32_e32 v2, vcc, 0, v2, vcc
	v_cmp_gt_i64_e32 vcc, s[22:23], v[8:9]
	v_readlane_b32 s23, v9, s101
	s_sub_i32 s22, 63, s101
	s_add_i32 s101, s101, 1
	v_addc_co_u32_e32 v2, vcc, 0, v2, vcc
	v_cmp_gt_i64_e32 vcc, s[24:25], v[8:9]
	v_readlane_b32 s25, v9, s101
	s_sub_i32 s24, 63, s101
	s_add_i32 s101, s101, 1
	v_addc_co_u32_e32 v2, vcc, 0, v2, vcc
	v_cmp_gt_i64_e32 vcc, s[22:23], v[8:9]
	v_readlane_b32 s23, v9, s101
	s_sub_i32 s22, 63, s101
	s_add_i32 s101, s101, 1
	v_addc_co_u32_e32 v2, vcc, 0, v2, vcc
	v_cmp_gt_i64_e32 vcc, s[24:25], v[8:9]
	v_readlane_b32 s25, v9, s101
	s_sub_i32 s24, 63, s101
	s_add_i32 s101, s101, 1
	v_addc_co_u32_e32 v2, vcc, 0, v2, vcc
	v_cmp_gt_i64_e32 vcc, s[22:23], v[8:9]
	v_readlane_b32 s23, v9, s101
	s_sub_i32 s22, 63, s101
	s_nop 0
	v_addc_co_u32_e32 v2, vcc, 0, v2, vcc
	v_cmp_gt_i64_e32 vcc, s[24:25], v[8:9]
	s_nop 1
	v_addc_co_u32_e32 v2, vcc, 0, v2, vcc
	v_cmp_gt_i64_e32 vcc, s[22:23], v[8:9]
	s_nop 1
	v_addc_co_u32_e32 v2, vcc, 0, v2, vcc
	v_cmp_gt_u32_e32 vcc, 6, v2
	s_nop 1
	v_cndmask_b32_e32 v6, 0, v5, vcc
	s_nop 1
	v_add_f32_dpp v6, v6, v6 quad_perm:[1,0,3,2] row_mask:0xf bank_mask:0xf
	s_nop 1
	v_add_f32_dpp v6, v6, v6 quad_perm:[2,3,0,1] row_mask:0xf bank_mask:0xf
	s_nop 1
	v_add_f32_dpp v6, v6, v6 row_half_mirror row_mask:0xf bank_mask:0xf
	s_nop 1
	v_add_f32_dpp v6, v6, v6 row_mirror row_mask:0xf bank_mask:0xf
	s_nop 0
	ds_bpermute_b32 v7, v222, v6
	s_waitcnt lgkmcnt(0)
	v_add_f32_e32 v6, v6, v7
	v_mov_b32_e32 v7, v6
	s_nop 1
	v_permlane32_swap_b32_e32 v7, v6
	s_and_saveexec_b64 s[22:23], vcc
	s_cbranch_execz .LBB0_543
	s_waitcnt lgkmcnt(0)
	v_add_f32_e32 v10, v6, v7
	v_mad_u64_u32 v[6:7], s[24:25], s42, 6, v[2:3]
	v_div_scale_f32 v2, s[24:25], v10, v10, v5
	v_rcp_f32_e32 v12, v2
	v_ashrrev_i32_e32 v7, 31, v6
	v_lshlrev_b64 v[6:7], 2, v[6:7]
	v_lshl_add_u64 v[8:9], s[26:27], 0, v[6:7]
	ds_add_rtn_u32 v11, v227, v243
	global_store_dword v[8:9], v230, off
	v_fma_f32 v8, -v2, v12, 1.0
	v_fmac_f32_e32 v12, v8, v12
	v_div_scale_f32 v8, vcc, v5, v10, v5
	v_mul_f32_e32 v9, v8, v12
	v_fma_f32 v13, -v2, v9, v8
	v_fmac_f32_e32 v9, v13, v12
	v_fma_f32 v2, -v2, v9, v8
	v_div_fmas_f32 v2, v2, v12, v9
	v_div_fixup_f32 v2, v2, v10, v5
	v_mul_f32_e32 v2, 0x40200000, v2
	v_lshl_add_u64 v[8:9], s[28:29], 0, v[6:7]
	v_lshl_add_u64 v[6:7], s[30:31], 0, v[6:7]
	global_store_dword v[8:9], v2, off
	s_waitcnt lgkmcnt(0)
	global_store_dword v[6:7], v11, off
; __device__ __forceinline__ void phase_nrr(const Frame& F, const Args& a, int l, const bf16_t* XA, const float* g, const float* modl, unsigned char* XN8) {
;     ...
;         for (int i = 0; i < 8; ++i) { const int t = tb + i;
;             const float lg = Pl[(w * 8 + i) * NE + lane] + Pl[(64 + w * 8 + i) * NE + lane]; const float sc = 1.f / (1.f + __expf(-lg)); const float bb = sc + bias;
;             float m1 = bb; m1 = fmaxf(m1, __shfl_xor(m1, 1)); m1 = fmaxf(m1, __shfl_xor(m1, 2)); m1 = fmaxf(m1, __shfl_xor(m1, 4));
;             const unsigned long long eq = __ballot(bb == m1); const int gbase = lane & ~7; const unsigned grpmask = (unsigned)((eq >> gbase) & 0xffull);
;             const int first = gbase + __builtin_ctz(grpmask);
;             float m2 = (lane == first) ? -INFINITY : bb; m2 = fmaxf(m2, __shfl_xor(m2, 1)); m2 = fmaxf(m2, __shfl_xor(m2, 2)); m2 = fmaxf(m2, __shfl_xor(m2, 4));
;             const float gsum = m1 + m2; const int gq = lane >> 3;
;             int grank = 0;
; #pragma unroll
;             for (int g2 = 0; g2 < 8; ++g2) { const float v = __int_as_float(__builtin_amdgcn_readlane(__float_as_int(gsum), g2 * 8)); grank += (v > gsum || (v == gsum && g2 < gq)) ? 1 : 0; }
;             const bool keep = grank < 4; const float val = keep ? bb : -INFINITY;
;             int rank = 0;
; #pragma unroll 8
;             for (int e2 = 0; e2 < 64; ++e2) { const float v = __int_as_float(__builtin_amdgcn_readlane(__float_as_int(val), e2)); rank += (v > val || (v == val && e2 < lane)) ? 1 : 0; }
.LBB0_543:
	s_or_b64 exec, exec, s[22:23]
	v_add_u32_e32 v2, s78, v226
	ds_read_b32 v2, v2
	ds_read_b32 v5, v4 offset:16896
	s_mov_b32 s3, 0
	s_waitcnt lgkmcnt(0)
	v_add_f32_e32 v2, v2, v5
	v_mul_f32_e32 v2, 0xbfb8aa3b, v2
	v_exp_f32_e32 v2, v2
	s_nop 0
	v_add_f32_e32 v2, 1.0, v2
	v_div_scale_f32 v5, s[22:23], v2, v2, 1.0
	v_rcp_f32_e32 v6, v5
	s_nop 0
	v_fma_f32 v7, -v5, v6, 1.0
	v_fmac_f32_e32 v6, v7, v6
	v_div_scale_f32 v7, vcc, 1.0, v2, 1.0
	v_mul_f32_e32 v8, v7, v6
	v_fma_f32 v9, -v5, v8, v7
	v_fmac_f32_e32 v8, v9, v6
	v_fma_f32 v5, -v5, v8, v7
	v_div_fmas_f32 v5, v5, v6, v8
	v_div_fixup_f32 v5, v5, v2, 1.0
	v_add_f32_e32 v2, v3, v5
	s_nop 1
	s_waitcnt lgkmcnt(0)
	v_max_f32_dpp v6, v2, v2 quad_perm:[1,0,3,2] row_mask:0xf bank_mask:0xf
	s_nop 1
	s_waitcnt lgkmcnt(0)
	v_max_f32_dpp v6, v6, v6 quad_perm:[2,3,0,1] row_mask:0xf bank_mask:0xf
	s_nop 1
	s_waitcnt lgkmcnt(0)
	v_max_f32_dpp v8, v6, v6 row_half_mirror row_mask:0xf bank_mask:0xf
	v_cmp_eq_f32_e32 vcc, v2, v8
	s_nop 1
	v_lshrrev_b64 v[6:7], v200, vcc
	v_ffbl_b32_sdwa v6, v6 dst_sel:DWORD dst_unused:UNUSED_PAD src0_sel:BYTE_0
	v_add_u32_e32 v6, v6, v200
	v_cmp_ne_u32_e32 vcc, v230, v6
	s_nop 1
	v_cndmask_b32_e32 v6, v245, v2, vcc
	s_nop 1
	s_waitcnt lgkmcnt(0)
	v_max_f32_dpp v6, v6, v6 quad_perm:[1,0,3,2] row_mask:0xf bank_mask:0xf
	s_nop 1
	s_waitcnt lgkmcnt(0)
	v_max_f32_dpp v6, v6, v6 quad_perm:[2,3,0,1] row_mask:0xf bank_mask:0xf
	s_nop 1
	s_waitcnt lgkmcnt(0)
	v_max_f32_dpp v6, v6, v6 row_half_mirror row_mask:0xf bank_mask:0xf
	v_add_f32_e32 v6, v8, v6
	s_nop 0
	v_readlane_b32 s5, v6, 0
	s_nop 1
	v_cmp_eq_f32_e64 s[22:23], s5, v6
	v_cmp_gt_f32_e32 vcc, s5, v6
	s_and_b64 s[22:23], s[6:7], s[22:23]
	s_or_b64 s[22:23], vcc, s[22:23]
	v_readlane_b32 s5, v6, 8
	v_cndmask_b32_e64 v7, 0, 1, s[22:23]
	s_nop 0
	v_cmp_eq_f32_e64 s[22:23], s5, v6
	v_cmp_gt_f32_e32 vcc, s5, v6
	s_and_b64 s[22:23], s[8:9], s[22:23]
	s_or_b64 s[22:23], vcc, s[22:23]
	v_readlane_b32 s5, v6, 16
	v_cndmask_b32_e64 v8, 0, 1, s[22:23]
	s_nop 0
	v_cmp_eq_f32_e64 s[22:23], s5, v6
	v_cmp_gt_f32_e32 vcc, s5, v6
	s_and_b64 s[22:23], s[10:11], s[22:23]
	s_or_b64 s[22:23], vcc, s[22:23]
	v_readlane_b32 s5, v6, 24
	v_cndmask_b32_e64 v9, 0, 1, s[22:23]
	s_nop 0
	v_cmp_eq_f32_e64 s[22:23], s5, v6
	v_cmp_gt_f32_e32 vcc, s5, v6
	s_and_b64 s[22:23], s[12:13], s[22:23]
	s_or_b64 s[22:23], vcc, s[22:23]
	v_readlane_b32 s5, v6, 32
	v_cndmask_b32_e64 v10, 0, 1, s[22:23]
	s_nop 0
	v_cmp_eq_f32_e64 s[22:23], s5, v6
	v_cmp_gt_f32_e32 vcc, s5, v6
	s_and_b64 s[22:23], s[14:15], s[22:23]
	s_or_b64 s[22:23], vcc, s[22:23]
	v_readlane_b32 s5, v6, 40
	v_cndmask_b32_e64 v11, 0, 1, s[22:23]
	s_nop 0
	v_cmp_eq_f32_e64 s[22:23], s5, v6
	v_cmp_gt_f32_e32 vcc, s5, v6
	s_and_b64 s[22:23], s[16:17], s[22:23]
	s_or_b64 s[22:23], vcc, s[22:23]
	v_readlane_b32 s5, v6, 48
	v_cndmask_b32_e64 v12, 0, 1, s[22:23]
	s_nop 0
	v_cmp_eq_f32_e64 s[22:23], s5, v6
	v_cmp_gt_f32_e32 vcc, s5, v6
	s_and_b64 s[22:23], s[18:19], s[22:23]
	v_readlane_b32 s5, v6, 56
	s_or_b64 s[22:23], vcc, s[22:23]
	v_cndmask_b32_e64 v13, 0, 1, s[22:23]
	v_cmp_gt_f32_e32 vcc, s5, v6
	s_nop 1
	v_cndmask_b32_e64 v6, 0, 1, vcc
	v_add_u32_e32 v6, v8, v6
	v_add3_u32 v6, v6, v7, v9
	v_add3_u32 v6, v6, v10, v11
	v_add3_u32 v6, v6, v12, v13
	v_cmp_eq_u32_e32 vcc, 0, v6
	s_ff1_i32_b64 s98, vcc
	v_cmp_eq_u32_e32 vcc, 1, v6
	s_ff1_i32_b64 s99, vcc
	v_cmp_eq_u32_e32 vcc, 2, v6
	s_ff1_i32_b64 s100, vcc
	v_cmp_eq_u32_e32 vcc, 3, v6
	s_ff1_i32_b64 s101, vcc
	v_cmp_gt_u32_e32 vcc, 4, v6
	s_nop 1
	v_cndmask_b32_e32 v6, v245, v2, vcc
	v_mov_b32_e32 v2, 0
	v_ashrrev_i32_e32 v9, 31, v6
	v_sub_u32_e32 v8, 63, v230
	v_and_b32_e32 v9, 0x7fffffff, v9
	v_xor_b32_e32 v9, v6, v9
	s_nop 0
	v_readlane_b32 s25, v9, s98
	s_sub_i32 s24, 63, s98
	s_add_i32 s98, s98, 1
	v_readlane_b32 s23, v9, s98
	s_sub_i32 s22, 63, s98
	s_add_i32 s98, s98, 1
	v_cmp_gt_i64_e32 vcc, s[24:25], v[8:9]
	v_readlane_b32 s25, v9, s98
	s_sub_i32 s24, 63, s98
	s_add_i32 s98, s98, 1
	v_addc_co_u32_e32 v2, vcc, 0, v2, vcc
	v_cmp_gt_i64_e32 vcc, s[22:23], v[8:9]
	v_readlane_b32 s23, v9, s98
	s_sub_i32 s22, 63, s98
	s_add_i32 s98, s98, 1
	v_addc_co_u32_e32 v2, vcc, 0, v2, vcc
	v_cmp_gt_i64_e32 vcc, s[24:25], v[8:9]
	v_readlane_b32 s25, v9, s98
	s_sub_i32 s24, 63, s98
	s_add_i32 s98, s98, 1
	v_addc_co_u32_e32 v2, vcc, 0, v2, vcc
	v_cmp_gt_i64_e32 vcc, s[22:23], v[8:9]
	v_readlane_b32 s23, v9, s98
	s_sub_i32 s22, 63, s98
	s_add_i32 s98, s98, 1
	v_addc_co_u32_e32 v2, vcc, 0, v2, vcc
	v_cmp_gt_i64_e32 vcc, s[24:25], v[8:9]
	v_readlane_b32 s25, v9, s98
	s_sub_i32 s24, 63, s98
	s_add_i32 s98, s98, 1
	v_addc_co_u32_e32 v2, vcc, 0, v2, vcc
	v_cmp_gt_i64_e32 vcc, s[22:23], v[8:9]
	v_readlane_b32 s23, v9, s98
	s_sub_i32 s22, 63, s98
	s_nop 0
	v_addc_co_u32_e32 v2, vcc, 0, v2, vcc
	v_cmp_gt_i64_e32 vcc, s[24:25], v[8:9]
	v_readlane_b32 s25, v9, s99
	s_sub_i32 s24, 63, s99
	s_add_i32 s99, s99, 1
	v_addc_co_u32_e32 v2, vcc, 0, v2, vcc
	v_cmp_gt_i64_e32 vcc, s[22:23], v[8:9]
	v_readlane_b32 s23, v9, s99
	s_sub_i32 s22, 63, s99
	s_add_i32 s99, s99, 1
	v_addc_co_u32_e32 v2, vcc, 0, v2, vcc
	v_cmp_gt_i64_e32 vcc, s[24:25], v[8:9]
	v_readlane_b32 s25, v9, s99
	s_sub_i32 s24, 63, s99
	s_add_i32 s99, s99, 1
	v_addc_co_u32_e32 v2, vcc, 0, v2, vcc
	v_cmp_gt_i64_e32 vcc, s[22:23], v[8:9]
	v_readlane_b32 s23, v9, s99
	s_sub_i32 s22, 63, s99
	s_add_i32 s99, s99, 1
	v_addc_co_u32_e32 v2, vcc, 0, v2, vcc
	v_cmp_gt_i64_e32 vcc, s[24:25], v[8:9]
	v_readlane_b32 s25, v9, s99
	s_sub_i32 s24, 63, s99
	s_add_i32 s99, s99, 1
	v_addc_co_u32_e32 v2, vcc, 0, v2, vcc
	v_cmp_gt_i64_e32 vcc, s[22:23], v[8:9]
	v_readlane_b32 s23, v9, s99
	s_sub_i32 s22, 63, s99
	s_add_i32 s99, s99, 1
; __device__ __forceinline__ void phase_nrr(const Frame& F, const Args& a, int l, const bf16_t* XA, const float* g, const float* modl, unsigned char* XN8) {
;     ...
;             int rank = 0;
; #pragma unroll 8
;             for (int e2 = 0; e2 < 64; ++e2) { const float v = __int_as_float(__builtin_amdgcn_readlane(__float_as_int(val), e2)); rank += (v > val || (v == val && e2 < lane)) ? 1 : 0; }
;             const bool sel = rank < TOPK;
;             const float ssum = wave_sum(sel ? sc : 0.f);
;             if (sel) { const int p = atomicAdd((int*)(hist + lane), 1); top_e[t * TOPK + rank] = lane; gate[t * TOPK + rank] = sc / ssum * 2.5f; lpos[t * TOPK + rank] = p; }
	v_addc_co_u32_e32 v2, vcc, 0, v2, vcc
	v_cmp_gt_i64_e32 vcc, s[24:25], v[8:9]
	v_readlane_b32 s25, v9, s99
	s_sub_i32 s24, 63, s99
	s_add_i32 s99, s99, 1
	v_addc_co_u32_e32 v2, vcc, 0, v2, vcc
	v_cmp_gt_i64_e32 vcc, s[22:23], v[8:9]
	v_readlane_b32 s23, v9, s99
	s_sub_i32 s22, 63, s99
	s_nop 0
	v_addc_co_u32_e32 v2, vcc, 0, v2, vcc
	v_cmp_gt_i64_e32 vcc, s[24:25], v[8:9]
	v_readlane_b32 s25, v9, s100
	s_sub_i32 s24, 63, s100
	s_add_i32 s100, s100, 1
	v_addc_co_u32_e32 v2, vcc, 0, v2, vcc
	v_cmp_gt_i64_e32 vcc, s[22:23], v[8:9]
	v_readlane_b32 s23, v9, s100
	s_sub_i32 s22, 63, s100
	s_add_i32 s100, s100, 1
	v_addc_co_u32_e32 v2, vcc, 0, v2, vcc
	v_cmp_gt_i64_e32 vcc, s[24:25], v[8:9]
	v_readlane_b32 s25, v9, s100
	s_sub_i32 s24, 63, s100
	s_add_i32 s100, s100, 1
	v_addc_co_u32_e32 v2, vcc, 0, v2, vcc
	v_cmp_gt_i64_e32 vcc, s[22:23], v[8:9]
	v_readlane_b32 s23, v9, s100
	s_sub_i32 s22, 63, s100
	s_add_i32 s100, s100, 1
	v_addc_co_u32_e32 v2, vcc, 0, v2, vcc
	v_cmp_gt_i64_e32 vcc, s[24:25], v[8:9]
	v_readlane_b32 s25, v9, s100
	s_sub_i32 s24, 63, s100
	s_add_i32 s100, s100, 1
	v_addc_co_u32_e32 v2, vcc, 0, v2, vcc
	v_cmp_gt_i64_e32 vcc, s[22:23], v[8:9]
	v_readlane_b32 s23, v9, s100
	s_sub_i32 s22, 63, s100
	s_add_i32 s100, s100, 1
	v_addc_co_u32_e32 v2, vcc, 0, v2, vcc
	v_cmp_gt_i64_e32 vcc, s[24:25], v[8:9]
	v_readlane_b32 s25, v9, s100
	s_sub_i32 s24, 63, s100
	s_add_i32 s100, s100, 1
	v_addc_co_u32_e32 v2, vcc, 0, v2, vcc
	v_cmp_gt_i64_e32 vcc, s[22:23], v[8:9]
	v_readlane_b32 s23, v9, s100
	s_sub_i32 s22, 63, s100
	s_nop 0
	v_addc_co_u32_e32 v2, vcc, 0, v2, vcc
	v_cmp_gt_i64_e32 vcc, s[24:25], v[8:9]
	v_readlane_b32 s25, v9, s101
	s_sub_i32 s24, 63, s101
	s_add_i32 s101, s101, 1
	v_addc_co_u32_e32 v2, vcc, 0, v2, vcc
	v_cmp_gt_i64_e32 vcc, s[22:23], v[8:9]
	v_readlane_b32 s23, v9, s101
	s_sub_i32 s22, 63, s101
	s_add_i32 s101, s101, 1
	v_addc_co_u32_e32 v2, vcc, 0, v2, vcc
	v_cmp_gt_i64_e32 vcc, s[24:25], v[8:9]
	v_readlane_b32 s25, v9, s101
	s_sub_i32 s24, 63, s101
	s_add_i32 s101, s101, 1
	v_addc_co_u32_e32 v2, vcc, 0, v2, vcc
	v_cmp_gt_i64_e32 vcc, s[22:23], v[8:9]
	v_readlane_b32 s23, v9, s101
	s_sub_i32 s22, 63, s101
	s_add_i32 s101, s101, 1
	v_addc_co_u32_e32 v2, vcc, 0, v2, vcc
	v_cmp_gt_i64_e32 vcc, s[24:25], v[8:9]
	v_readlane_b32 s25, v9, s101
	s_sub_i32 s24, 63, s101
	s_add_i32 s101, s101, 1
	v_addc_co_u32_e32 v2, vcc, 0, v2, vcc
	v_cmp_gt_i64_e32 vcc, s[22:23], v[8:9]
	v_readlane_b32 s23, v9, s101
	s_sub_i32 s22, 63, s101
	s_add_i32 s101, s101, 1
	v_addc_co_u32_e32 v2, vcc, 0, v2, vcc
	v_cmp_gt_i64_e32 vcc, s[24:25], v[8:9]
	v_readlane_b32 s25, v9, s101
	s_sub_i32 s24, 63, s101
	s_add_i32 s101, s101, 1
	v_addc_co_u32_e32 v2, vcc, 0, v2, vcc
	v_cmp_gt_i64_e32 vcc, s[22:23], v[8:9]
	v_readlane_b32 s23, v9, s101
	s_sub_i32 s22, 63, s101
	s_nop 0
	v_addc_co_u32_e32 v2, vcc, 0, v2, vcc
	v_cmp_gt_i64_e32 vcc, s[24:25], v[8:9]
	s_nop 1
	v_addc_co_u32_e32 v2, vcc, 0, v2, vcc
	v_cmp_gt_i64_e32 vcc, s[22:23], v[8:9]
	s_nop 1
	v_addc_co_u32_e32 v2, vcc, 0, v2, vcc
	v_cmp_gt_u32_e32 vcc, 6, v2
	s_nop 1
	v_cndmask_b32_e32 v6, 0, v5, vcc
	s_nop 1
	v_add_f32_dpp v6, v6, v6 quad_perm:[1,0,3,2] row_mask:0xf bank_mask:0xf
	s_nop 1
	v_add_f32_dpp v6, v6, v6 quad_perm:[2,3,0,1] row_mask:0xf bank_mask:0xf
	s_nop 1
	v_add_f32_dpp v6, v6, v6 row_half_mirror row_mask:0xf bank_mask:0xf
	s_nop 1
	v_add_f32_dpp v6, v6, v6 row_mirror row_mask:0xf bank_mask:0xf
	s_nop 0
	ds_bpermute_b32 v7, v222, v6
	s_waitcnt lgkmcnt(0)
	v_add_f32_e32 v6, v6, v7
	v_mov_b32_e32 v7, v6
	s_nop 1
	v_permlane32_swap_b32_e32 v7, v6
	s_and_saveexec_b64 s[22:23], vcc
	s_cbranch_execz .LBB0_547
	s_waitcnt lgkmcnt(0)
	v_add_f32_e32 v10, v6, v7
	v_mad_u64_u32 v[6:7], s[24:25], s40, 6, v[2:3]
	v_div_scale_f32 v2, s[24:25], v10, v10, v5
	v_rcp_f32_e32 v12, v2
	v_ashrrev_i32_e32 v7, 31, v6
	v_lshlrev_b64 v[6:7], 2, v[6:7]
	v_lshl_add_u64 v[8:9], s[26:27], 0, v[6:7]
	ds_add_rtn_u32 v11, v227, v243
	global_store_dword v[8:9], v230, off
	v_fma_f32 v8, -v2, v12, 1.0
	v_fmac_f32_e32 v12, v8, v12
	v_div_scale_f32 v8, vcc, v5, v10, v5
	v_mul_f32_e32 v9, v8, v12
	v_fma_f32 v13, -v2, v9, v8
	v_fmac_f32_e32 v9, v13, v12
	v_fma_f32 v2, -v2, v9, v8
	v_div_fmas_f32 v2, v2, v12, v9
	v_div_fixup_f32 v2, v2, v10, v5
	v_mul_f32_e32 v2, 0x40200000, v2
	v_lshl_add_u64 v[8:9], s[28:29], 0, v[6:7]
	v_lshl_add_u64 v[6:7], s[30:31], 0, v[6:7]
	global_store_dword v[8:9], v2, off
	s_waitcnt lgkmcnt(0)
	global_store_dword v[6:7], v11, off
; __device__ __forceinline__ void phase_nrr(const Frame& F, const Args& a, int l, const bf16_t* XA, const float* g, const float* modl, unsigned char* XN8) {
;     ...
;         for (int i = 0; i < 8; ++i) { const int t = tb + i;
;             const float lg = Pl[(w * 8 + i) * NE + lane] + Pl[(64 + w * 8 + i) * NE + lane]; const float sc = 1.f / (1.f + __expf(-lg)); const float bb = sc + bias;
;             float m1 = bb; m1 = fmaxf(m1, __shfl_xor(m1, 1)); m1 = fmaxf(m1, __shfl_xor(m1, 2)); m1 = fmaxf(m1, __shfl_xor(m1, 4));
;             const unsigned long long eq = __ballot(bb == m1); const int gbase = lane & ~7; const unsigned grpmask = (unsigned)((eq >> gbase) & 0xffull);
;             const int first = gbase + __builtin_ctz(grpmask);
;             float m2 = (lane == first) ? -INFINITY : bb; m2 = fmaxf(m2, __shfl_xor(m2, 1)); m2 = fmaxf(m2, __shfl_xor(m2, 2)); m2 = fmaxf(m2, __shfl_xor(m2, 4));
;             const float gsum = m1 + m2; const int gq = lane >> 3;
;             int grank = 0;
; #pragma unroll
;             for (int g2 = 0; g2 < 8; ++g2) { const float v = __int_as_float(__builtin_amdgcn_readlane(__float_as_int(gsum), g2 * 8)); grank += (v > gsum || (v == gsum && g2 < gq)) ? 1 : 0; }
;             const bool keep = grank < 4; const float val = keep ? bb : -INFINITY;
;             int rank = 0;
; #pragma unroll 8
;             for (int e2 = 0; e2 < 64; ++e2) { const float v = __int_as_float(__builtin_amdgcn_readlane(__float_as_int(val), e2)); rank += (v > val || (v == val && e2 < lane)) ? 1 : 0; }
.LBB0_547:
	s_or_b64 exec, exec, s[22:23]
	v_add_u32_e32 v2, s79, v226
	ds_read_b32 v2, v2
	ds_read_b32 v5, v4 offset:17152
	s_mov_b32 s3, 0
	s_waitcnt lgkmcnt(0)
	v_add_f32_e32 v2, v2, v5
	v_mul_f32_e32 v2, 0xbfb8aa3b, v2
	v_exp_f32_e32 v2, v2
	s_nop 0
	v_add_f32_e32 v2, 1.0, v2
	v_div_scale_f32 v5, s[22:23], v2, v2, 1.0
	v_rcp_f32_e32 v6, v5
	s_nop 0
	v_fma_f32 v7, -v5, v6, 1.0
	v_fmac_f32_e32 v6, v7, v6
	v_div_scale_f32 v7, vcc, 1.0, v2, 1.0
	v_mul_f32_e32 v8, v7, v6
	v_fma_f32 v9, -v5, v8, v7
	v_fmac_f32_e32 v8, v9, v6
	v_fma_f32 v5, -v5, v8, v7
	v_div_fmas_f32 v5, v5, v6, v8
	v_div_fixup_f32 v5, v5, v2, 1.0
	v_add_f32_e32 v2, v3, v5
	s_nop 1
	s_waitcnt lgkmcnt(0)
	v_max_f32_dpp v6, v2, v2 quad_perm:[1,0,3,2] row_mask:0xf bank_mask:0xf
	s_nop 1
	s_waitcnt lgkmcnt(0)
	v_max_f32_dpp v6, v6, v6 quad_perm:[2,3,0,1] row_mask:0xf bank_mask:0xf
	s_nop 1
	s_waitcnt lgkmcnt(0)
	v_max_f32_dpp v8, v6, v6 row_half_mirror row_mask:0xf bank_mask:0xf
	v_cmp_eq_f32_e32 vcc, v2, v8
	s_nop 1
	v_lshrrev_b64 v[6:7], v200, vcc
	v_ffbl_b32_sdwa v6, v6 dst_sel:DWORD dst_unused:UNUSED_PAD src0_sel:BYTE_0
	v_add_u32_e32 v6, v6, v200
	v_cmp_ne_u32_e32 vcc, v230, v6
	s_nop 1
	v_cndmask_b32_e32 v6, v245, v2, vcc
	s_nop 1
	s_waitcnt lgkmcnt(0)
	v_max_f32_dpp v6, v6, v6 quad_perm:[1,0,3,2] row_mask:0xf bank_mask:0xf
	s_nop 1
	s_waitcnt lgkmcnt(0)
	v_max_f32_dpp v6, v6, v6 quad_perm:[2,3,0,1] row_mask:0xf bank_mask:0xf
	s_nop 1
	s_waitcnt lgkmcnt(0)
	v_max_f32_dpp v6, v6, v6 row_half_mirror row_mask:0xf bank_mask:0xf
	v_add_f32_e32 v6, v8, v6
	s_nop 0
	v_readlane_b32 s5, v6, 0
	s_nop 1
	v_cmp_eq_f32_e64 s[22:23], s5, v6
	v_cmp_gt_f32_e32 vcc, s5, v6
	s_and_b64 s[22:23], s[6:7], s[22:23]
	s_or_b64 s[22:23], vcc, s[22:23]
	v_readlane_b32 s5, v6, 8
	v_cndmask_b32_e64 v7, 0, 1, s[22:23]
	s_nop 0
	v_cmp_eq_f32_e64 s[22:23], s5, v6
	v_cmp_gt_f32_e32 vcc, s5, v6
	s_and_b64 s[22:23], s[8:9], s[22:23]
	s_or_b64 s[22:23], vcc, s[22:23]
	v_readlane_b32 s5, v6, 16
	v_cndmask_b32_e64 v8, 0, 1, s[22:23]
	s_nop 0
	v_cmp_eq_f32_e64 s[22:23], s5, v6
	v_cmp_gt_f32_e32 vcc, s5, v6
	s_and_b64 s[22:23], s[10:11], s[22:23]
	s_or_b64 s[22:23], vcc, s[22:23]
	v_readlane_b32 s5, v6, 24
	v_cndmask_b32_e64 v9, 0, 1, s[22:23]
	s_nop 0
	v_cmp_eq_f32_e64 s[22:23], s5, v6
	v_cmp_gt_f32_e32 vcc, s5, v6
	s_and_b64 s[22:23], s[12:13], s[22:23]
	s_or_b64 s[22:23], vcc, s[22:23]
	v_readlane_b32 s5, v6, 32
	v_cndmask_b32_e64 v10, 0, 1, s[22:23]
	s_nop 0
	v_cmp_eq_f32_e64 s[22:23], s5, v6
	v_cmp_gt_f32_e32 vcc, s5, v6
	s_and_b64 s[22:23], s[14:15], s[22:23]
	s_or_b64 s[22:23], vcc, s[22:23]
	v_readlane_b32 s5, v6, 40
	v_cndmask_b32_e64 v11, 0, 1, s[22:23]
	s_nop 0
	v_cmp_eq_f32_e64 s[22:23], s5, v6
	v_cmp_gt_f32_e32 vcc, s5, v6
	s_and_b64 s[22:23], s[16:17], s[22:23]
	s_or_b64 s[22:23], vcc, s[22:23]
	v_readlane_b32 s5, v6, 48
	v_cndmask_b32_e64 v12, 0, 1, s[22:23]
	s_nop 0
	v_cmp_eq_f32_e64 s[22:23], s5, v6
	v_cmp_gt_f32_e32 vcc, s5, v6
	s_and_b64 s[22:23], s[18:19], s[22:23]
	v_readlane_b32 s5, v6, 56
	s_or_b64 s[22:23], vcc, s[22:23]
	v_cndmask_b32_e64 v13, 0, 1, s[22:23]
	v_cmp_gt_f32_e32 vcc, s5, v6
	s_nop 1
	v_cndmask_b32_e64 v6, 0, 1, vcc
	v_add_u32_e32 v6, v8, v6
	v_add3_u32 v6, v6, v7, v9
	v_add3_u32 v6, v6, v10, v11
	v_add3_u32 v6, v6, v12, v13
	v_cmp_eq_u32_e32 vcc, 0, v6
	s_ff1_i32_b64 s98, vcc
	v_cmp_eq_u32_e32 vcc, 1, v6
	s_ff1_i32_b64 s99, vcc
	v_cmp_eq_u32_e32 vcc, 2, v6
	s_ff1_i32_b64 s100, vcc
	v_cmp_eq_u32_e32 vcc, 3, v6
	s_ff1_i32_b64 s101, vcc
	v_cmp_gt_u32_e32 vcc, 4, v6
	s_nop 1
	v_cndmask_b32_e32 v6, v245, v2, vcc
	v_mov_b32_e32 v2, 0
	v_ashrrev_i32_e32 v9, 31, v6
	v_sub_u32_e32 v8, 63, v230
	v_and_b32_e32 v9, 0x7fffffff, v9
	v_xor_b32_e32 v9, v6, v9
	s_nop 0
	v_readlane_b32 s25, v9, s98
	s_sub_i32 s24, 63, s98
	s_add_i32 s98, s98, 1
	v_readlane_b32 s23, v9, s98
	s_sub_i32 s22, 63, s98
	s_add_i32 s98, s98, 1
	v_cmp_gt_i64_e32 vcc, s[24:25], v[8:9]
	v_readlane_b32 s25, v9, s98
	s_sub_i32 s24, 63, s98
	s_add_i32 s98, s98, 1
	v_addc_co_u32_e32 v2, vcc, 0, v2, vcc
	v_cmp_gt_i64_e32 vcc, s[22:23], v[8:9]
	v_readlane_b32 s23, v9, s98
	s_sub_i32 s22, 63, s98
	s_add_i32 s98, s98, 1
	v_addc_co_u32_e32 v2, vcc, 0, v2, vcc
	v_cmp_gt_i64_e32 vcc, s[24:25], v[8:9]
	v_readlane_b32 s25, v9, s98
	s_sub_i32 s24, 63, s98
	s_add_i32 s98, s98, 1
	v_addc_co_u32_e32 v2, vcc, 0, v2, vcc
	v_cmp_gt_i64_e32 vcc, s[22:23], v[8:9]
	v_readlane_b32 s23, v9, s98
	s_sub_i32 s22, 63, s98
	s_add_i32 s98, s98, 1
	v_addc_co_u32_e32 v2, vcc, 0, v2, vcc
	v_cmp_gt_i64_e32 vcc, s[24:25], v[8:9]
	v_readlane_b32 s25, v9, s98
	s_sub_i32 s24, 63, s98
	s_add_i32 s98, s98, 1
	v_addc_co_u32_e32 v2, vcc, 0, v2, vcc
	v_cmp_gt_i64_e32 vcc, s[22:23], v[8:9]
	v_readlane_b32 s23, v9, s98
	s_sub_i32 s22, 63, s98
	s_nop 0
	v_addc_co_u32_e32 v2, vcc, 0, v2, vcc
	v_cmp_gt_i64_e32 vcc, s[24:25], v[8:9]
	v_readlane_b32 s25, v9, s99
	s_sub_i32 s24, 63, s99
	s_add_i32 s99, s99, 1
	v_addc_co_u32_e32 v2, vcc, 0, v2, vcc
	v_cmp_gt_i64_e32 vcc, s[22:23], v[8:9]
	v_readlane_b32 s23, v9, s99
	s_sub_i32 s22, 63, s99
	s_add_i32 s99, s99, 1
	v_addc_co_u32_e32 v2, vcc, 0, v2, vcc
	v_cmp_gt_i64_e32 vcc, s[24:25], v[8:9]
	v_readlane_b32 s25, v9, s99
	s_sub_i32 s24, 63, s99
	s_add_i32 s99, s99, 1
	v_addc_co_u32_e32 v2, vcc, 0, v2, vcc
	v_cmp_gt_i64_e32 vcc, s[22:23], v[8:9]
	v_readlane_b32 s23, v9, s99
	s_sub_i32 s22, 63, s99
	s_add_i32 s99, s99, 1
	v_addc_co_u32_e32 v2, vcc, 0, v2, vcc
	v_cmp_gt_i64_e32 vcc, s[24:25], v[8:9]
	v_readlane_b32 s25, v9, s99
	s_sub_i32 s24, 63, s99
	s_add_i32 s99, s99, 1
	v_addc_co_u32_e32 v2, vcc, 0, v2, vcc
	v_cmp_gt_i64_e32 vcc, s[22:23], v[8:9]
	v_readlane_b32 s23, v9, s99
	s_sub_i32 s22, 63, s99
	s_add_i32 s99, s99, 1
; __device__ __forceinline__ void phase_nrr(const Frame& F, const Args& a, int l, const bf16_t* XA, const float* g, const float* modl, unsigned char* XN8) {
;     ...
;             int rank = 0;
; #pragma unroll 8
;             for (int e2 = 0; e2 < 64; ++e2) { const float v = __int_as_float(__builtin_amdgcn_readlane(__float_as_int(val), e2)); rank += (v > val || (v == val && e2 < lane)) ? 1 : 0; }
;             const bool sel = rank < TOPK;
;             const float ssum = wave_sum(sel ? sc : 0.f);
;             if (sel) { const int p = atomicAdd((int*)(hist + lane), 1); top_e[t * TOPK + rank] = lane; gate[t * TOPK + rank] = sc / ssum * 2.5f; lpos[t * TOPK + rank] = p; }
	v_addc_co_u32_e32 v2, vcc, 0, v2, vcc
	v_cmp_gt_i64_e32 vcc, s[24:25], v[8:9]
	v_readlane_b32 s25, v9, s99
	s_sub_i32 s24, 63, s99
	s_add_i32 s99, s99, 1
	v_addc_co_u32_e32 v2, vcc, 0, v2, vcc
	v_cmp_gt_i64_e32 vcc, s[22:23], v[8:9]
	v_readlane_b32 s23, v9, s99
	s_sub_i32 s22, 63, s99
	s_nop 0
	v_addc_co_u32_e32 v2, vcc, 0, v2, vcc
	v_cmp_gt_i64_e32 vcc, s[24:25], v[8:9]
	v_readlane_b32 s25, v9, s100
	s_sub_i32 s24, 63, s100
	s_add_i32 s100, s100, 1
	v_addc_co_u32_e32 v2, vcc, 0, v2, vcc
	v_cmp_gt_i64_e32 vcc, s[22:23], v[8:9]
	v_readlane_b32 s23, v9, s100
	s_sub_i32 s22, 63, s100
	s_add_i32 s100, s100, 1
	v_addc_co_u32_e32 v2, vcc, 0, v2, vcc
	v_cmp_gt_i64_e32 vcc, s[24:25], v[8:9]
	v_readlane_b32 s25, v9, s100
	s_sub_i32 s24, 63, s100
	s_add_i32 s100, s100, 1
	v_addc_co_u32_e32 v2, vcc, 0, v2, vcc
	v_cmp_gt_i64_e32 vcc, s[22:23], v[8:9]
	v_readlane_b32 s23, v9, s100
	s_sub_i32 s22, 63, s100
	s_add_i32 s100, s100, 1
	v_addc_co_u32_e32 v2, vcc, 0, v2, vcc
	v_cmp_gt_i64_e32 vcc, s[24:25], v[8:9]
	v_readlane_b32 s25, v9, s100
	s_sub_i32 s24, 63, s100
	s_add_i32 s100, s100, 1
	v_addc_co_u32_e32 v2, vcc, 0, v2, vcc
	v_cmp_gt_i64_e32 vcc, s[22:23], v[8:9]
	v_readlane_b32 s23, v9, s100
	s_sub_i32 s22, 63, s100
	s_add_i32 s100, s100, 1
	v_addc_co_u32_e32 v2, vcc, 0, v2, vcc
	v_cmp_gt_i64_e32 vcc, s[24:25], v[8:9]
	v_readlane_b32 s25, v9, s100
	s_sub_i32 s24, 63, s100
	s_add_i32 s100, s100, 1
	v_addc_co_u32_e32 v2, vcc, 0, v2, vcc
	v_cmp_gt_i64_e32 vcc, s[22:23], v[8:9]
	v_readlane_b32 s23, v9, s100
	s_sub_i32 s22, 63, s100
	s_nop 0
	v_addc_co_u32_e32 v2, vcc, 0, v2, vcc
	v_cmp_gt_i64_e32 vcc, s[24:25], v[8:9]
	v_readlane_b32 s25, v9, s101
	s_sub_i32 s24, 63, s101
	s_add_i32 s101, s101, 1
	v_addc_co_u32_e32 v2, vcc, 0, v2, vcc
	v_cmp_gt_i64_e32 vcc, s[22:23], v[8:9]
	v_readlane_b32 s23, v9, s101
	s_sub_i32 s22, 63, s101
	s_add_i32 s101, s101, 1
	v_addc_co_u32_e32 v2, vcc, 0, v2, vcc
	v_cmp_gt_i64_e32 vcc, s[24:25], v[8:9]
	v_readlane_b32 s25, v9, s101
	s_sub_i32 s24, 63, s101
	s_add_i32 s101, s101, 1
	v_addc_co_u32_e32 v2, vcc, 0, v2, vcc
	v_cmp_gt_i64_e32 vcc, s[22:23], v[8:9]
	v_readlane_b32 s23, v9, s101
	s_sub_i32 s22, 63, s101
	s_add_i32 s101, s101, 1
	v_addc_co_u32_e32 v2, vcc, 0, v2, vcc
	v_cmp_gt_i64_e32 vcc, s[24:25], v[8:9]
	v_readlane_b32 s25, v9, s101
	s_sub_i32 s24, 63, s101
	s_add_i32 s101, s101, 1
	v_addc_co_u32_e32 v2, vcc, 0, v2, vcc
	v_cmp_gt_i64_e32 vcc, s[22:23], v[8:9]
	v_readlane_b32 s23, v9, s101
	s_sub_i32 s22, 63, s101
	s_add_i32 s101, s101, 1
	v_addc_co_u32_e32 v2, vcc, 0, v2, vcc
	v_cmp_gt_i64_e32 vcc, s[24:25], v[8:9]
	v_readlane_b32 s25, v9, s101
	s_sub_i32 s24, 63, s101
	s_add_i32 s101, s101, 1
	v_addc_co_u32_e32 v2, vcc, 0, v2, vcc
	v_cmp_gt_i64_e32 vcc, s[22:23], v[8:9]
	v_readlane_b32 s23, v9, s101
	s_sub_i32 s22, 63, s101
	s_nop 0
	v_addc_co_u32_e32 v2, vcc, 0, v2, vcc
	v_cmp_gt_i64_e32 vcc, s[24:25], v[8:9]
	s_nop 1
	v_addc_co_u32_e32 v2, vcc, 0, v2, vcc
	v_cmp_gt_i64_e32 vcc, s[22:23], v[8:9]
	s_nop 1
	v_addc_co_u32_e32 v2, vcc, 0, v2, vcc
	v_cmp_gt_u32_e32 vcc, 6, v2
	s_nop 1
	v_cndmask_b32_e32 v6, 0, v5, vcc
	s_nop 1
	v_add_f32_dpp v6, v6, v6 quad_perm:[1,0,3,2] row_mask:0xf bank_mask:0xf
	s_nop 1
	v_add_f32_dpp v6, v6, v6 quad_perm:[2,3,0,1] row_mask:0xf bank_mask:0xf
	s_nop 1
	v_add_f32_dpp v6, v6, v6 row_half_mirror row_mask:0xf bank_mask:0xf
	s_nop 1
	v_add_f32_dpp v6, v6, v6 row_mirror row_mask:0xf bank_mask:0xf
	s_nop 0
	ds_bpermute_b32 v7, v222, v6
	s_waitcnt lgkmcnt(0)
	v_add_f32_e32 v6, v6, v7
	v_mov_b32_e32 v7, v6
	s_nop 1
	v_permlane32_swap_b32_e32 v7, v6
	s_and_saveexec_b64 s[22:23], vcc
	s_cbranch_execz .LBB0_551
	s_waitcnt lgkmcnt(0)
	v_add_f32_e32 v10, v6, v7
	v_mad_u64_u32 v[6:7], s[4:5], s4, 6, v[2:3]
	v_div_scale_f32 v2, s[4:5], v10, v10, v5
	v_rcp_f32_e32 v12, v2
	v_ashrrev_i32_e32 v7, 31, v6
	v_lshlrev_b64 v[6:7], 2, v[6:7]
	v_lshl_add_u64 v[8:9], s[26:27], 0, v[6:7]
	ds_add_rtn_u32 v11, v227, v243
	global_store_dword v[8:9], v230, off
	v_fma_f32 v8, -v2, v12, 1.0
	v_fmac_f32_e32 v12, v8, v12
	v_div_scale_f32 v8, vcc, v5, v10, v5
	v_mul_f32_e32 v9, v8, v12
	v_fma_f32 v13, -v2, v9, v8
	v_fmac_f32_e32 v9, v13, v12
	v_fma_f32 v2, -v2, v9, v8
	v_div_fmas_f32 v2, v2, v12, v9
	v_div_fixup_f32 v2, v2, v10, v5
	v_mul_f32_e32 v2, 0x40200000, v2
	v_lshl_add_u64 v[8:9], s[28:29], 0, v[6:7]
	v_lshl_add_u64 v[6:7], s[30:31], 0, v[6:7]
	global_store_dword v[8:9], v2, off
	s_waitcnt lgkmcnt(0)
	global_store_dword v[6:7], v11, off
; __device__ __forceinline__ void phase_nrr(const Frame& F, const Args& a, int l, const bf16_t* XA, const float* g, const float* modl, unsigned char* XN8) {
;     ...
;         for (int i = 0; i < 8; ++i) { const int t = tb + i;
;             const float lg = Pl[(w * 8 + i) * NE + lane] + Pl[(64 + w * 8 + i) * NE + lane]; const float sc = 1.f / (1.f + __expf(-lg)); const float bb = sc + bias;
;             float m1 = bb; m1 = fmaxf(m1, __shfl_xor(m1, 1)); m1 = fmaxf(m1, __shfl_xor(m1, 2)); m1 = fmaxf(m1, __shfl_xor(m1, 4));
;             const unsigned long long eq = __ballot(bb == m1); const int gbase = lane & ~7; const unsigned grpmask = (unsigned)((eq >> gbase) & 0xffull);
;             const int first = gbase + __builtin_ctz(grpmask);
;             float m2 = (lane == first) ? -INFINITY : bb; m2 = fmaxf(m2, __shfl_xor(m2, 1)); m2 = fmaxf(m2, __shfl_xor(m2, 2)); m2 = fmaxf(m2, __shfl_xor(m2, 4));
;             const float gsum = m1 + m2; const int gq = lane >> 3;
;             int grank = 0;
; #pragma unroll
;             for (int g2 = 0; g2 < 8; ++g2) { const float v = __int_as_float(__builtin_amdgcn_readlane(__float_as_int(gsum), g2 * 8)); grank += (v > gsum || (v == gsum && g2 < gq)) ? 1 : 0; }
;             const bool keep = grank < 4; const float val = keep ? bb : -INFINITY;
;             int rank = 0;
; #pragma unroll 8
;             for (int e2 = 0; e2 < 64; ++e2) { const float v = __int_as_float(__builtin_amdgcn_readlane(__float_as_int(val), e2)); rank += (v > val || (v == val && e2 < lane)) ? 1 : 0; }
.LBB0_551:
	s_or_b64 exec, exec, s[22:23]
	v_add_u32_e32 v2, s84, v226
	ds_read_b32 v2, v2
	ds_read_b32 v5, v4 offset:17408
	s_mov_b32 s3, 0
	s_waitcnt lgkmcnt(0)
	v_add_f32_e32 v2, v2, v5
	v_mul_f32_e32 v2, 0xbfb8aa3b, v2
	v_exp_f32_e32 v2, v2
	s_nop 0
	v_add_f32_e32 v2, 1.0, v2
	v_div_scale_f32 v5, s[4:5], v2, v2, 1.0
	v_rcp_f32_e32 v6, v5
	s_nop 0
	v_fma_f32 v7, -v5, v6, 1.0
	v_fmac_f32_e32 v6, v7, v6
	v_div_scale_f32 v7, vcc, 1.0, v2, 1.0
	v_mul_f32_e32 v8, v7, v6
	v_fma_f32 v9, -v5, v8, v7
	v_fmac_f32_e32 v8, v9, v6
	v_fma_f32 v5, -v5, v8, v7
	v_div_fmas_f32 v5, v5, v6, v8
	v_div_fixup_f32 v2, v5, v2, 1.0
	v_add_f32_e32 v5, v3, v2
	s_nop 1
	s_waitcnt lgkmcnt(0)
	v_max_f32_dpp v6, v5, v5 quad_perm:[1,0,3,2] row_mask:0xf bank_mask:0xf
	s_nop 1
	s_waitcnt lgkmcnt(0)
	v_max_f32_dpp v6, v6, v6 quad_perm:[2,3,0,1] row_mask:0xf bank_mask:0xf
	s_nop 1
	s_waitcnt lgkmcnt(0)
	v_max_f32_dpp v8, v6, v6 row_half_mirror row_mask:0xf bank_mask:0xf
	v_cmp_eq_f32_e32 vcc, v5, v8
	s_nop 1
	v_lshrrev_b64 v[6:7], v200, vcc
	v_ffbl_b32_sdwa v6, v6 dst_sel:DWORD dst_unused:UNUSED_PAD src0_sel:BYTE_0
	v_add_u32_e32 v6, v6, v200
	v_cmp_ne_u32_e32 vcc, v230, v6
	s_nop 1
	v_cndmask_b32_e32 v6, v245, v5, vcc
	s_nop 1
	s_waitcnt lgkmcnt(0)
	v_max_f32_dpp v6, v6, v6 quad_perm:[1,0,3,2] row_mask:0xf bank_mask:0xf
	s_nop 1
	s_waitcnt lgkmcnt(0)
	v_max_f32_dpp v6, v6, v6 quad_perm:[2,3,0,1] row_mask:0xf bank_mask:0xf
	s_nop 1
	s_waitcnt lgkmcnt(0)
	v_max_f32_dpp v6, v6, v6 row_half_mirror row_mask:0xf bank_mask:0xf
	v_add_f32_e32 v6, v8, v6
	s_nop 0
	v_readlane_b32 s4, v6, 0
	s_nop 1
	v_cmp_eq_f32_e64 s[22:23], s4, v6
	v_cmp_gt_f32_e32 vcc, s4, v6
	s_and_b64 s[4:5], s[6:7], s[22:23]
	s_or_b64 s[4:5], vcc, s[4:5]
	v_cndmask_b32_e64 v7, 0, 1, s[4:5]
	v_readlane_b32 s4, v6, 8
	s_nop 1
	v_cmp_eq_f32_e64 s[22:23], s4, v6
	v_cmp_gt_f32_e32 vcc, s4, v6
	s_and_b64 s[4:5], s[8:9], s[22:23]
	s_or_b64 s[4:5], vcc, s[4:5]
	v_cndmask_b32_e64 v8, 0, 1, s[4:5]
	v_readlane_b32 s4, v6, 16
	s_nop 1
	v_cmp_eq_f32_e64 s[22:23], s4, v6
	v_cmp_gt_f32_e32 vcc, s4, v6
	s_and_b64 s[4:5], s[10:11], s[22:23]
	s_or_b64 s[4:5], vcc, s[4:5]
	v_cndmask_b32_e64 v9, 0, 1, s[4:5]
	v_readlane_b32 s4, v6, 24
	s_nop 1
	v_cmp_eq_f32_e64 s[22:23], s4, v6
	v_cmp_gt_f32_e32 vcc, s4, v6
	s_and_b64 s[4:5], s[12:13], s[22:23]
	s_or_b64 s[4:5], vcc, s[4:5]
	v_cndmask_b32_e64 v10, 0, 1, s[4:5]
	v_readlane_b32 s4, v6, 32
	s_nop 1
	v_cmp_eq_f32_e64 s[22:23], s4, v6
	v_cmp_gt_f32_e32 vcc, s4, v6
	s_and_b64 s[4:5], s[14:15], s[22:23]
	s_or_b64 s[4:5], vcc, s[4:5]
	v_cndmask_b32_e64 v11, 0, 1, s[4:5]
	v_readlane_b32 s4, v6, 40
	s_nop 1
	v_cmp_eq_f32_e64 s[22:23], s4, v6
	v_cmp_gt_f32_e32 vcc, s4, v6
	s_and_b64 s[4:5], s[16:17], s[22:23]
	s_or_b64 s[4:5], vcc, s[4:5]
	v_cndmask_b32_e64 v12, 0, 1, s[4:5]
	v_readlane_b32 s4, v6, 48
	s_nop 1
	v_cmp_eq_f32_e64 s[22:23], s4, v6
	v_cmp_gt_f32_e32 vcc, s4, v6
	s_and_b64 s[4:5], s[18:19], s[22:23]
	s_or_b64 s[4:5], vcc, s[4:5]
	v_cndmask_b32_e64 v13, 0, 1, s[4:5]
	v_readlane_b32 s4, v6, 56
	s_nop 1
	v_cmp_gt_f32_e32 vcc, s4, v6
	s_nop 1
	v_cndmask_b32_e64 v6, 0, 1, vcc
	v_add_u32_e32 v6, v8, v6
	v_add3_u32 v6, v6, v7, v9
	v_add3_u32 v6, v6, v10, v11
	v_add3_u32 v6, v6, v12, v13
	v_cmp_eq_u32_e32 vcc, 0, v6
	s_ff1_i32_b64 s98, vcc
	v_cmp_eq_u32_e32 vcc, 1, v6
	s_ff1_i32_b64 s99, vcc
	v_cmp_eq_u32_e32 vcc, 2, v6
	s_ff1_i32_b64 s100, vcc
	v_cmp_eq_u32_e32 vcc, 3, v6
	s_ff1_i32_b64 s101, vcc
	v_cmp_gt_u32_e32 vcc, 4, v6
	v_mov_b32_e32 v6, 0
	s_nop 0
	v_cndmask_b32_e32 v5, v245, v5, vcc
	v_ashrrev_i32_e32 v9, 31, v5
	v_sub_u32_e32 v8, 63, v230
	v_and_b32_e32 v9, 0x7fffffff, v9
	v_xor_b32_e32 v9, v5, v9
	s_nop 0
	v_readlane_b32 s25, v9, s98
	s_sub_i32 s24, 63, s98
	s_add_i32 s98, s98, 1
	v_readlane_b32 s23, v9, s98
	s_sub_i32 s22, 63, s98
	s_add_i32 s98, s98, 1
	v_cmp_gt_i64_e32 vcc, s[24:25], v[8:9]
	v_readlane_b32 s25, v9, s98
	s_sub_i32 s24, 63, s98
	s_add_i32 s98, s98, 1
	v_addc_co_u32_e32 v6, vcc, 0, v6, vcc
	v_cmp_gt_i64_e32 vcc, s[22:23], v[8:9]
	v_readlane_b32 s23, v9, s98
	s_sub_i32 s22, 63, s98
	s_add_i32 s98, s98, 1
	v_addc_co_u32_e32 v6, vcc, 0, v6, vcc
	v_cmp_gt_i64_e32 vcc, s[24:25], v[8:9]
	v_readlane_b32 s25, v9, s98
	s_sub_i32 s24, 63, s98
	s_add_i32 s98, s98, 1
	v_addc_co_u32_e32 v6, vcc, 0, v6, vcc
	v_cmp_gt_i64_e32 vcc, s[22:23], v[8:9]
	v_readlane_b32 s23, v9, s98
	s_sub_i32 s22, 63, s98
	s_add_i32 s98, s98, 1
	v_addc_co_u32_e32 v6, vcc, 0, v6, vcc
	v_cmp_gt_i64_e32 vcc, s[24:25], v[8:9]
	v_readlane_b32 s25, v9, s98
	s_sub_i32 s24, 63, s98
	s_add_i32 s98, s98, 1
	v_addc_co_u32_e32 v6, vcc, 0, v6, vcc
	v_cmp_gt_i64_e32 vcc, s[22:23], v[8:9]
	v_readlane_b32 s23, v9, s98
	s_sub_i32 s22, 63, s98
	s_nop 0
	v_addc_co_u32_e32 v6, vcc, 0, v6, vcc
	v_cmp_gt_i64_e32 vcc, s[24:25], v[8:9]
	v_readlane_b32 s25, v9, s99
	s_sub_i32 s24, 63, s99
	s_add_i32 s99, s99, 1
	v_addc_co_u32_e32 v6, vcc, 0, v6, vcc
	v_cmp_gt_i64_e32 vcc, s[22:23], v[8:9]
	v_readlane_b32 s23, v9, s99
	s_sub_i32 s22, 63, s99
	s_add_i32 s99, s99, 1
	v_addc_co_u32_e32 v6, vcc, 0, v6, vcc
	v_cmp_gt_i64_e32 vcc, s[24:25], v[8:9]
	v_readlane_b32 s25, v9, s99
	s_sub_i32 s24, 63, s99
	s_add_i32 s99, s99, 1
	v_addc_co_u32_e32 v6, vcc, 0, v6, vcc
	v_cmp_gt_i64_e32 vcc, s[22:23], v[8:9]
	v_readlane_b32 s23, v9, s99
	s_sub_i32 s22, 63, s99
	s_add_i32 s99, s99, 1
	v_addc_co_u32_e32 v6, vcc, 0, v6, vcc
	v_cmp_gt_i64_e32 vcc, s[24:25], v[8:9]
	v_readlane_b32 s25, v9, s99
	s_sub_i32 s24, 63, s99
	s_add_i32 s99, s99, 1
	v_addc_co_u32_e32 v6, vcc, 0, v6, vcc
	v_cmp_gt_i64_e32 vcc, s[22:23], v[8:9]
	v_readlane_b32 s23, v9, s99
	s_sub_i32 s22, 63, s99
	s_add_i32 s99, s99, 1
	v_addc_co_u32_e32 v6, vcc, 0, v6, vcc
; __device__ __forceinline__ void phase_nrr(const Frame& F, const Args& a, int l, const bf16_t* XA, const float* g, const float* modl, unsigned char* XN8) {
;     ...
;             int rank = 0;
; #pragma unroll 8
;             for (int e2 = 0; e2 < 64; ++e2) { const float v = __int_as_float(__builtin_amdgcn_readlane(__float_as_int(val), e2)); rank += (v > val || (v == val && e2 < lane)) ? 1 : 0; }
;             const bool sel = rank < TOPK;
;             const float ssum = wave_sum(sel ? sc : 0.f);
;             if (sel) { const int p = atomicAdd((int*)(hist + lane), 1); top_e[t * TOPK + rank] = lane; gate[t * TOPK + rank] = sc / ssum * 2.5f; lpos[t * TOPK + rank] = p; }
	v_cmp_gt_i64_e32 vcc, s[24:25], v[8:9]
	v_readlane_b32 s25, v9, s99
	s_sub_i32 s24, 63, s99
	s_add_i32 s99, s99, 1
	v_addc_co_u32_e32 v6, vcc, 0, v6, vcc
	v_cmp_gt_i64_e32 vcc, s[22:23], v[8:9]
	v_readlane_b32 s23, v9, s99
	s_sub_i32 s22, 63, s99
	s_nop 0
	v_addc_co_u32_e32 v6, vcc, 0, v6, vcc
	v_cmp_gt_i64_e32 vcc, s[24:25], v[8:9]
	v_readlane_b32 s25, v9, s100
	s_sub_i32 s24, 63, s100
	s_add_i32 s100, s100, 1
	v_addc_co_u32_e32 v6, vcc, 0, v6, vcc
	v_cmp_gt_i64_e32 vcc, s[22:23], v[8:9]
	v_readlane_b32 s23, v9, s100
	s_sub_i32 s22, 63, s100
	s_add_i32 s100, s100, 1
	v_addc_co_u32_e32 v6, vcc, 0, v6, vcc
	v_cmp_gt_i64_e32 vcc, s[24:25], v[8:9]
	v_readlane_b32 s25, v9, s100
	s_sub_i32 s24, 63, s100
	s_add_i32 s100, s100, 1
	v_addc_co_u32_e32 v6, vcc, 0, v6, vcc
	v_cmp_gt_i64_e32 vcc, s[22:23], v[8:9]
	v_readlane_b32 s23, v9, s100
	s_sub_i32 s22, 63, s100
	s_add_i32 s100, s100, 1
	v_addc_co_u32_e32 v6, vcc, 0, v6, vcc
	v_cmp_gt_i64_e32 vcc, s[24:25], v[8:9]
	v_readlane_b32 s25, v9, s100
	s_sub_i32 s24, 63, s100
	s_add_i32 s100, s100, 1
	v_addc_co_u32_e32 v6, vcc, 0, v6, vcc
	v_cmp_gt_i64_e32 vcc, s[22:23], v[8:9]
	v_readlane_b32 s23, v9, s100
	s_sub_i32 s22, 63, s100
	s_add_i32 s100, s100, 1
	v_addc_co_u32_e32 v6, vcc, 0, v6, vcc
	v_cmp_gt_i64_e32 vcc, s[24:25], v[8:9]
	v_readlane_b32 s25, v9, s100
	s_sub_i32 s24, 63, s100
	s_add_i32 s100, s100, 1
	v_addc_co_u32_e32 v6, vcc, 0, v6, vcc
	v_cmp_gt_i64_e32 vcc, s[22:23], v[8:9]
	v_readlane_b32 s23, v9, s100
	s_sub_i32 s22, 63, s100
	s_nop 0
	v_addc_co_u32_e32 v6, vcc, 0, v6, vcc
	v_cmp_gt_i64_e32 vcc, s[24:25], v[8:9]
	v_readlane_b32 s25, v9, s101
	s_sub_i32 s24, 63, s101
	s_add_i32 s101, s101, 1
	v_addc_co_u32_e32 v6, vcc, 0, v6, vcc
	v_cmp_gt_i64_e32 vcc, s[22:23], v[8:9]
	v_readlane_b32 s23, v9, s101
	s_sub_i32 s22, 63, s101
	s_add_i32 s101, s101, 1
	v_addc_co_u32_e32 v6, vcc, 0, v6, vcc
	v_cmp_gt_i64_e32 vcc, s[24:25], v[8:9]
	v_readlane_b32 s25, v9, s101
	s_sub_i32 s24, 63, s101
	s_add_i32 s101, s101, 1
	v_addc_co_u32_e32 v6, vcc, 0, v6, vcc
	v_cmp_gt_i64_e32 vcc, s[22:23], v[8:9]
	v_readlane_b32 s23, v9, s101
	s_sub_i32 s22, 63, s101
	s_add_i32 s101, s101, 1
	v_addc_co_u32_e32 v6, vcc, 0, v6, vcc
	v_cmp_gt_i64_e32 vcc, s[24:25], v[8:9]
	v_readlane_b32 s25, v9, s101
	s_sub_i32 s24, 63, s101
	s_add_i32 s101, s101, 1
	v_addc_co_u32_e32 v6, vcc, 0, v6, vcc
	v_cmp_gt_i64_e32 vcc, s[22:23], v[8:9]
	v_readlane_b32 s23, v9, s101
	s_sub_i32 s22, 63, s101
	s_add_i32 s101, s101, 1
	v_addc_co_u32_e32 v6, vcc, 0, v6, vcc
	v_cmp_gt_i64_e32 vcc, s[24:25], v[8:9]
	v_readlane_b32 s25, v9, s101
	s_sub_i32 s24, 63, s101
	s_add_i32 s101, s101, 1
	v_addc_co_u32_e32 v6, vcc, 0, v6, vcc
	v_cmp_gt_i64_e32 vcc, s[22:23], v[8:9]
	v_readlane_b32 s23, v9, s101
	s_sub_i32 s22, 63, s101
	s_nop 0
	v_addc_co_u32_e32 v6, vcc, 0, v6, vcc
	v_cmp_gt_i64_e32 vcc, s[24:25], v[8:9]
	s_nop 1
	v_addc_co_u32_e32 v6, vcc, 0, v6, vcc
	v_cmp_gt_i64_e32 vcc, s[22:23], v[8:9]
	s_nop 1
	v_addc_co_u32_e32 v6, vcc, 0, v6, vcc
	v_cmp_gt_u32_e32 vcc, 6, v6
	s_nop 1
	v_cndmask_b32_e32 v5, 0, v2, vcc
	s_nop 1
	v_add_f32_dpp v5, v5, v5 quad_perm:[1,0,3,2] row_mask:0xf bank_mask:0xf
	s_nop 1
	v_add_f32_dpp v5, v5, v5 quad_perm:[2,3,0,1] row_mask:0xf bank_mask:0xf
	s_nop 1
	v_add_f32_dpp v5, v5, v5 row_half_mirror row_mask:0xf bank_mask:0xf
	s_nop 1
	v_add_f32_dpp v5, v5, v5 row_mirror row_mask:0xf bank_mask:0xf
	s_nop 0
	ds_bpermute_b32 v7, v222, v5
	s_waitcnt lgkmcnt(0)
	v_add_f32_e32 v5, v5, v7
	v_mov_b32_e32 v7, v5
	s_nop 1
	v_permlane32_swap_b32_e32 v7, v5
	s_and_saveexec_b64 s[4:5], vcc
	s_cbranch_execz .LBB0_555
	s_waitcnt lgkmcnt(0)
	v_add_f32_e32 v5, v5, v7
	s_mul_i32 s2, s2, 6
	v_or_b32_e32 v6, s2, v6
	v_div_scale_f32 v11, s[2:3], v5, v5, v2
	v_rcp_f32_e32 v12, v11
	v_ashrrev_i32_e32 v7, 31, v6
	v_lshlrev_b64 v[6:7], 2, v[6:7]
	v_lshl_add_u64 v[8:9], s[26:27], 0, v[6:7]
	ds_add_rtn_u32 v10, v227, v243
	global_store_dword v[8:9], v230, off
	v_fma_f32 v8, -v11, v12, 1.0
	v_fmac_f32_e32 v12, v8, v12
	v_div_scale_f32 v8, vcc, v2, v5, v2
	v_mul_f32_e32 v9, v8, v12
	v_fma_f32 v13, -v11, v9, v8
	v_fmac_f32_e32 v9, v13, v12
	v_fma_f32 v8, -v11, v9, v8
	v_div_fmas_f32 v8, v8, v12, v9
	v_div_fixup_f32 v2, v8, v5, v2
	v_mul_f32_e32 v2, 0x40200000, v2
	v_lshl_add_u64 v[8:9], s[28:29], 0, v[6:7]
	v_lshl_add_u64 v[6:7], s[30:31], 0, v[6:7]
	global_store_dword v[8:9], v2, off
	s_waitcnt lgkmcnt(0)
	global_store_dword v[6:7], v10, off
; __device__ __forceinline__ void phase_nrr(const Frame& F, const Args& a, int l, const bf16_t* XA, const float* g, const float* modl, unsigned char* XN8) {
;     ...
;         for (int i = 0; i < 8; ++i) { const int t = tb + i;
;             const float lg = Pl[(w * 8 + i) * NE + lane] + Pl[(64 + w * 8 + i) * NE + lane]; const float sc = 1.f / (1.f + __expf(-lg)); const float bb = sc + bias;
;             float m1 = bb; m1 = fmaxf(m1, __shfl_xor(m1, 1)); m1 = fmaxf(m1, __shfl_xor(m1, 2)); m1 = fmaxf(m1, __shfl_xor(m1, 4));
;             const unsigned long long eq = __ballot(bb == m1); const int gbase = lane & ~7; const unsigned grpmask = (unsigned)((eq >> gbase) & 0xffull);
;             const int first = gbase + __builtin_ctz(grpmask);
;             float m2 = (lane == first) ? -INFINITY : bb; m2 = fmaxf(m2, __shfl_xor(m2, 1)); m2 = fmaxf(m2, __shfl_xor(m2, 2)); m2 = fmaxf(m2, __shfl_xor(m2, 4));
;             const float gsum = m1 + m2; const int gq = lane >> 3;
;             int grank = 0;
; #pragma unroll
;             for (int g2 = 0; g2 < 8; ++g2) { const float v = __int_as_float(__builtin_amdgcn_readlane(__float_as_int(gsum), g2 * 8)); grank += (v > gsum || (v == gsum && g2 < gq)) ? 1 : 0; }
;             const bool keep = grank < 4; const float val = keep ? bb : -INFINITY;
;             int rank = 0;
; #pragma unroll 8
;             for (int e2 = 0; e2 < 64; ++e2) { const float v = __int_as_float(__builtin_amdgcn_readlane(__float_as_int(val), e2)); rank += (v > val || (v == val && e2 < lane)) ? 1 : 0; }
.LBB0_555:
	s_or_b64 exec, exec, s[4:5]
	v_add_u32_e32 v2, s85, v226
	ds_read_b32 v2, v2
	ds_read_b32 v5, v4 offset:17664
	s_waitcnt lgkmcnt(0)
	v_add_f32_e32 v2, v2, v5
	v_mul_f32_e32 v2, 0xbfb8aa3b, v2
	v_exp_f32_e32 v2, v2
	s_nop 0
	v_add_f32_e32 v2, 1.0, v2
	v_div_scale_f32 v5, s[2:3], v2, v2, 1.0
	v_rcp_f32_e32 v6, v5
	s_mov_b32 s2, 0
	v_fma_f32 v7, -v5, v6, 1.0
	v_fmac_f32_e32 v6, v7, v6
	v_div_scale_f32 v7, vcc, 1.0, v2, 1.0
	v_mul_f32_e32 v8, v7, v6
	v_fma_f32 v9, -v5, v8, v7
	v_fmac_f32_e32 v8, v9, v6
	v_fma_f32 v5, -v5, v8, v7
	v_div_fmas_f32 v5, v5, v6, v8
	v_div_fixup_f32 v2, v5, v2, 1.0
	v_add_f32_e32 v5, v3, v2
	s_nop 1
	s_waitcnt lgkmcnt(0)
	v_max_f32_dpp v6, v5, v5 quad_perm:[1,0,3,2] row_mask:0xf bank_mask:0xf
	s_nop 1
	s_waitcnt lgkmcnt(0)
	v_max_f32_dpp v6, v6, v6 quad_perm:[2,3,0,1] row_mask:0xf bank_mask:0xf
	s_nop 1
	s_waitcnt lgkmcnt(0)
	v_max_f32_dpp v8, v6, v6 row_half_mirror row_mask:0xf bank_mask:0xf
	v_cmp_eq_f32_e32 vcc, v5, v8
	s_nop 1
	v_lshrrev_b64 v[6:7], v200, vcc
	v_ffbl_b32_sdwa v6, v6 dst_sel:DWORD dst_unused:UNUSED_PAD src0_sel:BYTE_0
	v_add_u32_e32 v6, v6, v200
	v_cmp_ne_u32_e32 vcc, v230, v6
	s_nop 1
	v_cndmask_b32_e32 v6, v245, v5, vcc
	s_nop 1
	s_waitcnt lgkmcnt(0)
	v_max_f32_dpp v6, v6, v6 quad_perm:[1,0,3,2] row_mask:0xf bank_mask:0xf
	s_nop 1
	s_waitcnt lgkmcnt(0)
	v_max_f32_dpp v6, v6, v6 quad_perm:[2,3,0,1] row_mask:0xf bank_mask:0xf
	s_nop 1
	s_waitcnt lgkmcnt(0)
	v_max_f32_dpp v6, v6, v6 row_half_mirror row_mask:0xf bank_mask:0xf
	v_add_f32_e32 v6, v8, v6
	s_nop 0
	v_readlane_b32 s3, v6, 0
	s_nop 1
	v_cmp_eq_f32_e64 s[22:23], s3, v6
	v_cmp_gt_f32_e32 vcc, s3, v6
	s_and_b64 s[4:5], s[6:7], s[22:23]
	v_readlane_b32 s3, v6, 8
	s_or_b64 s[4:5], vcc, s[4:5]
	v_cndmask_b32_e64 v7, 0, 1, s[4:5]
	v_cmp_eq_f32_e64 s[22:23], s3, v6
	v_cmp_gt_f32_e32 vcc, s3, v6
	s_and_b64 s[4:5], s[8:9], s[22:23]
	v_readlane_b32 s3, v6, 16
	s_or_b64 s[4:5], vcc, s[4:5]
	v_cndmask_b32_e64 v8, 0, 1, s[4:5]
	v_cmp_eq_f32_e64 s[22:23], s3, v6
	v_cmp_gt_f32_e32 vcc, s3, v6
	s_and_b64 s[4:5], s[10:11], s[22:23]
	v_readlane_b32 s3, v6, 24
	s_or_b64 s[4:5], vcc, s[4:5]
	v_cndmask_b32_e64 v9, 0, 1, s[4:5]
	v_cmp_eq_f32_e64 s[22:23], s3, v6
	v_cmp_gt_f32_e32 vcc, s3, v6
	s_and_b64 s[4:5], s[12:13], s[22:23]
	v_readlane_b32 s3, v6, 32
	s_or_b64 s[4:5], vcc, s[4:5]
	v_cndmask_b32_e64 v10, 0, 1, s[4:5]
	v_cmp_eq_f32_e64 s[22:23], s3, v6
	v_cmp_gt_f32_e32 vcc, s3, v6
	s_and_b64 s[4:5], s[14:15], s[22:23]
	v_readlane_b32 s3, v6, 40
	s_or_b64 s[4:5], vcc, s[4:5]
	v_cndmask_b32_e64 v11, 0, 1, s[4:5]
	v_cmp_eq_f32_e64 s[22:23], s3, v6
	v_cmp_gt_f32_e32 vcc, s3, v6
	s_and_b64 s[4:5], s[16:17], s[22:23]
	v_readlane_b32 s3, v6, 48
	s_or_b64 s[4:5], vcc, s[4:5]
	v_cndmask_b32_e64 v12, 0, 1, s[4:5]
	v_cmp_eq_f32_e64 s[22:23], s3, v6
	v_cmp_gt_f32_e32 vcc, s3, v6
	s_and_b64 s[4:5], s[18:19], s[22:23]
	v_readlane_b32 s3, v6, 56
	s_or_b64 s[4:5], vcc, s[4:5]
	v_cndmask_b32_e64 v13, 0, 1, s[4:5]
	v_cmp_gt_f32_e32 vcc, s3, v6
	s_nop 1
	v_cndmask_b32_e64 v6, 0, 1, vcc
	v_add_u32_e32 v6, v8, v6
	v_add3_u32 v6, v6, v7, v9
	v_add3_u32 v6, v6, v10, v11
	v_add3_u32 v6, v6, v12, v13
	v_cmp_eq_u32_e32 vcc, 0, v6
	s_ff1_i32_b64 s98, vcc
	v_cmp_eq_u32_e32 vcc, 1, v6
	s_ff1_i32_b64 s99, vcc
	v_cmp_eq_u32_e32 vcc, 2, v6
	s_ff1_i32_b64 s100, vcc
	v_cmp_eq_u32_e32 vcc, 3, v6
	s_ff1_i32_b64 s101, vcc
	v_cmp_gt_u32_e32 vcc, 4, v6
	v_mov_b32_e32 v6, 0
	s_nop 0
	v_cndmask_b32_e32 v5, v245, v5, vcc
	v_ashrrev_i32_e32 v9, 31, v5
	v_sub_u32_e32 v8, 63, v230
	v_and_b32_e32 v9, 0x7fffffff, v9
	v_xor_b32_e32 v9, v5, v9
	s_nop 0
	v_readlane_b32 s25, v9, s98
	s_sub_i32 s24, 63, s98
	s_add_i32 s98, s98, 1
	v_readlane_b32 s23, v9, s98
	s_sub_i32 s22, 63, s98
	s_add_i32 s98, s98, 1
	v_cmp_gt_i64_e32 vcc, s[24:25], v[8:9]
	v_readlane_b32 s25, v9, s98
	s_sub_i32 s24, 63, s98
	s_add_i32 s98, s98, 1
	v_addc_co_u32_e32 v6, vcc, 0, v6, vcc
	v_cmp_gt_i64_e32 vcc, s[22:23], v[8:9]
	v_readlane_b32 s23, v9, s98
	s_sub_i32 s22, 63, s98
	s_add_i32 s98, s98, 1
	v_addc_co_u32_e32 v6, vcc, 0, v6, vcc
	v_cmp_gt_i64_e32 vcc, s[24:25], v[8:9]
	v_readlane_b32 s25, v9, s98
	s_sub_i32 s24, 63, s98
	s_add_i32 s98, s98, 1
	v_addc_co_u32_e32 v6, vcc, 0, v6, vcc
	v_cmp_gt_i64_e32 vcc, s[22:23], v[8:9]
	v_readlane_b32 s23, v9, s98
	s_sub_i32 s22, 63, s98
	s_add_i32 s98, s98, 1
	v_addc_co_u32_e32 v6, vcc, 0, v6, vcc
	v_cmp_gt_i64_e32 vcc, s[24:25], v[8:9]
	v_readlane_b32 s25, v9, s98
	s_sub_i32 s24, 63, s98
	s_add_i32 s98, s98, 1
	v_addc_co_u32_e32 v6, vcc, 0, v6, vcc
	v_cmp_gt_i64_e32 vcc, s[22:23], v[8:9]
	v_readlane_b32 s23, v9, s98
	s_sub_i32 s22, 63, s98
	s_nop 0
	v_addc_co_u32_e32 v6, vcc, 0, v6, vcc
	v_cmp_gt_i64_e32 vcc, s[24:25], v[8:9]
	v_readlane_b32 s25, v9, s99
	s_sub_i32 s24, 63, s99
	s_add_i32 s99, s99, 1
	v_addc_co_u32_e32 v6, vcc, 0, v6, vcc
	v_cmp_gt_i64_e32 vcc, s[22:23], v[8:9]
	v_readlane_b32 s23, v9, s99
	s_sub_i32 s22, 63, s99
	s_add_i32 s99, s99, 1
	v_addc_co_u32_e32 v6, vcc, 0, v6, vcc
	v_cmp_gt_i64_e32 vcc, s[24:25], v[8:9]
	v_readlane_b32 s25, v9, s99
	s_sub_i32 s24, 63, s99
	s_add_i32 s99, s99, 1
	v_addc_co_u32_e32 v6, vcc, 0, v6, vcc
	v_cmp_gt_i64_e32 vcc, s[22:23], v[8:9]
	v_readlane_b32 s23, v9, s99
	s_sub_i32 s22, 63, s99
	s_add_i32 s99, s99, 1
	v_addc_co_u32_e32 v6, vcc, 0, v6, vcc
	v_cmp_gt_i64_e32 vcc, s[24:25], v[8:9]
	v_readlane_b32 s25, v9, s99
	s_sub_i32 s24, 63, s99
	s_add_i32 s99, s99, 1
	v_addc_co_u32_e32 v6, vcc, 0, v6, vcc
	v_cmp_gt_i64_e32 vcc, s[22:23], v[8:9]
	v_readlane_b32 s23, v9, s99
	s_sub_i32 s22, 63, s99
	s_add_i32 s99, s99, 1
	v_addc_co_u32_e32 v6, vcc, 0, v6, vcc
	v_cmp_gt_i64_e32 vcc, s[24:25], v[8:9]
	v_readlane_b32 s25, v9, s99
; __device__ __forceinline__ void phase_nrr(const Frame& F, const Args& a, int l, const bf16_t* XA, const float* g, const float* modl, unsigned char* XN8) {
;     ...
;             int rank = 0;
; #pragma unroll 8
;             for (int e2 = 0; e2 < 64; ++e2) { const float v = __int_as_float(__builtin_amdgcn_readlane(__float_as_int(val), e2)); rank += (v > val || (v == val && e2 < lane)) ? 1 : 0; }
;             const bool sel = rank < TOPK;
;             const float ssum = wave_sum(sel ? sc : 0.f);
;             if (sel) { const int p = atomicAdd((int*)(hist + lane), 1); top_e[t * TOPK + rank] = lane; gate[t * TOPK + rank] = sc / ssum * 2.5f; lpos[t * TOPK + rank] = p; }
	s_sub_i32 s24, 63, s99
	s_add_i32 s99, s99, 1
	v_addc_co_u32_e32 v6, vcc, 0, v6, vcc
	v_cmp_gt_i64_e32 vcc, s[22:23], v[8:9]
	v_readlane_b32 s23, v9, s99
	s_sub_i32 s22, 63, s99
	s_nop 0
	v_addc_co_u32_e32 v6, vcc, 0, v6, vcc
	v_cmp_gt_i64_e32 vcc, s[24:25], v[8:9]
	v_readlane_b32 s25, v9, s100
	s_sub_i32 s24, 63, s100
	s_add_i32 s100, s100, 1
	v_addc_co_u32_e32 v6, vcc, 0, v6, vcc
	v_cmp_gt_i64_e32 vcc, s[22:23], v[8:9]
	v_readlane_b32 s23, v9, s100
	s_sub_i32 s22, 63, s100
	s_add_i32 s100, s100, 1
	v_addc_co_u32_e32 v6, vcc, 0, v6, vcc
	v_cmp_gt_i64_e32 vcc, s[24:25], v[8:9]
	v_readlane_b32 s25, v9, s100
	s_sub_i32 s24, 63, s100
	s_add_i32 s100, s100, 1
	v_addc_co_u32_e32 v6, vcc, 0, v6, vcc
	v_cmp_gt_i64_e32 vcc, s[22:23], v[8:9]
	v_readlane_b32 s23, v9, s100
	s_sub_i32 s22, 63, s100
	s_add_i32 s100, s100, 1
	v_addc_co_u32_e32 v6, vcc, 0, v6, vcc
	v_cmp_gt_i64_e32 vcc, s[24:25], v[8:9]
	v_readlane_b32 s25, v9, s100
	s_sub_i32 s24, 63, s100
	s_add_i32 s100, s100, 1
	v_addc_co_u32_e32 v6, vcc, 0, v6, vcc
	v_cmp_gt_i64_e32 vcc, s[22:23], v[8:9]
	v_readlane_b32 s23, v9, s100
	s_sub_i32 s22, 63, s100
	s_add_i32 s100, s100, 1
	v_addc_co_u32_e32 v6, vcc, 0, v6, vcc
	v_cmp_gt_i64_e32 vcc, s[24:25], v[8:9]
	v_readlane_b32 s25, v9, s100
	s_sub_i32 s24, 63, s100
	s_add_i32 s100, s100, 1
	v_addc_co_u32_e32 v6, vcc, 0, v6, vcc
	v_cmp_gt_i64_e32 vcc, s[22:23], v[8:9]
	v_readlane_b32 s23, v9, s100
	s_sub_i32 s22, 63, s100
	s_nop 0
	v_addc_co_u32_e32 v6, vcc, 0, v6, vcc
	v_cmp_gt_i64_e32 vcc, s[24:25], v[8:9]
	v_readlane_b32 s25, v9, s101
	s_sub_i32 s24, 63, s101
	s_add_i32 s101, s101, 1
	v_addc_co_u32_e32 v6, vcc, 0, v6, vcc
	v_cmp_gt_i64_e32 vcc, s[22:23], v[8:9]
	v_readlane_b32 s23, v9, s101
	s_sub_i32 s22, 63, s101
	s_add_i32 s101, s101, 1
	v_addc_co_u32_e32 v6, vcc, 0, v6, vcc
	v_cmp_gt_i64_e32 vcc, s[24:25], v[8:9]
	v_readlane_b32 s25, v9, s101
	s_sub_i32 s24, 63, s101
	s_add_i32 s101, s101, 1
	v_addc_co_u32_e32 v6, vcc, 0, v6, vcc
	v_cmp_gt_i64_e32 vcc, s[22:23], v[8:9]
	v_readlane_b32 s23, v9, s101
	s_sub_i32 s22, 63, s101
	s_add_i32 s101, s101, 1
	v_addc_co_u32_e32 v6, vcc, 0, v6, vcc
	v_cmp_gt_i64_e32 vcc, s[24:25], v[8:9]
	v_readlane_b32 s25, v9, s101
	s_sub_i32 s24, 63, s101
	s_add_i32 s101, s101, 1
	v_addc_co_u32_e32 v6, vcc, 0, v6, vcc
	v_cmp_gt_i64_e32 vcc, s[22:23], v[8:9]
	v_readlane_b32 s23, v9, s101
	s_sub_i32 s22, 63, s101
	s_add_i32 s101, s101, 1
	v_addc_co_u32_e32 v6, vcc, 0, v6, vcc
	v_cmp_gt_i64_e32 vcc, s[24:25], v[8:9]
	v_readlane_b32 s25, v9, s101
	s_sub_i32 s24, 63, s101
	s_add_i32 s101, s101, 1
	v_addc_co_u32_e32 v6, vcc, 0, v6, vcc
	v_cmp_gt_i64_e32 vcc, s[22:23], v[8:9]
	v_readlane_b32 s23, v9, s101
	s_sub_i32 s22, 63, s101
	s_nop 0
	v_addc_co_u32_e32 v6, vcc, 0, v6, vcc
	v_cmp_gt_i64_e32 vcc, s[24:25], v[8:9]
	s_nop 1
	v_addc_co_u32_e32 v6, vcc, 0, v6, vcc
	v_cmp_gt_i64_e32 vcc, s[22:23], v[8:9]
	s_nop 1
	v_addc_co_u32_e32 v6, vcc, 0, v6, vcc
	v_cmp_gt_u32_e32 vcc, 6, v6
	s_nop 1
	v_cndmask_b32_e32 v5, 0, v2, vcc
	s_nop 1
	v_add_f32_dpp v5, v5, v5 quad_perm:[1,0,3,2] row_mask:0xf bank_mask:0xf
	s_nop 1
	v_add_f32_dpp v5, v5, v5 quad_perm:[2,3,0,1] row_mask:0xf bank_mask:0xf
	s_nop 1
	v_add_f32_dpp v5, v5, v5 row_half_mirror row_mask:0xf bank_mask:0xf
	s_nop 1
	v_add_f32_dpp v5, v5, v5 row_mirror row_mask:0xf bank_mask:0xf
	s_nop 0
	ds_bpermute_b32 v7, v222, v5
	s_waitcnt lgkmcnt(0)
	v_add_f32_e32 v5, v5, v7
	v_mov_b32_e32 v7, v5
	s_nop 1
	v_permlane32_swap_b32_e32 v7, v5
	s_and_saveexec_b64 s[2:3], vcc
	s_cbranch_execz .LBB0_559
	s_waitcnt lgkmcnt(0)
	v_add_f32_e32 v5, v5, v7
	v_div_scale_f32 v11, s[4:5], v5, v5, v2
	v_add3_u32 v6, s36, 30, v6
	v_rcp_f32_e32 v12, v11
	v_ashrrev_i32_e32 v7, 31, v6
	v_lshlrev_b64 v[6:7], 2, v[6:7]
	v_lshl_add_u64 v[8:9], s[26:27], 0, v[6:7]
	ds_add_rtn_u32 v10, v227, v243
	global_store_dword v[8:9], v230, off
	v_fma_f32 v8, -v11, v12, 1.0
	v_fmac_f32_e32 v12, v8, v12
	v_div_scale_f32 v8, vcc, v2, v5, v2
	v_mul_f32_e32 v9, v8, v12
	v_fma_f32 v13, -v11, v9, v8
	v_fmac_f32_e32 v9, v13, v12
	v_fma_f32 v8, -v11, v9, v8
	v_div_fmas_f32 v8, v8, v12, v9
	v_div_fixup_f32 v2, v8, v5, v2
	v_mul_f32_e32 v2, 0x40200000, v2
	v_lshl_add_u64 v[8:9], s[28:29], 0, v[6:7]
	v_lshl_add_u64 v[6:7], s[30:31], 0, v[6:7]
	global_store_dword v[8:9], v2, off
	s_waitcnt lgkmcnt(0)
	global_store_dword v[6:7], v10, off
; __device__ __forceinline__ void phase_nrr(const Frame& F, const Args& a, int l, const bf16_t* XA, const float* g, const float* modl, unsigned char* XN8) {
;     ...
;         for (int i = 0; i < 8; ++i) { const int t = tb + i;
;             const float lg = Pl[(w * 8 + i) * NE + lane] + Pl[(64 + w * 8 + i) * NE + lane]; const float sc = 1.f / (1.f + __expf(-lg)); const float bb = sc + bias;
;             float m1 = bb; m1 = fmaxf(m1, __shfl_xor(m1, 1)); m1 = fmaxf(m1, __shfl_xor(m1, 2)); m1 = fmaxf(m1, __shfl_xor(m1, 4));
;             const unsigned long long eq = __ballot(bb == m1); const int gbase = lane & ~7; const unsigned grpmask = (unsigned)((eq >> gbase) & 0xffull);
;             const int first = gbase + __builtin_ctz(grpmask);
;             float m2 = (lane == first) ? -INFINITY : bb; m2 = fmaxf(m2, __shfl_xor(m2, 1)); m2 = fmaxf(m2, __shfl_xor(m2, 2)); m2 = fmaxf(m2, __shfl_xor(m2, 4));
;             const float gsum = m1 + m2; const int gq = lane >> 3;
;             int grank = 0;
; #pragma unroll
;             for (int g2 = 0; g2 < 8; ++g2) { const float v = __int_as_float(__builtin_amdgcn_readlane(__float_as_int(gsum), g2 * 8)); grank += (v > gsum || (v == gsum && g2 < gq)) ? 1 : 0; }
;             const bool keep = grank < 4; const float val = keep ? bb : -INFINITY;
;             int rank = 0;
; #pragma unroll 8
;             for (int e2 = 0; e2 < 64; ++e2) { const float v = __int_as_float(__builtin_amdgcn_readlane(__float_as_int(val), e2)); rank += (v > val || (v == val && e2 < lane)) ? 1 : 0; }
.LBB0_559:
	s_or_b64 exec, exec, s[2:3]
	v_add_u32_e32 v2, s86, v226
	ds_read_b32 v2, v2
	ds_read_b32 v5, v4 offset:17920
	s_waitcnt lgkmcnt(0)
	v_add_f32_e32 v2, v2, v5
	v_mul_f32_e32 v2, 0xbfb8aa3b, v2
	v_exp_f32_e32 v2, v2
	s_nop 0
	v_add_f32_e32 v2, 1.0, v2
	v_div_scale_f32 v5, s[2:3], v2, v2, 1.0
	v_rcp_f32_e32 v6, v5
	s_mov_b32 s2, 0
	v_fma_f32 v7, -v5, v6, 1.0
	v_fmac_f32_e32 v6, v7, v6
	v_div_scale_f32 v7, vcc, 1.0, v2, 1.0
	v_mul_f32_e32 v8, v7, v6
	v_fma_f32 v9, -v5, v8, v7
	v_fmac_f32_e32 v8, v9, v6
	v_fma_f32 v5, -v5, v8, v7
	v_div_fmas_f32 v5, v5, v6, v8
	v_div_fixup_f32 v2, v5, v2, 1.0
	v_add_f32_e32 v5, v3, v2
	s_nop 1
	s_waitcnt lgkmcnt(0)
	v_max_f32_dpp v6, v5, v5 quad_perm:[1,0,3,2] row_mask:0xf bank_mask:0xf
	s_nop 1
	s_waitcnt lgkmcnt(0)
	v_max_f32_dpp v6, v6, v6 quad_perm:[2,3,0,1] row_mask:0xf bank_mask:0xf
	s_nop 1
	s_waitcnt lgkmcnt(0)
	v_max_f32_dpp v8, v6, v6 row_half_mirror row_mask:0xf bank_mask:0xf
	v_cmp_eq_f32_e32 vcc, v5, v8
	s_nop 1
	v_lshrrev_b64 v[6:7], v200, vcc
	v_ffbl_b32_sdwa v6, v6 dst_sel:DWORD dst_unused:UNUSED_PAD src0_sel:BYTE_0
	v_add_u32_e32 v6, v6, v200
	v_cmp_ne_u32_e32 vcc, v230, v6
	s_nop 1
	v_cndmask_b32_e32 v6, v245, v5, vcc
	s_nop 1
	s_waitcnt lgkmcnt(0)
	v_max_f32_dpp v6, v6, v6 quad_perm:[1,0,3,2] row_mask:0xf bank_mask:0xf
	s_nop 1
	s_waitcnt lgkmcnt(0)
	v_max_f32_dpp v6, v6, v6 quad_perm:[2,3,0,1] row_mask:0xf bank_mask:0xf
	s_nop 1
	s_waitcnt lgkmcnt(0)
	v_max_f32_dpp v6, v6, v6 row_half_mirror row_mask:0xf bank_mask:0xf
	v_add_f32_e32 v6, v8, v6
	s_nop 0
	v_readlane_b32 s3, v6, 0
	s_nop 1
	v_cmp_eq_f32_e64 s[22:23], s3, v6
	v_cmp_gt_f32_e32 vcc, s3, v6
	s_and_b64 s[4:5], s[6:7], s[22:23]
	v_readlane_b32 s3, v6, 8
	s_or_b64 s[4:5], vcc, s[4:5]
	v_cndmask_b32_e64 v7, 0, 1, s[4:5]
	v_cmp_eq_f32_e64 s[22:23], s3, v6
	v_cmp_gt_f32_e32 vcc, s3, v6
	s_and_b64 s[4:5], s[8:9], s[22:23]
	v_readlane_b32 s3, v6, 16
	s_or_b64 s[4:5], vcc, s[4:5]
	v_cndmask_b32_e64 v8, 0, 1, s[4:5]
	v_cmp_eq_f32_e64 s[22:23], s3, v6
	v_cmp_gt_f32_e32 vcc, s3, v6
	s_and_b64 s[4:5], s[10:11], s[22:23]
	v_readlane_b32 s3, v6, 24
	s_or_b64 s[4:5], vcc, s[4:5]
	v_cndmask_b32_e64 v9, 0, 1, s[4:5]
	v_cmp_eq_f32_e64 s[22:23], s3, v6
	v_cmp_gt_f32_e32 vcc, s3, v6
	s_and_b64 s[4:5], s[12:13], s[22:23]
	v_readlane_b32 s3, v6, 32
	s_or_b64 s[4:5], vcc, s[4:5]
	v_cndmask_b32_e64 v10, 0, 1, s[4:5]
	v_cmp_eq_f32_e64 s[22:23], s3, v6
	v_cmp_gt_f32_e32 vcc, s3, v6
	s_and_b64 s[4:5], s[14:15], s[22:23]
	v_readlane_b32 s3, v6, 40
	s_or_b64 s[4:5], vcc, s[4:5]
	v_cndmask_b32_e64 v11, 0, 1, s[4:5]
	v_cmp_eq_f32_e64 s[22:23], s3, v6
	v_cmp_gt_f32_e32 vcc, s3, v6
	s_and_b64 s[4:5], s[16:17], s[22:23]
	v_readlane_b32 s3, v6, 48
	s_or_b64 s[4:5], vcc, s[4:5]
	v_cndmask_b32_e64 v12, 0, 1, s[4:5]
	v_cmp_eq_f32_e64 s[22:23], s3, v6
	v_cmp_gt_f32_e32 vcc, s3, v6
	s_and_b64 s[4:5], s[18:19], s[22:23]
	v_readlane_b32 s3, v6, 56
	s_or_b64 s[4:5], vcc, s[4:5]
	v_cndmask_b32_e64 v13, 0, 1, s[4:5]
	v_cmp_gt_f32_e32 vcc, s3, v6
	s_nop 1
	v_cndmask_b32_e64 v6, 0, 1, vcc
	v_add_u32_e32 v6, v8, v6
	v_add3_u32 v6, v6, v7, v9
	v_add3_u32 v6, v6, v10, v11
	v_add3_u32 v6, v6, v12, v13
	v_cmp_eq_u32_e32 vcc, 0, v6
	s_ff1_i32_b64 s98, vcc
	v_cmp_eq_u32_e32 vcc, 1, v6
	s_ff1_i32_b64 s99, vcc
	v_cmp_eq_u32_e32 vcc, 2, v6
	s_ff1_i32_b64 s100, vcc
	v_cmp_eq_u32_e32 vcc, 3, v6
	s_ff1_i32_b64 s101, vcc
	v_cmp_gt_u32_e32 vcc, 4, v6
	v_mov_b32_e32 v6, 0
	s_nop 0
	v_cndmask_b32_e32 v5, v245, v5, vcc
	v_ashrrev_i32_e32 v9, 31, v5
	v_sub_u32_e32 v8, 63, v230
	v_and_b32_e32 v9, 0x7fffffff, v9
	v_xor_b32_e32 v9, v5, v9
	s_nop 0
	v_readlane_b32 s25, v9, s98
	s_sub_i32 s24, 63, s98
	s_add_i32 s98, s98, 1
	v_readlane_b32 s23, v9, s98
	s_sub_i32 s22, 63, s98
	s_add_i32 s98, s98, 1
	v_cmp_gt_i64_e32 vcc, s[24:25], v[8:9]
	v_readlane_b32 s25, v9, s98
	s_sub_i32 s24, 63, s98
	s_add_i32 s98, s98, 1
	v_addc_co_u32_e32 v6, vcc, 0, v6, vcc
	v_cmp_gt_i64_e32 vcc, s[22:23], v[8:9]
	v_readlane_b32 s23, v9, s98
	s_sub_i32 s22, 63, s98
	s_add_i32 s98, s98, 1
	v_addc_co_u32_e32 v6, vcc, 0, v6, vcc
	v_cmp_gt_i64_e32 vcc, s[24:25], v[8:9]
	v_readlane_b32 s25, v9, s98
	s_sub_i32 s24, 63, s98
	s_add_i32 s98, s98, 1
	v_addc_co_u32_e32 v6, vcc, 0, v6, vcc
	v_cmp_gt_i64_e32 vcc, s[22:23], v[8:9]
	v_readlane_b32 s23, v9, s98
	s_sub_i32 s22, 63, s98
	s_add_i32 s98, s98, 1
	v_addc_co_u32_e32 v6, vcc, 0, v6, vcc
	v_cmp_gt_i64_e32 vcc, s[24:25], v[8:9]
	v_readlane_b32 s25, v9, s98
	s_sub_i32 s24, 63, s98
	s_add_i32 s98, s98, 1
	v_addc_co_u32_e32 v6, vcc, 0, v6, vcc
	v_cmp_gt_i64_e32 vcc, s[22:23], v[8:9]
	v_readlane_b32 s23, v9, s98
	s_sub_i32 s22, 63, s98
	s_nop 0
	v_addc_co_u32_e32 v6, vcc, 0, v6, vcc
	v_cmp_gt_i64_e32 vcc, s[24:25], v[8:9]
	v_readlane_b32 s25, v9, s99
	s_sub_i32 s24, 63, s99
	s_add_i32 s99, s99, 1
	v_addc_co_u32_e32 v6, vcc, 0, v6, vcc
	v_cmp_gt_i64_e32 vcc, s[22:23], v[8:9]
	v_readlane_b32 s23, v9, s99
	s_sub_i32 s22, 63, s99
	s_add_i32 s99, s99, 1
	v_addc_co_u32_e32 v6, vcc, 0, v6, vcc
	v_cmp_gt_i64_e32 vcc, s[24:25], v[8:9]
	v_readlane_b32 s25, v9, s99
	s_sub_i32 s24, 63, s99
	s_add_i32 s99, s99, 1
	v_addc_co_u32_e32 v6, vcc, 0, v6, vcc
	v_cmp_gt_i64_e32 vcc, s[22:23], v[8:9]
	v_readlane_b32 s23, v9, s99
	s_sub_i32 s22, 63, s99
	s_add_i32 s99, s99, 1
	v_addc_co_u32_e32 v6, vcc, 0, v6, vcc
	v_cmp_gt_i64_e32 vcc, s[24:25], v[8:9]
	v_readlane_b32 s25, v9, s99
	s_sub_i32 s24, 63, s99
	s_add_i32 s99, s99, 1
	v_addc_co_u32_e32 v6, vcc, 0, v6, vcc
	v_cmp_gt_i64_e32 vcc, s[22:23], v[8:9]
	v_readlane_b32 s23, v9, s99
	s_sub_i32 s22, 63, s99
	s_add_i32 s99, s99, 1
	v_addc_co_u32_e32 v6, vcc, 0, v6, vcc
	v_cmp_gt_i64_e32 vcc, s[24:25], v[8:9]
	v_readlane_b32 s25, v9, s99
; __device__ __forceinline__ void phase_nrr(const Frame& F, const Args& a, int l, const bf16_t* XA, const float* g, const float* modl, unsigned char* XN8) {
;     ...
;             int rank = 0;
; #pragma unroll 8
;             for (int e2 = 0; e2 < 64; ++e2) { const float v = __int_as_float(__builtin_amdgcn_readlane(__float_as_int(val), e2)); rank += (v > val || (v == val && e2 < lane)) ? 1 : 0; }
;             const bool sel = rank < TOPK;
;             const float ssum = wave_sum(sel ? sc : 0.f);
;             if (sel) { const int p = atomicAdd((int*)(hist + lane), 1); top_e[t * TOPK + rank] = lane; gate[t * TOPK + rank] = sc / ssum * 2.5f; lpos[t * TOPK + rank] = p; }
	s_sub_i32 s24, 63, s99
	s_add_i32 s99, s99, 1
	v_addc_co_u32_e32 v6, vcc, 0, v6, vcc
	v_cmp_gt_i64_e32 vcc, s[22:23], v[8:9]
	v_readlane_b32 s23, v9, s99
	s_sub_i32 s22, 63, s99
	s_nop 0
	v_addc_co_u32_e32 v6, vcc, 0, v6, vcc
	v_cmp_gt_i64_e32 vcc, s[24:25], v[8:9]
	v_readlane_b32 s25, v9, s100
	s_sub_i32 s24, 63, s100
	s_add_i32 s100, s100, 1
	v_addc_co_u32_e32 v6, vcc, 0, v6, vcc
	v_cmp_gt_i64_e32 vcc, s[22:23], v[8:9]
	v_readlane_b32 s23, v9, s100
	s_sub_i32 s22, 63, s100
	s_add_i32 s100, s100, 1
	v_addc_co_u32_e32 v6, vcc, 0, v6, vcc
	v_cmp_gt_i64_e32 vcc, s[24:25], v[8:9]
	v_readlane_b32 s25, v9, s100
	s_sub_i32 s24, 63, s100
	s_add_i32 s100, s100, 1
	v_addc_co_u32_e32 v6, vcc, 0, v6, vcc
	v_cmp_gt_i64_e32 vcc, s[22:23], v[8:9]
	v_readlane_b32 s23, v9, s100
	s_sub_i32 s22, 63, s100
	s_add_i32 s100, s100, 1
	v_addc_co_u32_e32 v6, vcc, 0, v6, vcc
	v_cmp_gt_i64_e32 vcc, s[24:25], v[8:9]
	v_readlane_b32 s25, v9, s100
	s_sub_i32 s24, 63, s100
	s_add_i32 s100, s100, 1
	v_addc_co_u32_e32 v6, vcc, 0, v6, vcc
	v_cmp_gt_i64_e32 vcc, s[22:23], v[8:9]
	v_readlane_b32 s23, v9, s100
	s_sub_i32 s22, 63, s100
	s_add_i32 s100, s100, 1
	v_addc_co_u32_e32 v6, vcc, 0, v6, vcc
	v_cmp_gt_i64_e32 vcc, s[24:25], v[8:9]
	v_readlane_b32 s25, v9, s100
	s_sub_i32 s24, 63, s100
	s_add_i32 s100, s100, 1
	v_addc_co_u32_e32 v6, vcc, 0, v6, vcc
	v_cmp_gt_i64_e32 vcc, s[22:23], v[8:9]
	v_readlane_b32 s23, v9, s100
	s_sub_i32 s22, 63, s100
	s_nop 0
	v_addc_co_u32_e32 v6, vcc, 0, v6, vcc
	v_cmp_gt_i64_e32 vcc, s[24:25], v[8:9]
	v_readlane_b32 s25, v9, s101
	s_sub_i32 s24, 63, s101
	s_add_i32 s101, s101, 1
	v_addc_co_u32_e32 v6, vcc, 0, v6, vcc
	v_cmp_gt_i64_e32 vcc, s[22:23], v[8:9]
	v_readlane_b32 s23, v9, s101
	s_sub_i32 s22, 63, s101
	s_add_i32 s101, s101, 1
	v_addc_co_u32_e32 v6, vcc, 0, v6, vcc
	v_cmp_gt_i64_e32 vcc, s[24:25], v[8:9]
	v_readlane_b32 s25, v9, s101
	s_sub_i32 s24, 63, s101
	s_add_i32 s101, s101, 1
	v_addc_co_u32_e32 v6, vcc, 0, v6, vcc
	v_cmp_gt_i64_e32 vcc, s[22:23], v[8:9]
	v_readlane_b32 s23, v9, s101
	s_sub_i32 s22, 63, s101
	s_add_i32 s101, s101, 1
	v_addc_co_u32_e32 v6, vcc, 0, v6, vcc
	v_cmp_gt_i64_e32 vcc, s[24:25], v[8:9]
	v_readlane_b32 s25, v9, s101
	s_sub_i32 s24, 63, s101
	s_add_i32 s101, s101, 1
	v_addc_co_u32_e32 v6, vcc, 0, v6, vcc
	v_cmp_gt_i64_e32 vcc, s[22:23], v[8:9]
	v_readlane_b32 s23, v9, s101
	s_sub_i32 s22, 63, s101
	s_add_i32 s101, s101, 1
	v_addc_co_u32_e32 v6, vcc, 0, v6, vcc
	v_cmp_gt_i64_e32 vcc, s[24:25], v[8:9]
	v_readlane_b32 s25, v9, s101
	s_sub_i32 s24, 63, s101
	s_add_i32 s101, s101, 1
	v_addc_co_u32_e32 v6, vcc, 0, v6, vcc
	v_cmp_gt_i64_e32 vcc, s[22:23], v[8:9]
	v_readlane_b32 s23, v9, s101
	s_sub_i32 s22, 63, s101
	s_nop 0
	v_addc_co_u32_e32 v6, vcc, 0, v6, vcc
	v_cmp_gt_i64_e32 vcc, s[24:25], v[8:9]
	s_nop 1
	v_addc_co_u32_e32 v6, vcc, 0, v6, vcc
	v_cmp_gt_i64_e32 vcc, s[22:23], v[8:9]
	s_nop 1
	v_addc_co_u32_e32 v6, vcc, 0, v6, vcc
	v_cmp_gt_u32_e32 vcc, 6, v6
	s_nop 1
	v_cndmask_b32_e32 v5, 0, v2, vcc
	s_nop 1
	v_add_f32_dpp v5, v5, v5 quad_perm:[1,0,3,2] row_mask:0xf bank_mask:0xf
	s_nop 1
	v_add_f32_dpp v5, v5, v5 quad_perm:[2,3,0,1] row_mask:0xf bank_mask:0xf
	s_nop 1
	v_add_f32_dpp v5, v5, v5 row_half_mirror row_mask:0xf bank_mask:0xf
	s_nop 1
	v_add_f32_dpp v5, v5, v5 row_mirror row_mask:0xf bank_mask:0xf
	s_nop 0
	ds_bpermute_b32 v7, v222, v5
	s_waitcnt lgkmcnt(0)
	v_add_f32_e32 v5, v5, v7
	v_mov_b32_e32 v7, v5
	s_nop 1
	v_permlane32_swap_b32_e32 v7, v5
	s_and_saveexec_b64 s[2:3], vcc
	s_cbranch_execz .LBB0_563
	s_waitcnt lgkmcnt(0)
	v_add_f32_e32 v5, v5, v7
	v_div_scale_f32 v11, s[4:5], v5, v5, v2
	v_add3_u32 v6, s36, 36, v6
	v_rcp_f32_e32 v12, v11
	v_ashrrev_i32_e32 v7, 31, v6
	v_lshlrev_b64 v[6:7], 2, v[6:7]
	v_lshl_add_u64 v[8:9], s[26:27], 0, v[6:7]
	ds_add_rtn_u32 v10, v227, v243
	global_store_dword v[8:9], v230, off
	v_fma_f32 v8, -v11, v12, 1.0
	v_fmac_f32_e32 v12, v8, v12
	v_div_scale_f32 v8, vcc, v2, v5, v2
	v_mul_f32_e32 v9, v8, v12
	v_fma_f32 v13, -v11, v9, v8
	v_fmac_f32_e32 v9, v13, v12
	v_fma_f32 v8, -v11, v9, v8
	v_div_fmas_f32 v8, v8, v12, v9
	v_div_fixup_f32 v2, v8, v5, v2
	v_mul_f32_e32 v2, 0x40200000, v2
	v_lshl_add_u64 v[8:9], s[28:29], 0, v[6:7]
	v_lshl_add_u64 v[6:7], s[30:31], 0, v[6:7]
	global_store_dword v[8:9], v2, off
	s_waitcnt lgkmcnt(0)
	global_store_dword v[6:7], v10, off
; __device__ __forceinline__ void phase_nrr(const Frame& F, const Args& a, int l, const bf16_t* XA, const float* g, const float* modl, unsigned char* XN8) {
;     ...
;         for (int i = 0; i < 8; ++i) { const int t = tb + i;
;             const float lg = Pl[(w * 8 + i) * NE + lane] + Pl[(64 + w * 8 + i) * NE + lane]; const float sc = 1.f / (1.f + __expf(-lg)); const float bb = sc + bias;
;             float m1 = bb; m1 = fmaxf(m1, __shfl_xor(m1, 1)); m1 = fmaxf(m1, __shfl_xor(m1, 2)); m1 = fmaxf(m1, __shfl_xor(m1, 4));
;             const unsigned long long eq = __ballot(bb == m1); const int gbase = lane & ~7; const unsigned grpmask = (unsigned)((eq >> gbase) & 0xffull);
;             const int first = gbase + __builtin_ctz(grpmask);
;             float m2 = (lane == first) ? -INFINITY : bb; m2 = fmaxf(m2, __shfl_xor(m2, 1)); m2 = fmaxf(m2, __shfl_xor(m2, 2)); m2 = fmaxf(m2, __shfl_xor(m2, 4));
;             const float gsum = m1 + m2; const int gq = lane >> 3;
;             int grank = 0;
; #pragma unroll
;             for (int g2 = 0; g2 < 8; ++g2) { const float v = __int_as_float(__builtin_amdgcn_readlane(__float_as_int(gsum), g2 * 8)); grank += (v > gsum || (v == gsum && g2 < gq)) ? 1 : 0; }
;             const bool keep = grank < 4; const float val = keep ? bb : -INFINITY;
;             int rank = 0;
; #pragma unroll 8
;             for (int e2 = 0; e2 < 64; ++e2) { const float v = __int_as_float(__builtin_amdgcn_readlane(__float_as_int(val), e2)); rank += (v > val || (v == val && e2 < lane)) ? 1 : 0; }
.LBB0_563:
	s_or_b64 exec, exec, s[2:3]
	v_add_u32_e32 v2, s87, v226
	ds_read_b32 v2, v2
	ds_read_b32 v4, v4 offset:18176
	s_waitcnt lgkmcnt(0)
	v_add_f32_e32 v2, v2, v4
	v_mul_f32_e32 v2, 0xbfb8aa3b, v2
	v_exp_f32_e32 v2, v2
	s_nop 0
	v_add_f32_e32 v2, 1.0, v2
	v_div_scale_f32 v4, s[2:3], v2, v2, 1.0
	v_rcp_f32_e32 v5, v4
	s_mov_b32 s2, 0
	v_fma_f32 v6, -v4, v5, 1.0
	v_fmac_f32_e32 v5, v6, v5
	v_div_scale_f32 v6, vcc, 1.0, v2, 1.0
	v_mul_f32_e32 v7, v6, v5
	v_fma_f32 v8, -v4, v7, v6
	v_fmac_f32_e32 v7, v8, v5
	v_fma_f32 v4, -v4, v7, v6
	v_div_fmas_f32 v4, v4, v5, v7
	v_div_fixup_f32 v2, v4, v2, 1.0
	v_add_f32_e32 v3, v3, v2
	s_nop 1
	s_waitcnt lgkmcnt(0)
	v_max_f32_dpp v4, v3, v3 quad_perm:[1,0,3,2] row_mask:0xf bank_mask:0xf
	s_nop 1
	s_waitcnt lgkmcnt(0)
	v_max_f32_dpp v4, v4, v4 quad_perm:[2,3,0,1] row_mask:0xf bank_mask:0xf
	s_nop 1
	s_waitcnt lgkmcnt(0)
	v_max_f32_dpp v6, v4, v4 row_half_mirror row_mask:0xf bank_mask:0xf
	v_cmp_eq_f32_e32 vcc, v3, v6
	s_nop 1
	v_lshrrev_b64 v[4:5], v200, vcc
	v_ffbl_b32_sdwa v4, v4 dst_sel:DWORD dst_unused:UNUSED_PAD src0_sel:BYTE_0
	v_add_u32_e32 v4, v4, v200
	v_cmp_ne_u32_e32 vcc, v230, v4
	s_nop 1
	v_cndmask_b32_e32 v4, v245, v3, vcc
	s_nop 1
	s_waitcnt lgkmcnt(0)
	v_max_f32_dpp v4, v4, v4 quad_perm:[1,0,3,2] row_mask:0xf bank_mask:0xf
	s_nop 1
	s_waitcnt lgkmcnt(0)
	v_max_f32_dpp v4, v4, v4 quad_perm:[2,3,0,1] row_mask:0xf bank_mask:0xf
	s_nop 1
	s_waitcnt lgkmcnt(0)
	v_max_f32_dpp v4, v4, v4 row_half_mirror row_mask:0xf bank_mask:0xf
	v_add_f32_e32 v4, v6, v4
	s_nop 0
	v_readlane_b32 s3, v4, 0
	s_nop 1
	v_cmp_eq_f32_e64 s[22:23], s3, v4
	v_cmp_gt_f32_e32 vcc, s3, v4
	s_and_b64 s[4:5], s[6:7], s[22:23]
	v_readlane_b32 s3, v4, 8
	s_or_b64 s[4:5], vcc, s[4:5]
	v_cndmask_b32_e64 v5, 0, 1, s[4:5]
	v_cmp_eq_f32_e64 s[22:23], s3, v4
	v_cmp_gt_f32_e32 vcc, s3, v4
	s_and_b64 s[4:5], s[8:9], s[22:23]
	v_readlane_b32 s3, v4, 16
	s_or_b64 s[4:5], vcc, s[4:5]
	v_cndmask_b32_e64 v6, 0, 1, s[4:5]
	v_cmp_eq_f32_e64 s[22:23], s3, v4
	v_cmp_gt_f32_e32 vcc, s3, v4
	s_and_b64 s[4:5], s[10:11], s[22:23]
	v_readlane_b32 s3, v4, 24
	s_or_b64 s[4:5], vcc, s[4:5]
	v_cndmask_b32_e64 v7, 0, 1, s[4:5]
	v_cmp_eq_f32_e64 s[22:23], s3, v4
	v_cmp_gt_f32_e32 vcc, s3, v4
	s_and_b64 s[4:5], s[12:13], s[22:23]
	v_readlane_b32 s3, v4, 32
	s_or_b64 s[4:5], vcc, s[4:5]
	v_cndmask_b32_e64 v8, 0, 1, s[4:5]
	v_cmp_eq_f32_e64 s[22:23], s3, v4
	v_cmp_gt_f32_e32 vcc, s3, v4
	s_and_b64 s[4:5], s[14:15], s[22:23]
	v_readlane_b32 s3, v4, 40
	s_or_b64 s[4:5], vcc, s[4:5]
	v_cndmask_b32_e64 v9, 0, 1, s[4:5]
	v_cmp_eq_f32_e64 s[22:23], s3, v4
	v_cmp_gt_f32_e32 vcc, s3, v4
	s_and_b64 s[4:5], s[16:17], s[22:23]
	v_readlane_b32 s3, v4, 48
	s_or_b64 s[4:5], vcc, s[4:5]
	v_cndmask_b32_e64 v10, 0, 1, s[4:5]
	v_cmp_eq_f32_e64 s[22:23], s3, v4
	v_cmp_gt_f32_e32 vcc, s3, v4
	s_and_b64 s[4:5], s[18:19], s[22:23]
	v_readlane_b32 s3, v4, 56
	s_or_b64 s[4:5], vcc, s[4:5]
	v_cndmask_b32_e64 v11, 0, 1, s[4:5]
	v_cmp_gt_f32_e32 vcc, s3, v4
	s_nop 1
	v_cndmask_b32_e64 v4, 0, 1, vcc
	v_add_u32_e32 v4, v6, v4
	v_add3_u32 v4, v4, v5, v7
	v_add3_u32 v4, v4, v8, v9
	v_add3_u32 v4, v4, v10, v11
	v_cmp_eq_u32_e32 vcc, 0, v4
	s_ff1_i32_b64 s98, vcc
	v_cmp_eq_u32_e32 vcc, 1, v4
	s_ff1_i32_b64 s99, vcc
	v_cmp_eq_u32_e32 vcc, 2, v4
	s_ff1_i32_b64 s100, vcc
	v_cmp_eq_u32_e32 vcc, 3, v4
	s_ff1_i32_b64 s101, vcc
	v_cmp_gt_u32_e32 vcc, 4, v4
	v_mov_b32_e32 v4, 0
	s_nop 0
	v_cndmask_b32_e32 v3, v245, v3, vcc
	v_ashrrev_i32_e32 v9, 31, v3
	v_sub_u32_e32 v8, 63, v230
	v_and_b32_e32 v9, 0x7fffffff, v9
	v_xor_b32_e32 v9, v3, v9
	s_nop 0
	v_readlane_b32 s25, v9, s98
	s_sub_i32 s24, 63, s98
	s_add_i32 s98, s98, 1
	v_readlane_b32 s23, v9, s98
	s_sub_i32 s22, 63, s98
	s_add_i32 s98, s98, 1
	v_cmp_gt_i64_e32 vcc, s[24:25], v[8:9]
	v_readlane_b32 s25, v9, s98
	s_sub_i32 s24, 63, s98
	s_add_i32 s98, s98, 1
	v_addc_co_u32_e32 v4, vcc, 0, v4, vcc
	v_cmp_gt_i64_e32 vcc, s[22:23], v[8:9]
	v_readlane_b32 s23, v9, s98
	s_sub_i32 s22, 63, s98
	s_add_i32 s98, s98, 1
	v_addc_co_u32_e32 v4, vcc, 0, v4, vcc
	v_cmp_gt_i64_e32 vcc, s[24:25], v[8:9]
	v_readlane_b32 s25, v9, s98
	s_sub_i32 s24, 63, s98
	s_add_i32 s98, s98, 1
	v_addc_co_u32_e32 v4, vcc, 0, v4, vcc
	v_cmp_gt_i64_e32 vcc, s[22:23], v[8:9]
	v_readlane_b32 s23, v9, s98
	s_sub_i32 s22, 63, s98
	s_add_i32 s98, s98, 1
	v_addc_co_u32_e32 v4, vcc, 0, v4, vcc
	v_cmp_gt_i64_e32 vcc, s[24:25], v[8:9]
	v_readlane_b32 s25, v9, s98
	s_sub_i32 s24, 63, s98
	s_add_i32 s98, s98, 1
	v_addc_co_u32_e32 v4, vcc, 0, v4, vcc
	v_cmp_gt_i64_e32 vcc, s[22:23], v[8:9]
	v_readlane_b32 s23, v9, s98
	s_sub_i32 s22, 63, s98
	s_nop 0
	v_addc_co_u32_e32 v4, vcc, 0, v4, vcc
	v_cmp_gt_i64_e32 vcc, s[24:25], v[8:9]
	v_readlane_b32 s25, v9, s99
	s_sub_i32 s24, 63, s99
	s_add_i32 s99, s99, 1
	v_addc_co_u32_e32 v4, vcc, 0, v4, vcc
	v_cmp_gt_i64_e32 vcc, s[22:23], v[8:9]
	v_readlane_b32 s23, v9, s99
	s_sub_i32 s22, 63, s99
	s_add_i32 s99, s99, 1
	v_addc_co_u32_e32 v4, vcc, 0, v4, vcc
	v_cmp_gt_i64_e32 vcc, s[24:25], v[8:9]
; __device__ __forceinline__ void phase_nrr(const Frame& F, const Args& a, int l, const bf16_t* XA, const float* g, const float* modl, unsigned char* XN8) {
;     ...
;             int rank = 0;
; #pragma unroll 8
;             for (int e2 = 0; e2 < 64; ++e2) { const float v = __int_as_float(__builtin_amdgcn_readlane(__float_as_int(val), e2)); rank += (v > val || (v == val && e2 < lane)) ? 1 : 0; }
;             const bool sel = rank < TOPK;
;             const float ssum = wave_sum(sel ? sc : 0.f);
;             if (sel) { const int p = atomicAdd((int*)(hist + lane), 1); top_e[t * TOPK + rank] = lane; gate[t * TOPK + rank] = sc / ssum * 2.5f; lpos[t * TOPK + rank] = p; }
	v_readlane_b32 s25, v9, s99
	s_sub_i32 s24, 63, s99
	s_add_i32 s99, s99, 1
	v_addc_co_u32_e32 v4, vcc, 0, v4, vcc
	v_cmp_gt_i64_e32 vcc, s[22:23], v[8:9]
	v_readlane_b32 s23, v9, s99
	s_sub_i32 s22, 63, s99
	s_add_i32 s99, s99, 1
	v_addc_co_u32_e32 v4, vcc, 0, v4, vcc
	v_cmp_gt_i64_e32 vcc, s[24:25], v[8:9]
	v_readlane_b32 s25, v9, s99
	s_sub_i32 s24, 63, s99
	s_add_i32 s99, s99, 1
	v_addc_co_u32_e32 v4, vcc, 0, v4, vcc
	v_cmp_gt_i64_e32 vcc, s[22:23], v[8:9]
	v_readlane_b32 s23, v9, s99
	s_sub_i32 s22, 63, s99
	s_add_i32 s99, s99, 1
	v_addc_co_u32_e32 v4, vcc, 0, v4, vcc
	v_cmp_gt_i64_e32 vcc, s[24:25], v[8:9]
	v_readlane_b32 s25, v9, s99
	s_sub_i32 s24, 63, s99
	s_add_i32 s99, s99, 1
	v_addc_co_u32_e32 v4, vcc, 0, v4, vcc
	v_cmp_gt_i64_e32 vcc, s[22:23], v[8:9]
	v_readlane_b32 s23, v9, s99
	s_sub_i32 s22, 63, s99
	s_nop 0
	v_addc_co_u32_e32 v4, vcc, 0, v4, vcc
	v_cmp_gt_i64_e32 vcc, s[24:25], v[8:9]
	v_readlane_b32 s25, v9, s100
	s_sub_i32 s24, 63, s100
	s_add_i32 s100, s100, 1
	v_addc_co_u32_e32 v4, vcc, 0, v4, vcc
	v_cmp_gt_i64_e32 vcc, s[22:23], v[8:9]
	v_readlane_b32 s23, v9, s100
	s_sub_i32 s22, 63, s100
	s_add_i32 s100, s100, 1
	v_addc_co_u32_e32 v4, vcc, 0, v4, vcc
	v_cmp_gt_i64_e32 vcc, s[24:25], v[8:9]
	v_readlane_b32 s25, v9, s100
	s_sub_i32 s24, 63, s100
	s_add_i32 s100, s100, 1
	v_addc_co_u32_e32 v4, vcc, 0, v4, vcc
	v_cmp_gt_i64_e32 vcc, s[22:23], v[8:9]
	v_readlane_b32 s23, v9, s100
	s_sub_i32 s22, 63, s100
	s_add_i32 s100, s100, 1
	v_addc_co_u32_e32 v4, vcc, 0, v4, vcc
	v_cmp_gt_i64_e32 vcc, s[24:25], v[8:9]
	v_readlane_b32 s25, v9, s100
	s_sub_i32 s24, 63, s100
	s_add_i32 s100, s100, 1
	v_addc_co_u32_e32 v4, vcc, 0, v4, vcc
	v_cmp_gt_i64_e32 vcc, s[22:23], v[8:9]
	v_readlane_b32 s23, v9, s100
	s_sub_i32 s22, 63, s100
	s_add_i32 s100, s100, 1
	v_addc_co_u32_e32 v4, vcc, 0, v4, vcc
	v_cmp_gt_i64_e32 vcc, s[24:25], v[8:9]
	v_readlane_b32 s25, v9, s100
	s_sub_i32 s24, 63, s100
	s_add_i32 s100, s100, 1
	v_addc_co_u32_e32 v4, vcc, 0, v4, vcc
	v_cmp_gt_i64_e32 vcc, s[22:23], v[8:9]
	v_readlane_b32 s23, v9, s100
	s_sub_i32 s22, 63, s100
	s_nop 0
	v_addc_co_u32_e32 v4, vcc, 0, v4, vcc
	v_cmp_gt_i64_e32 vcc, s[24:25], v[8:9]
	v_readlane_b32 s25, v9, s101
	s_sub_i32 s24, 63, s101
	s_add_i32 s101, s101, 1
	v_addc_co_u32_e32 v4, vcc, 0, v4, vcc
	v_cmp_gt_i64_e32 vcc, s[22:23], v[8:9]
	v_readlane_b32 s23, v9, s101
	s_sub_i32 s22, 63, s101
	s_add_i32 s101, s101, 1
	v_addc_co_u32_e32 v4, vcc, 0, v4, vcc
	v_cmp_gt_i64_e32 vcc, s[24:25], v[8:9]
	v_readlane_b32 s25, v9, s101
	s_sub_i32 s24, 63, s101
	s_add_i32 s101, s101, 1
	v_addc_co_u32_e32 v4, vcc, 0, v4, vcc
	v_cmp_gt_i64_e32 vcc, s[22:23], v[8:9]
	v_readlane_b32 s23, v9, s101
	s_sub_i32 s22, 63, s101
	s_add_i32 s101, s101, 1
	v_addc_co_u32_e32 v4, vcc, 0, v4, vcc
	v_cmp_gt_i64_e32 vcc, s[24:25], v[8:9]
	v_readlane_b32 s25, v9, s101
	s_sub_i32 s24, 63, s101
	s_add_i32 s101, s101, 1
	v_addc_co_u32_e32 v4, vcc, 0, v4, vcc
	v_cmp_gt_i64_e32 vcc, s[22:23], v[8:9]
	v_readlane_b32 s23, v9, s101
	s_sub_i32 s22, 63, s101
	s_add_i32 s101, s101, 1
	v_addc_co_u32_e32 v4, vcc, 0, v4, vcc
	v_cmp_gt_i64_e32 vcc, s[24:25], v[8:9]
	v_readlane_b32 s25, v9, s101
	s_sub_i32 s24, 63, s101
	s_add_i32 s101, s101, 1
	v_addc_co_u32_e32 v4, vcc, 0, v4, vcc
	v_cmp_gt_i64_e32 vcc, s[22:23], v[8:9]
	v_readlane_b32 s23, v9, s101
	s_sub_i32 s22, 63, s101
	s_nop 0
	v_addc_co_u32_e32 v4, vcc, 0, v4, vcc
	v_cmp_gt_i64_e32 vcc, s[24:25], v[8:9]
	s_nop 1
	v_addc_co_u32_e32 v4, vcc, 0, v4, vcc
	v_cmp_gt_i64_e32 vcc, s[22:23], v[8:9]
	s_nop 1
	v_addc_co_u32_e32 v4, vcc, 0, v4, vcc
	v_cmp_gt_u32_e32 vcc, 6, v4
	s_nop 1
	v_cndmask_b32_e32 v3, 0, v2, vcc
	s_nop 1
	v_add_f32_dpp v3, v3, v3 quad_perm:[1,0,3,2] row_mask:0xf bank_mask:0xf
	s_nop 1
	v_add_f32_dpp v3, v3, v3 quad_perm:[2,3,0,1] row_mask:0xf bank_mask:0xf
	s_nop 1
	v_add_f32_dpp v3, v3, v3 row_half_mirror row_mask:0xf bank_mask:0xf
	s_nop 1
	v_add_f32_dpp v3, v3, v3 row_mirror row_mask:0xf bank_mask:0xf
	s_nop 0
	ds_bpermute_b32 v5, v222, v3
	s_waitcnt lgkmcnt(0)
	v_add_f32_e32 v3, v3, v5
	v_mov_b32_e32 v5, v3
	s_nop 1
	v_permlane32_swap_b32_e32 v5, v3
	s_and_saveexec_b64 s[2:3], vcc
	s_cbranch_execz .LBB0_567
	s_waitcnt lgkmcnt(0)
	v_add_f32_e32 v3, v3, v5
	v_div_scale_f32 v9, s[4:5], v3, v3, v2
	v_add3_u32 v4, s36, 42, v4
	v_rcp_f32_e32 v10, v9
	v_ashrrev_i32_e32 v5, 31, v4
	v_lshlrev_b64 v[4:5], 2, v[4:5]
	v_lshl_add_u64 v[6:7], s[26:27], 0, v[4:5]
	ds_add_rtn_u32 v8, v227, v243
	global_store_dword v[6:7], v230, off
	v_fma_f32 v6, -v9, v10, 1.0
	v_fmac_f32_e32 v10, v6, v10
	v_div_scale_f32 v6, vcc, v2, v3, v2
	v_mul_f32_e32 v7, v6, v10
	v_fma_f32 v11, -v9, v7, v6
	v_fmac_f32_e32 v7, v11, v10
	v_fma_f32 v6, -v9, v7, v6
	v_div_fmas_f32 v6, v6, v10, v7
	v_div_fixup_f32 v2, v6, v3, v2
	v_mul_f32_e32 v6, 0x40200000, v2
	v_lshl_add_u64 v[2:3], s[28:29], 0, v[4:5]
	global_store_dword v[2:3], v6, off
	v_lshl_add_u64 v[2:3], s[30:31], 0, v[4:5]
	s_waitcnt lgkmcnt(0)
	global_store_dword v[2:3], v8, off

; #define LAS __attribute__((address_space(3)))
; __device__ __forceinline__ void phase_nrr(const Frame& F, const Args& a, int l, const bf16_t* XA, const float* g, const float* modl, unsigned char* XN8) {
;     ...
;         __syncthreads();
; #pragma unroll
;         for (int rb = 0; rb < 4; ++rb) *(LAS f32x4*)(Pl + (size_t)((kq * 64 + 16 * rb + fr) * NE + 16 * eb + 4 * fq)) = acc[rb];
;         __syncthreads();
;         const float bias = rbias[lane];
; #pragma unroll
;         for (int i = 0; i < 8; ++i) { const int t = tb + i;
;             const float lg = Pl[(w * 8 + i) * NE + lane] + Pl[(64 + w * 8 + i) * NE + lane]; const float sc = 1.f / (1.f + __expf(-lg)); const float bb = sc + bias;
;             float m1 = bb; m1 = fmaxf(m1, __shfl_xor(m1, 1)); m1 = fmaxf(m1, __shfl_xor(m1, 2)); m1 = fmaxf(m1, __shfl_xor(m1, 4));
;             const unsigned long long eq = __ballot(bb == m1); const int gbase = lane & ~7; const unsigned grpmask = (unsigned)((eq >> gbase) & 0xffull);
;             const int first = gbase + __builtin_ctz(grpmask);
;             float m2 = (lane == first) ? -INFINITY : bb; m2 = fmaxf(m2, __shfl_xor(m2, 1)); m2 = fmaxf(m2, __shfl_xor(m2, 2)); m2 = fmaxf(m2, __shfl_xor(m2, 4));
;             const float gsum = m1 + m2; const int gq = lane >> 3;
;             int grank = 0;
; #pragma unroll
;             for (int g2 = 0; g2 < 8; ++g2) { const float v = __int_as_float(__builtin_amdgcn_readlane(__float_as_int(gsum), g2 * 8)); grank += (v > gsum || (v == gsum && g2 < gq)) ? 1 : 0; }
;             const bool keep = grank < 4; const float val = keep ? bb : -INFINITY;
;             int rank = 0;
; #pragma unroll 8
;             for (int e2 = 0; e2 < 64; ++e2) { const float v = __int_as_float(__builtin_amdgcn_readlane(__float_as_int(val), e2)); rank += (v > val || (v == val && e2 < lane)) ? 1 : 0; }
.LBB0_1308:
	s_barrier
	ds_write_b128 v242, v[110:113]
	ds_write_b128 v242, v[118:121] offset:4096
	s_nop 0
	ds_write_b128 v242, v[126:129] offset:8192
	s_nop 1
	ds_write_b128 v242, v[130:133] offset:12288
	s_waitcnt lgkmcnt(0)
	s_barrier
	global_load_dword v3, v[198:199], off offset:256
	s_waitcnt vmcnt(15)
	v_add_u32_e32 v4, s33, v226
	ds_read2st64_b32 v[6:7], v4 offset1:64
	s_mov_b32 s3, 0
	s_waitcnt lgkmcnt(0)
	v_add_f32_e32 v2, v6, v7
	v_mul_f32_e32 v2, 0xbfb8aa3b, v2
	v_exp_f32_e32 v2, v2
	s_nop 0
	v_add_f32_e32 v2, 1.0, v2
	v_div_scale_f32 v5, s[20:21], v2, v2, 1.0
	v_rcp_f32_e32 v6, v5
	s_nop 0
	v_fma_f32 v7, -v5, v6, 1.0
	v_fmac_f32_e32 v6, v7, v6
	v_div_scale_f32 v7, vcc, 1.0, v2, 1.0
	v_mul_f32_e32 v8, v7, v6
	v_fma_f32 v9, -v5, v8, v7
	v_fmac_f32_e32 v8, v9, v6
	v_fma_f32 v5, -v5, v8, v7
	v_div_fmas_f32 v5, v5, v6, v8
	v_div_fixup_f32 v2, v5, v2, 1.0
	s_waitcnt vmcnt(0)
	v_add_f32_e32 v5, v3, v2
	s_nop 1
	s_waitcnt lgkmcnt(0)
	v_max_f32_dpp v6, v5, v5 quad_perm:[1,0,3,2] row_mask:0xf bank_mask:0xf
	s_nop 1
	s_waitcnt lgkmcnt(0)
	v_max_f32_dpp v6, v6, v6 quad_perm:[2,3,0,1] row_mask:0xf bank_mask:0xf
	s_nop 1
	s_waitcnt lgkmcnt(0)
	v_max_f32_dpp v8, v6, v6 row_half_mirror row_mask:0xf bank_mask:0xf
	v_cmp_eq_f32_e32 vcc, v5, v8
	s_nop 1
	v_lshrrev_b64 v[6:7], v200, vcc
	v_ffbl_b32_sdwa v6, v6 dst_sel:DWORD dst_unused:UNUSED_PAD src0_sel:BYTE_0
	v_add_u32_e32 v6, v6, v200
	v_cmp_ne_u32_e32 vcc, v230, v6
	s_nop 1
	v_cndmask_b32_e32 v6, v245, v5, vcc
	s_nop 1
	s_waitcnt lgkmcnt(0)
	v_max_f32_dpp v6, v6, v6 quad_perm:[1,0,3,2] row_mask:0xf bank_mask:0xf
	s_nop 1
	s_waitcnt lgkmcnt(0)
	v_max_f32_dpp v6, v6, v6 quad_perm:[2,3,0,1] row_mask:0xf bank_mask:0xf
	s_nop 1
	s_waitcnt lgkmcnt(0)
	v_max_f32_dpp v6, v6, v6 row_half_mirror row_mask:0xf bank_mask:0xf
	v_add_f32_e32 v6, v8, v6
	s_nop 0
	v_readlane_b32 s5, v6, 0
	s_nop 1
	v_cmp_eq_f32_e64 s[20:21], s5, v6
	v_cmp_gt_f32_e32 vcc, s5, v6
	s_and_b64 s[20:21], s[0:1], s[20:21]
	s_or_b64 s[20:21], vcc, s[20:21]
	v_readlane_b32 s5, v6, 8
	v_cndmask_b32_e64 v7, 0, 1, s[20:21]
	s_nop 0
	v_cmp_eq_f32_e64 s[20:21], s5, v6
	v_cmp_gt_f32_e32 vcc, s5, v6
	s_and_b64 s[20:21], s[6:7], s[20:21]
	s_or_b64 s[20:21], vcc, s[20:21]
	v_readlane_b32 s5, v6, 16
	v_cndmask_b32_e64 v8, 0, 1, s[20:21]
	s_nop 0
	v_cmp_eq_f32_e64 s[20:21], s5, v6
	v_cmp_gt_f32_e32 vcc, s5, v6
	s_and_b64 s[20:21], s[8:9], s[20:21]
	s_or_b64 s[20:21], vcc, s[20:21]
	v_readlane_b32 s5, v6, 24
	v_cndmask_b32_e64 v9, 0, 1, s[20:21]
	s_nop 0
	v_cmp_eq_f32_e64 s[20:21], s5, v6
	v_cmp_gt_f32_e32 vcc, s5, v6
	s_and_b64 s[20:21], s[10:11], s[20:21]
	s_or_b64 s[20:21], vcc, s[20:21]
	v_readlane_b32 s5, v6, 32
	v_cndmask_b32_e64 v10, 0, 1, s[20:21]
	s_nop 0
	v_cmp_eq_f32_e64 s[20:21], s5, v6
	v_cmp_gt_f32_e32 vcc, s5, v6
	s_and_b64 s[20:21], s[12:13], s[20:21]
	s_or_b64 s[20:21], vcc, s[20:21]
	v_readlane_b32 s5, v6, 40
	v_cndmask_b32_e64 v11, 0, 1, s[20:21]
	s_nop 0
	v_cmp_eq_f32_e64 s[20:21], s5, v6
	v_cmp_gt_f32_e32 vcc, s5, v6
	s_and_b64 s[20:21], s[14:15], s[20:21]
	s_or_b64 s[20:21], vcc, s[20:21]
	v_readlane_b32 s5, v6, 48
	v_cndmask_b32_e64 v12, 0, 1, s[20:21]
	s_nop 0
	v_cmp_eq_f32_e64 s[20:21], s5, v6
	v_cmp_gt_f32_e32 vcc, s5, v6
	s_and_b64 s[20:21], s[16:17], s[20:21]
	v_readlane_b32 s5, v6, 56
	s_or_b64 s[20:21], vcc, s[20:21]
	v_cndmask_b32_e64 v13, 0, 1, s[20:21]
	v_cmp_gt_f32_e32 vcc, s5, v6
	s_nop 1
	v_cndmask_b32_e64 v6, 0, 1, vcc
	v_add_u32_e32 v6, v8, v6
	v_add3_u32 v6, v6, v7, v9
	v_add3_u32 v6, v6, v10, v11
	v_add3_u32 v6, v6, v12, v13
	v_cmp_eq_u32_e32 vcc, 0, v6
	s_ff1_i32_b64 s98, vcc
	v_cmp_eq_u32_e32 vcc, 1, v6
	s_ff1_i32_b64 s99, vcc
	v_cmp_eq_u32_e32 vcc, 2, v6
	s_ff1_i32_b64 s100, vcc
	v_cmp_eq_u32_e32 vcc, 3, v6
	s_ff1_i32_b64 s101, vcc
	v_cmp_gt_u32_e32 vcc, 4, v6
	v_mov_b32_e32 v6, 0
	s_nop 0
	v_cndmask_b32_e32 v5, v245, v5, vcc
	v_ashrrev_i32_e32 v9, 31, v5
	v_sub_u32_e32 v8, 63, v230
	v_and_b32_e32 v9, 0x7fffffff, v9
	v_xor_b32_e32 v9, v5, v9
	s_nop 0
	v_readlane_b32 s23, v9, s98
	s_sub_i32 s22, 63, s98
	s_add_i32 s98, s98, 1
	v_readlane_b32 s21, v9, s98
	s_sub_i32 s20, 63, s98
	s_add_i32 s98, s98, 1
	v_cmp_gt_i64_e32 vcc, s[22:23], v[8:9]
	v_readlane_b32 s23, v9, s98
	s_sub_i32 s22, 63, s98
	s_add_i32 s98, s98, 1
	v_addc_co_u32_e32 v6, vcc, 0, v6, vcc
	v_cmp_gt_i64_e32 vcc, s[20:21], v[8:9]
	v_readlane_b32 s21, v9, s98
	s_sub_i32 s20, 63, s98
	s_add_i32 s98, s98, 1
	v_addc_co_u32_e32 v6, vcc, 0, v6, vcc
	v_cmp_gt_i64_e32 vcc, s[22:23], v[8:9]
	v_readlane_b32 s23, v9, s98
	s_sub_i32 s22, 63, s98
	s_add_i32 s98, s98, 1
	v_addc_co_u32_e32 v6, vcc, 0, v6, vcc
	v_cmp_gt_i64_e32 vcc, s[20:21], v[8:9]
	v_readlane_b32 s21, v9, s98
	s_sub_i32 s20, 63, s98
	s_add_i32 s98, s98, 1
	v_addc_co_u32_e32 v6, vcc, 0, v6, vcc
	v_cmp_gt_i64_e32 vcc, s[22:23], v[8:9]
	v_readlane_b32 s23, v9, s98
	s_sub_i32 s22, 63, s98
	s_add_i32 s98, s98, 1
	v_addc_co_u32_e32 v6, vcc, 0, v6, vcc
	v_cmp_gt_i64_e32 vcc, s[20:21], v[8:9]
	v_readlane_b32 s21, v9, s98
	s_sub_i32 s20, 63, s98
	s_nop 0
	v_addc_co_u32_e32 v6, vcc, 0, v6, vcc
	v_cmp_gt_i64_e32 vcc, s[22:23], v[8:9]
	v_readlane_b32 s23, v9, s99
	s_sub_i32 s22, 63, s99
	s_add_i32 s99, s99, 1
	v_addc_co_u32_e32 v6, vcc, 0, v6, vcc
	v_cmp_gt_i64_e32 vcc, s[20:21], v[8:9]
	v_readlane_b32 s21, v9, s99
	s_sub_i32 s20, 63, s99
	s_add_i32 s99, s99, 1
	v_addc_co_u32_e32 v6, vcc, 0, v6, vcc
	v_cmp_gt_i64_e32 vcc, s[22:23], v[8:9]
	v_readlane_b32 s23, v9, s99
	s_sub_i32 s22, 63, s99
	s_add_i32 s99, s99, 1
	v_addc_co_u32_e32 v6, vcc, 0, v6, vcc
	v_cmp_gt_i64_e32 vcc, s[20:21], v[8:9]
	v_readlane_b32 s21, v9, s99
	s_sub_i32 s20, 63, s99
	s_add_i32 s99, s99, 1
	v_addc_co_u32_e32 v6, vcc, 0, v6, vcc
; __device__ __forceinline__ void phase_nrr(const Frame& F, const Args& a, int l, const bf16_t* XA, const float* g, const float* modl, unsigned char* XN8) {
;     ...
;             int rank = 0;
; #pragma unroll 8
;             for (int e2 = 0; e2 < 64; ++e2) { const float v = __int_as_float(__builtin_amdgcn_readlane(__float_as_int(val), e2)); rank += (v > val || (v == val && e2 < lane)) ? 1 : 0; }
;             const bool sel = rank < TOPK;
;             const float ssum = wave_sum(sel ? sc : 0.f);
;             if (sel) { const int p = atomicAdd((int*)(hist + lane), 1); top_e[t * TOPK + rank] = lane; gate[t * TOPK + rank] = sc / ssum * 2.5f; lpos[t * TOPK + rank] = p; }
	v_cmp_gt_i64_e32 vcc, s[22:23], v[8:9]
	v_readlane_b32 s23, v9, s99
	s_sub_i32 s22, 63, s99
	s_add_i32 s99, s99, 1
	v_addc_co_u32_e32 v6, vcc, 0, v6, vcc
	v_cmp_gt_i64_e32 vcc, s[20:21], v[8:9]
	v_readlane_b32 s21, v9, s99
	s_sub_i32 s20, 63, s99
	s_add_i32 s99, s99, 1
	v_addc_co_u32_e32 v6, vcc, 0, v6, vcc
	v_cmp_gt_i64_e32 vcc, s[22:23], v[8:9]
	v_readlane_b32 s23, v9, s99
	s_sub_i32 s22, 63, s99
	s_add_i32 s99, s99, 1
	v_addc_co_u32_e32 v6, vcc, 0, v6, vcc
	v_cmp_gt_i64_e32 vcc, s[20:21], v[8:9]
	v_readlane_b32 s21, v9, s99
	s_sub_i32 s20, 63, s99
	s_nop 0
	v_addc_co_u32_e32 v6, vcc, 0, v6, vcc
	v_cmp_gt_i64_e32 vcc, s[22:23], v[8:9]
	v_readlane_b32 s23, v9, s100
	s_sub_i32 s22, 63, s100
	s_add_i32 s100, s100, 1
	v_addc_co_u32_e32 v6, vcc, 0, v6, vcc
	v_cmp_gt_i64_e32 vcc, s[20:21], v[8:9]
	v_readlane_b32 s21, v9, s100
	s_sub_i32 s20, 63, s100
	s_add_i32 s100, s100, 1
	v_addc_co_u32_e32 v6, vcc, 0, v6, vcc
	v_cmp_gt_i64_e32 vcc, s[22:23], v[8:9]
	v_readlane_b32 s23, v9, s100
	s_sub_i32 s22, 63, s100
	s_add_i32 s100, s100, 1
	v_addc_co_u32_e32 v6, vcc, 0, v6, vcc
	v_cmp_gt_i64_e32 vcc, s[20:21], v[8:9]
	v_readlane_b32 s21, v9, s100
	s_sub_i32 s20, 63, s100
	s_add_i32 s100, s100, 1
	v_addc_co_u32_e32 v6, vcc, 0, v6, vcc
	v_cmp_gt_i64_e32 vcc, s[22:23], v[8:9]
	v_readlane_b32 s23, v9, s100
	s_sub_i32 s22, 63, s100
	s_add_i32 s100, s100, 1
	v_addc_co_u32_e32 v6, vcc, 0, v6, vcc
	v_cmp_gt_i64_e32 vcc, s[20:21], v[8:9]
	v_readlane_b32 s21, v9, s100
	s_sub_i32 s20, 63, s100
	s_add_i32 s100, s100, 1
	v_addc_co_u32_e32 v6, vcc, 0, v6, vcc
	v_cmp_gt_i64_e32 vcc, s[22:23], v[8:9]
	v_readlane_b32 s23, v9, s100
	s_sub_i32 s22, 63, s100
	s_add_i32 s100, s100, 1
	v_addc_co_u32_e32 v6, vcc, 0, v6, vcc
	v_cmp_gt_i64_e32 vcc, s[20:21], v[8:9]
	v_readlane_b32 s21, v9, s100
	s_sub_i32 s20, 63, s100
	s_nop 0
	v_addc_co_u32_e32 v6, vcc, 0, v6, vcc
	v_cmp_gt_i64_e32 vcc, s[22:23], v[8:9]
	v_readlane_b32 s23, v9, s101
	s_sub_i32 s22, 63, s101
	s_add_i32 s101, s101, 1
	v_addc_co_u32_e32 v6, vcc, 0, v6, vcc
	v_cmp_gt_i64_e32 vcc, s[20:21], v[8:9]
	v_readlane_b32 s21, v9, s101
	s_sub_i32 s20, 63, s101
	s_add_i32 s101, s101, 1
	v_addc_co_u32_e32 v6, vcc, 0, v6, vcc
	v_cmp_gt_i64_e32 vcc, s[22:23], v[8:9]
	v_readlane_b32 s23, v9, s101
	s_sub_i32 s22, 63, s101
	s_add_i32 s101, s101, 1
	v_addc_co_u32_e32 v6, vcc, 0, v6, vcc
	v_cmp_gt_i64_e32 vcc, s[20:21], v[8:9]
	v_readlane_b32 s21, v9, s101
	s_sub_i32 s20, 63, s101
	s_add_i32 s101, s101, 1
	v_addc_co_u32_e32 v6, vcc, 0, v6, vcc
	v_cmp_gt_i64_e32 vcc, s[22:23], v[8:9]
	v_readlane_b32 s23, v9, s101
	s_sub_i32 s22, 63, s101
	s_add_i32 s101, s101, 1
	v_addc_co_u32_e32 v6, vcc, 0, v6, vcc
	v_cmp_gt_i64_e32 vcc, s[20:21], v[8:9]
	v_readlane_b32 s21, v9, s101
	s_sub_i32 s20, 63, s101
	s_add_i32 s101, s101, 1
	v_addc_co_u32_e32 v6, vcc, 0, v6, vcc
	v_cmp_gt_i64_e32 vcc, s[22:23], v[8:9]
	v_readlane_b32 s23, v9, s101
	s_sub_i32 s22, 63, s101
	s_add_i32 s101, s101, 1
	v_addc_co_u32_e32 v6, vcc, 0, v6, vcc
	v_cmp_gt_i64_e32 vcc, s[20:21], v[8:9]
	v_readlane_b32 s21, v9, s101
	s_sub_i32 s20, 63, s101
	s_nop 0
	v_addc_co_u32_e32 v6, vcc, 0, v6, vcc
	v_cmp_gt_i64_e32 vcc, s[22:23], v[8:9]
	s_nop 1
	v_addc_co_u32_e32 v6, vcc, 0, v6, vcc
	v_cmp_gt_i64_e32 vcc, s[20:21], v[8:9]
	s_nop 1
	v_addc_co_u32_e32 v6, vcc, 0, v6, vcc
	v_cmp_gt_u32_e32 vcc, 6, v6
	s_mul_i32 s50, s24, 6
	s_nop 0
	v_cndmask_b32_e32 v5, 0, v2, vcc
	s_nop 1
	v_add_f32_dpp v5, v5, v5 quad_perm:[1,0,3,2] row_mask:0xf bank_mask:0xf
	s_nop 1
	v_add_f32_dpp v5, v5, v5 quad_perm:[2,3,0,1] row_mask:0xf bank_mask:0xf
	s_nop 1
	v_add_f32_dpp v5, v5, v5 row_half_mirror row_mask:0xf bank_mask:0xf
	s_nop 1
	v_add_f32_dpp v5, v5, v5 row_mirror row_mask:0xf bank_mask:0xf
	s_nop 0
	ds_bpermute_b32 v7, v222, v5
	s_waitcnt lgkmcnt(0)
	v_add_f32_e32 v5, v5, v7
	v_mov_b32_e32 v7, v5
	s_nop 1
	v_permlane32_swap_b32_e32 v7, v5
	s_and_saveexec_b64 s[20:21], vcc
	s_cbranch_execz .LBB0_1312
	s_waitcnt lgkmcnt(0)
	v_add_f32_e32 v5, v5, v7
	v_div_scale_f32 v11, s[22:23], v5, v5, v2
	v_or_b32_e32 v6, s50, v6
	v_rcp_f32_e32 v12, v11
	v_ashrrev_i32_e32 v7, 31, v6
	v_lshlrev_b64 v[6:7], 2, v[6:7]
	v_lshl_add_u64 v[8:9], s[42:43], 0, v[6:7]
	ds_add_rtn_u32 v10, v227, v243
	global_store_dword v[8:9], v230, off
	v_fma_f32 v8, -v11, v12, 1.0
	v_fmac_f32_e32 v12, v8, v12
	v_div_scale_f32 v8, vcc, v2, v5, v2
	v_mul_f32_e32 v9, v8, v12
	v_fma_f32 v13, -v11, v9, v8
	v_fmac_f32_e32 v9, v13, v12
	v_fma_f32 v8, -v11, v9, v8
	v_div_fmas_f32 v8, v8, v12, v9
	v_div_fixup_f32 v2, v8, v5, v2
	v_mul_f32_e32 v2, 0x40200000, v2
	v_lshl_add_u64 v[8:9], s[44:45], 0, v[6:7]
	v_lshl_add_u64 v[6:7], s[46:47], 0, v[6:7]
	global_store_dword v[8:9], v2, off
	s_waitcnt lgkmcnt(0)
	global_store_dword v[6:7], v10, off
; __device__ __forceinline__ void phase_nrr(const Frame& F, const Args& a, int l, const bf16_t* XA, const float* g, const float* modl, unsigned char* XN8) {
;     ...
;         for (int i = 0; i < 8; ++i) { const int t = tb + i;
;             const float lg = Pl[(w * 8 + i) * NE + lane] + Pl[(64 + w * 8 + i) * NE + lane]; const float sc = 1.f / (1.f + __expf(-lg)); const float bb = sc + bias;
;             float m1 = bb; m1 = fmaxf(m1, __shfl_xor(m1, 1)); m1 = fmaxf(m1, __shfl_xor(m1, 2)); m1 = fmaxf(m1, __shfl_xor(m1, 4));
;             const unsigned long long eq = __ballot(bb == m1); const int gbase = lane & ~7; const unsigned grpmask = (unsigned)((eq >> gbase) & 0xffull);
;             const int first = gbase + __builtin_ctz(grpmask);
;             float m2 = (lane == first) ? -INFINITY : bb; m2 = fmaxf(m2, __shfl_xor(m2, 1)); m2 = fmaxf(m2, __shfl_xor(m2, 2)); m2 = fmaxf(m2, __shfl_xor(m2, 4));
;             const float gsum = m1 + m2; const int gq = lane >> 3;
;             int grank = 0;
; #pragma unroll
;             for (int g2 = 0; g2 < 8; ++g2) { const float v = __int_as_float(__builtin_amdgcn_readlane(__float_as_int(gsum), g2 * 8)); grank += (v > gsum || (v == gsum && g2 < gq)) ? 1 : 0; }
;             const bool keep = grank < 4; const float val = keep ? bb : -INFINITY;
;             int rank = 0;
; #pragma unroll 8
;             for (int e2 = 0; e2 < 64; ++e2) { const float v = __int_as_float(__builtin_amdgcn_readlane(__float_as_int(val), e2)); rank += (v > val || (v == val && e2 < lane)) ? 1 : 0; }
.LBB0_1312:
	s_or_b64 exec, exec, s[20:21]
	v_add_u32_e32 v2, s76, v226
	ds_read_b32 v2, v2
	ds_read_b32 v5, v4 offset:16640
	s_mov_b32 s3, 0
	s_waitcnt lgkmcnt(0)
	v_add_f32_e32 v2, v2, v5
	v_mul_f32_e32 v2, 0xbfb8aa3b, v2
	v_exp_f32_e32 v2, v2
	s_nop 0
	v_add_f32_e32 v2, 1.0, v2
	v_div_scale_f32 v5, s[20:21], v2, v2, 1.0
	v_rcp_f32_e32 v6, v5
	v_div_scale_f32 v7, vcc, 1.0, v2, 1.0
	v_fma_f32 v8, -v5, v6, 1.0
	v_fmac_f32_e32 v6, v8, v6
	v_mul_f32_e32 v8, v7, v6
	v_fma_f32 v9, -v5, v8, v7
	v_fmac_f32_e32 v8, v9, v6
	v_fma_f32 v5, -v5, v8, v7
	v_div_fmas_f32 v5, v5, v6, v8
	v_div_fixup_f32 v5, v5, v2, 1.0
	v_add_f32_e32 v2, v3, v5
	s_nop 1
	s_waitcnt lgkmcnt(0)
	v_max_f32_dpp v6, v2, v2 quad_perm:[1,0,3,2] row_mask:0xf bank_mask:0xf
	s_nop 1
	s_waitcnt lgkmcnt(0)
	v_max_f32_dpp v6, v6, v6 quad_perm:[2,3,0,1] row_mask:0xf bank_mask:0xf
	s_nop 1
	s_waitcnt lgkmcnt(0)
	v_max_f32_dpp v8, v6, v6 row_half_mirror row_mask:0xf bank_mask:0xf
	v_cmp_eq_f32_e32 vcc, v2, v8
	s_nop 1
	v_lshrrev_b64 v[6:7], v200, vcc
	v_ffbl_b32_sdwa v6, v6 dst_sel:DWORD dst_unused:UNUSED_PAD src0_sel:BYTE_0
	v_add_u32_e32 v6, v6, v200
	v_cmp_ne_u32_e32 vcc, v230, v6
	s_nop 1
	v_cndmask_b32_e32 v6, v245, v2, vcc
	s_nop 1
	s_waitcnt lgkmcnt(0)
	v_max_f32_dpp v6, v6, v6 quad_perm:[1,0,3,2] row_mask:0xf bank_mask:0xf
	s_nop 1
	s_waitcnt lgkmcnt(0)
	v_max_f32_dpp v6, v6, v6 quad_perm:[2,3,0,1] row_mask:0xf bank_mask:0xf
	s_nop 1
	s_waitcnt lgkmcnt(0)
	v_max_f32_dpp v6, v6, v6 row_half_mirror row_mask:0xf bank_mask:0xf
	v_add_f32_e32 v6, v8, v6
	s_nop 0
	v_readlane_b32 s5, v6, 0
	v_readlane_b32 s24, v6, 8
	v_readlane_b32 s28, v6, 16
	v_cmp_eq_f32_e64 s[20:21], s5, v6
	v_cmp_gt_f32_e32 vcc, s5, v6
	v_cmp_gt_f32_e64 s[22:23], s24, v6
	v_cmp_eq_f32_e64 s[24:25], s24, v6
	s_and_b64 s[20:21], s[0:1], s[20:21]
	v_readlane_b32 s34, v6, 24
	v_cmp_gt_f32_e64 s[26:27], s28, v6
	v_cmp_eq_f32_e64 s[28:29], s28, v6
	s_and_b64 s[24:25], s[6:7], s[24:25]
	s_or_b64 s[20:21], vcc, s[20:21]
	v_readlane_b32 s40, v6, 32
	v_cmp_gt_f32_e64 s[30:31], s34, v6
	v_cmp_eq_f32_e64 s[34:35], s34, v6
	s_and_b64 s[28:29], s[8:9], s[28:29]
	v_cndmask_b32_e64 v7, 0, 1, s[20:21]
	s_or_b64 s[20:21], s[22:23], s[24:25]
	v_cmp_gt_f32_e64 s[36:37], s40, v6
	v_cmp_eq_f32_e64 s[40:41], s40, v6
	s_and_b64 s[34:35], s[10:11], s[34:35]
	v_cndmask_b32_e64 v8, 0, 1, s[20:21]
	s_or_b64 s[20:21], s[26:27], s[28:29]
	s_and_b64 s[40:41], s[12:13], s[40:41]
	v_cndmask_b32_e64 v9, 0, 1, s[20:21]
	s_or_b64 s[20:21], s[30:31], s[34:35]
	v_readlane_b32 s55, v6, 40
	v_cndmask_b32_e64 v10, 0, 1, s[20:21]
	s_or_b64 s[20:21], s[36:37], s[40:41]
	v_cndmask_b32_e64 v11, 0, 1, s[20:21]
	v_cmp_eq_f32_e64 s[20:21], s55, v6
	v_cmp_gt_f32_e32 vcc, s55, v6
	s_and_b64 s[20:21], s[14:15], s[20:21]
	s_or_b64 s[20:21], vcc, s[20:21]
	v_readlane_b32 s5, v6, 48
	v_cndmask_b32_e64 v12, 0, 1, s[20:21]
	s_nop 0
	v_cmp_eq_f32_e64 s[20:21], s5, v6
	v_cmp_gt_f32_e32 vcc, s5, v6
	s_and_b64 s[20:21], s[16:17], s[20:21]
	v_readlane_b32 s5, v6, 56
	s_or_b64 s[20:21], vcc, s[20:21]
	v_cndmask_b32_e64 v13, 0, 1, s[20:21]
	v_cmp_gt_f32_e32 vcc, s5, v6
	s_nop 1
	v_cndmask_b32_e64 v6, 0, 1, vcc
	v_add_u32_e32 v6, v8, v6
	v_add3_u32 v6, v6, v7, v9
	v_add3_u32 v6, v6, v10, v11
	v_add3_u32 v6, v6, v12, v13
	v_cmp_eq_u32_e32 vcc, 0, v6
	s_ff1_i32_b64 s98, vcc
	v_cmp_eq_u32_e32 vcc, 1, v6
	s_ff1_i32_b64 s99, vcc
	v_cmp_eq_u32_e32 vcc, 2, v6
	s_ff1_i32_b64 s100, vcc
	v_cmp_eq_u32_e32 vcc, 3, v6
	s_ff1_i32_b64 s101, vcc
	v_cmp_gt_u32_e32 vcc, 4, v6
	s_nop 1
	v_cndmask_b32_e32 v6, v245, v2, vcc
	v_mov_b32_e32 v2, 0
	v_ashrrev_i32_e32 v9, 31, v6
	v_sub_u32_e32 v8, 63, v230
	v_and_b32_e32 v9, 0x7fffffff, v9
	v_xor_b32_e32 v9, v6, v9
	s_nop 0
	v_readlane_b32 s23, v9, s98
	s_sub_i32 s22, 63, s98
	s_add_i32 s98, s98, 1
	v_readlane_b32 s21, v9, s98
	s_sub_i32 s20, 63, s98
	s_add_i32 s98, s98, 1
	v_cmp_gt_i64_e32 vcc, s[22:23], v[8:9]
	v_readlane_b32 s23, v9, s98
	s_sub_i32 s22, 63, s98
	s_add_i32 s98, s98, 1
	v_addc_co_u32_e32 v2, vcc, 0, v2, vcc
	v_cmp_gt_i64_e32 vcc, s[20:21], v[8:9]
	v_readlane_b32 s21, v9, s98
	s_sub_i32 s20, 63, s98
	s_add_i32 s98, s98, 1
	v_addc_co_u32_e32 v2, vcc, 0, v2, vcc
	v_cmp_gt_i64_e32 vcc, s[22:23], v[8:9]
	v_readlane_b32 s23, v9, s98
	s_sub_i32 s22, 63, s98
	s_add_i32 s98, s98, 1
	v_addc_co_u32_e32 v2, vcc, 0, v2, vcc
	v_cmp_gt_i64_e32 vcc, s[20:21], v[8:9]
	v_readlane_b32 s21, v9, s98
	s_sub_i32 s20, 63, s98
	s_add_i32 s98, s98, 1
	v_addc_co_u32_e32 v2, vcc, 0, v2, vcc
	v_cmp_gt_i64_e32 vcc, s[22:23], v[8:9]
	v_readlane_b32 s23, v9, s98
	s_sub_i32 s22, 63, s98
	s_add_i32 s98, s98, 1
	v_addc_co_u32_e32 v2, vcc, 0, v2, vcc
	v_cmp_gt_i64_e32 vcc, s[20:21], v[8:9]
	v_readlane_b32 s21, v9, s98
	s_sub_i32 s20, 63, s98
	s_nop 0
	v_addc_co_u32_e32 v2, vcc, 0, v2, vcc
	v_cmp_gt_i64_e32 vcc, s[22:23], v[8:9]
	v_readlane_b32 s23, v9, s99
	s_sub_i32 s22, 63, s99
	s_add_i32 s99, s99, 1
	v_addc_co_u32_e32 v2, vcc, 0, v2, vcc
	v_cmp_gt_i64_e32 vcc, s[20:21], v[8:9]
	v_readlane_b32 s21, v9, s99
	s_sub_i32 s20, 63, s99
	s_add_i32 s99, s99, 1
	v_addc_co_u32_e32 v2, vcc, 0, v2, vcc
	v_cmp_gt_i64_e32 vcc, s[22:23], v[8:9]
	v_readlane_b32 s23, v9, s99
	s_sub_i32 s22, 63, s99
	s_add_i32 s99, s99, 1
	v_addc_co_u32_e32 v2, vcc, 0, v2, vcc
	v_cmp_gt_i64_e32 vcc, s[20:21], v[8:9]
	v_readlane_b32 s21, v9, s99
	s_sub_i32 s20, 63, s99
	s_add_i32 s99, s99, 1
	v_addc_co_u32_e32 v2, vcc, 0, v2, vcc
	v_cmp_gt_i64_e32 vcc, s[22:23], v[8:9]
	v_readlane_b32 s23, v9, s99
	s_sub_i32 s22, 63, s99
	s_add_i32 s99, s99, 1
	v_addc_co_u32_e32 v2, vcc, 0, v2, vcc
	v_cmp_gt_i64_e32 vcc, s[20:21], v[8:9]
	v_readlane_b32 s21, v9, s99
	s_sub_i32 s20, 63, s99
	s_add_i32 s99, s99, 1
; __device__ __forceinline__ void phase_nrr(const Frame& F, const Args& a, int l, const bf16_t* XA, const float* g, const float* modl, unsigned char* XN8) {
;     ...
;             int rank = 0;
; #pragma unroll 8
;             for (int e2 = 0; e2 < 64; ++e2) { const float v = __int_as_float(__builtin_amdgcn_readlane(__float_as_int(val), e2)); rank += (v > val || (v == val && e2 < lane)) ? 1 : 0; }
;             const bool sel = rank < TOPK;
;             const float ssum = wave_sum(sel ? sc : 0.f);
;             if (sel) { const int p = atomicAdd((int*)(hist + lane), 1); top_e[t * TOPK + rank] = lane; gate[t * TOPK + rank] = sc / ssum * 2.5f; lpos[t * TOPK + rank] = p; }
	v_addc_co_u32_e32 v2, vcc, 0, v2, vcc
	v_cmp_gt_i64_e32 vcc, s[22:23], v[8:9]
	v_readlane_b32 s23, v9, s99
	s_sub_i32 s22, 63, s99
	s_add_i32 s99, s99, 1
	v_addc_co_u32_e32 v2, vcc, 0, v2, vcc
	v_cmp_gt_i64_e32 vcc, s[20:21], v[8:9]
	v_readlane_b32 s21, v9, s99
	s_sub_i32 s20, 63, s99
	s_nop 0
	v_addc_co_u32_e32 v2, vcc, 0, v2, vcc
	v_cmp_gt_i64_e32 vcc, s[22:23], v[8:9]
	v_readlane_b32 s23, v9, s100
	s_sub_i32 s22, 63, s100
	s_add_i32 s100, s100, 1
	v_addc_co_u32_e32 v2, vcc, 0, v2, vcc
	v_cmp_gt_i64_e32 vcc, s[20:21], v[8:9]
	v_readlane_b32 s21, v9, s100
	s_sub_i32 s20, 63, s100
	s_add_i32 s100, s100, 1
	v_addc_co_u32_e32 v2, vcc, 0, v2, vcc
	v_cmp_gt_i64_e32 vcc, s[22:23], v[8:9]
	v_readlane_b32 s23, v9, s100
	s_sub_i32 s22, 63, s100
	s_add_i32 s100, s100, 1
	v_addc_co_u32_e32 v2, vcc, 0, v2, vcc
	v_cmp_gt_i64_e32 vcc, s[20:21], v[8:9]
	v_readlane_b32 s21, v9, s100
	s_sub_i32 s20, 63, s100
	s_add_i32 s100, s100, 1
	v_addc_co_u32_e32 v2, vcc, 0, v2, vcc
	v_cmp_gt_i64_e32 vcc, s[22:23], v[8:9]
	v_readlane_b32 s23, v9, s100
	s_sub_i32 s22, 63, s100
	s_add_i32 s100, s100, 1
	v_addc_co_u32_e32 v2, vcc, 0, v2, vcc
	v_cmp_gt_i64_e32 vcc, s[20:21], v[8:9]
	v_readlane_b32 s21, v9, s100
	s_sub_i32 s20, 63, s100
	s_add_i32 s100, s100, 1
	v_addc_co_u32_e32 v2, vcc, 0, v2, vcc
	v_cmp_gt_i64_e32 vcc, s[22:23], v[8:9]
	v_readlane_b32 s23, v9, s100
	s_sub_i32 s22, 63, s100
	s_add_i32 s100, s100, 1
	v_addc_co_u32_e32 v2, vcc, 0, v2, vcc
	v_cmp_gt_i64_e32 vcc, s[20:21], v[8:9]
	v_readlane_b32 s21, v9, s100
	s_sub_i32 s20, 63, s100
	s_nop 0
	v_addc_co_u32_e32 v2, vcc, 0, v2, vcc
	v_cmp_gt_i64_e32 vcc, s[22:23], v[8:9]
	v_readlane_b32 s23, v9, s101
	s_sub_i32 s22, 63, s101
	s_add_i32 s101, s101, 1
	v_addc_co_u32_e32 v2, vcc, 0, v2, vcc
	v_cmp_gt_i64_e32 vcc, s[20:21], v[8:9]
	v_readlane_b32 s21, v9, s101
	s_sub_i32 s20, 63, s101
	s_add_i32 s101, s101, 1
	v_addc_co_u32_e32 v2, vcc, 0, v2, vcc
	v_cmp_gt_i64_e32 vcc, s[22:23], v[8:9]
	v_readlane_b32 s23, v9, s101
	s_sub_i32 s22, 63, s101
	s_add_i32 s101, s101, 1
	v_addc_co_u32_e32 v2, vcc, 0, v2, vcc
	v_cmp_gt_i64_e32 vcc, s[20:21], v[8:9]
	v_readlane_b32 s21, v9, s101
	s_sub_i32 s20, 63, s101
	s_add_i32 s101, s101, 1
	v_addc_co_u32_e32 v2, vcc, 0, v2, vcc
	v_cmp_gt_i64_e32 vcc, s[22:23], v[8:9]
	v_readlane_b32 s23, v9, s101
	s_sub_i32 s22, 63, s101
	s_add_i32 s101, s101, 1
	v_addc_co_u32_e32 v2, vcc, 0, v2, vcc
	v_cmp_gt_i64_e32 vcc, s[20:21], v[8:9]
	v_readlane_b32 s21, v9, s101
	s_sub_i32 s20, 63, s101
	s_add_i32 s101, s101, 1
	v_addc_co_u32_e32 v2, vcc, 0, v2, vcc
	v_cmp_gt_i64_e32 vcc, s[22:23], v[8:9]
	v_readlane_b32 s23, v9, s101
	s_sub_i32 s22, 63, s101
	s_add_i32 s101, s101, 1
	v_addc_co_u32_e32 v2, vcc, 0, v2, vcc
	v_cmp_gt_i64_e32 vcc, s[20:21], v[8:9]
	v_readlane_b32 s21, v9, s101
	s_sub_i32 s20, 63, s101
	s_nop 0
	v_addc_co_u32_e32 v2, vcc, 0, v2, vcc
	v_cmp_gt_i64_e32 vcc, s[22:23], v[8:9]
	s_nop 1
	v_addc_co_u32_e32 v2, vcc, 0, v2, vcc
	v_cmp_gt_i64_e32 vcc, s[20:21], v[8:9]
	s_nop 1
	v_addc_co_u32_e32 v2, vcc, 0, v2, vcc
	v_cmp_gt_u32_e32 vcc, 6, v2
	s_nop 1
	v_cndmask_b32_e32 v6, 0, v5, vcc
	s_nop 1
	v_add_f32_dpp v6, v6, v6 quad_perm:[1,0,3,2] row_mask:0xf bank_mask:0xf
	s_nop 1
	v_add_f32_dpp v6, v6, v6 quad_perm:[2,3,0,1] row_mask:0xf bank_mask:0xf
	s_nop 1
	v_add_f32_dpp v6, v6, v6 row_half_mirror row_mask:0xf bank_mask:0xf
	s_nop 1
	v_add_f32_dpp v6, v6, v6 row_mirror row_mask:0xf bank_mask:0xf
	s_nop 0
	ds_bpermute_b32 v7, v222, v6
	s_waitcnt lgkmcnt(0)
	v_add_f32_e32 v6, v6, v7
	v_mov_b32_e32 v7, v6
	s_nop 1
	v_permlane32_swap_b32_e32 v7, v6
	s_and_saveexec_b64 s[20:21], vcc
	s_cbranch_execz .LBB0_1316
	s_waitcnt lgkmcnt(0)
	v_add_f32_e32 v10, v6, v7
	v_mad_u64_u32 v[6:7], s[22:23], s56, 6, v[2:3]
	v_div_scale_f32 v2, s[22:23], v10, v10, v5
	v_rcp_f32_e32 v12, v2
	v_ashrrev_i32_e32 v7, 31, v6
	v_lshlrev_b64 v[6:7], 2, v[6:7]
	v_lshl_add_u64 v[8:9], s[42:43], 0, v[6:7]
	ds_add_rtn_u32 v11, v227, v243
	global_store_dword v[8:9], v230, off
	v_fma_f32 v8, -v2, v12, 1.0
	v_fmac_f32_e32 v12, v8, v12
	v_div_scale_f32 v8, vcc, v5, v10, v5
	v_mul_f32_e32 v9, v8, v12
	v_fma_f32 v13, -v2, v9, v8
	v_fmac_f32_e32 v9, v13, v12
	v_fma_f32 v2, -v2, v9, v8
	v_div_fmas_f32 v2, v2, v12, v9
	v_div_fixup_f32 v2, v2, v10, v5
	v_mul_f32_e32 v2, 0x40200000, v2
	v_lshl_add_u64 v[8:9], s[44:45], 0, v[6:7]
	v_lshl_add_u64 v[6:7], s[46:47], 0, v[6:7]
	global_store_dword v[8:9], v2, off
	s_waitcnt lgkmcnt(0)
	global_store_dword v[6:7], v11, off
; __device__ __forceinline__ void phase_nrr(const Frame& F, const Args& a, int l, const bf16_t* XA, const float* g, const float* modl, unsigned char* XN8) {
;     ...
;         for (int i = 0; i < 8; ++i) { const int t = tb + i;
;             const float lg = Pl[(w * 8 + i) * NE + lane] + Pl[(64 + w * 8 + i) * NE + lane]; const float sc = 1.f / (1.f + __expf(-lg)); const float bb = sc + bias;
;             float m1 = bb; m1 = fmaxf(m1, __shfl_xor(m1, 1)); m1 = fmaxf(m1, __shfl_xor(m1, 2)); m1 = fmaxf(m1, __shfl_xor(m1, 4));
;             const unsigned long long eq = __ballot(bb == m1); const int gbase = lane & ~7; const unsigned grpmask = (unsigned)((eq >> gbase) & 0xffull);
;             const int first = gbase + __builtin_ctz(grpmask);
;             float m2 = (lane == first) ? -INFINITY : bb; m2 = fmaxf(m2, __shfl_xor(m2, 1)); m2 = fmaxf(m2, __shfl_xor(m2, 2)); m2 = fmaxf(m2, __shfl_xor(m2, 4));
;             const float gsum = m1 + m2; const int gq = lane >> 3;
;             int grank = 0;
; #pragma unroll
;             for (int g2 = 0; g2 < 8; ++g2) { const float v = __int_as_float(__builtin_amdgcn_readlane(__float_as_int(gsum), g2 * 8)); grank += (v > gsum || (v == gsum && g2 < gq)) ? 1 : 0; }
;             const bool keep = grank < 4; const float val = keep ? bb : -INFINITY;
;             int rank = 0;
; #pragma unroll 8
;             for (int e2 = 0; e2 < 64; ++e2) { const float v = __int_as_float(__builtin_amdgcn_readlane(__float_as_int(val), e2)); rank += (v > val || (v == val && e2 < lane)) ? 1 : 0; }
.LBB0_1316:
	s_or_b64 exec, exec, s[20:21]
	v_add_u32_e32 v2, s77, v226
	ds_read_b32 v2, v2
	ds_read_b32 v5, v4 offset:16896
	s_mov_b32 s3, 0
	s_waitcnt lgkmcnt(0)
	v_add_f32_e32 v2, v2, v5
	v_mul_f32_e32 v2, 0xbfb8aa3b, v2
	v_exp_f32_e32 v2, v2
	s_nop 0
	v_add_f32_e32 v2, 1.0, v2
	v_div_scale_f32 v5, s[20:21], v2, v2, 1.0
	v_rcp_f32_e32 v6, v5
	v_div_scale_f32 v7, vcc, 1.0, v2, 1.0
	v_fma_f32 v8, -v5, v6, 1.0
	v_fmac_f32_e32 v6, v8, v6
	v_mul_f32_e32 v8, v7, v6
	v_fma_f32 v9, -v5, v8, v7
	v_fmac_f32_e32 v8, v9, v6
	v_fma_f32 v5, -v5, v8, v7
	v_div_fmas_f32 v5, v5, v6, v8
	v_div_fixup_f32 v5, v5, v2, 1.0
	v_add_f32_e32 v2, v3, v5
	s_nop 1
	s_waitcnt lgkmcnt(0)
	v_max_f32_dpp v6, v2, v2 quad_perm:[1,0,3,2] row_mask:0xf bank_mask:0xf
	s_nop 1
	s_waitcnt lgkmcnt(0)
	v_max_f32_dpp v6, v6, v6 quad_perm:[2,3,0,1] row_mask:0xf bank_mask:0xf
	s_nop 1
	s_waitcnt lgkmcnt(0)
	v_max_f32_dpp v8, v6, v6 row_half_mirror row_mask:0xf bank_mask:0xf
	v_cmp_eq_f32_e32 vcc, v2, v8
	s_nop 1
	v_lshrrev_b64 v[6:7], v200, vcc
	v_ffbl_b32_sdwa v6, v6 dst_sel:DWORD dst_unused:UNUSED_PAD src0_sel:BYTE_0
	v_add_u32_e32 v6, v6, v200
	v_cmp_ne_u32_e32 vcc, v230, v6
	s_nop 1
	v_cndmask_b32_e32 v6, v245, v2, vcc
	s_nop 1
	s_waitcnt lgkmcnt(0)
	v_max_f32_dpp v6, v6, v6 quad_perm:[1,0,3,2] row_mask:0xf bank_mask:0xf
	s_nop 1
	s_waitcnt lgkmcnt(0)
	v_max_f32_dpp v6, v6, v6 quad_perm:[2,3,0,1] row_mask:0xf bank_mask:0xf
	s_nop 1
	s_waitcnt lgkmcnt(0)
	v_max_f32_dpp v6, v6, v6 row_half_mirror row_mask:0xf bank_mask:0xf
	v_add_f32_e32 v6, v8, v6
	s_nop 0
	v_readlane_b32 s5, v6, 0
	v_readlane_b32 s24, v6, 8
	v_readlane_b32 s28, v6, 16
	v_cmp_eq_f32_e64 s[20:21], s5, v6
	v_cmp_gt_f32_e32 vcc, s5, v6
	v_cmp_gt_f32_e64 s[22:23], s24, v6
	v_cmp_eq_f32_e64 s[24:25], s24, v6
	s_and_b64 s[20:21], s[0:1], s[20:21]
	v_readlane_b32 s34, v6, 24
	v_cmp_gt_f32_e64 s[26:27], s28, v6
	v_cmp_eq_f32_e64 s[28:29], s28, v6
	s_and_b64 s[24:25], s[6:7], s[24:25]
	s_or_b64 s[20:21], vcc, s[20:21]
	v_readlane_b32 s40, v6, 32
	v_cmp_gt_f32_e64 s[30:31], s34, v6
	v_cmp_eq_f32_e64 s[34:35], s34, v6
	s_and_b64 s[28:29], s[8:9], s[28:29]
	v_cndmask_b32_e64 v7, 0, 1, s[20:21]
	s_or_b64 s[20:21], s[22:23], s[24:25]
	v_cmp_gt_f32_e64 s[36:37], s40, v6
	v_cmp_eq_f32_e64 s[40:41], s40, v6
	s_and_b64 s[34:35], s[10:11], s[34:35]
	v_cndmask_b32_e64 v8, 0, 1, s[20:21]
	s_or_b64 s[20:21], s[26:27], s[28:29]
	s_and_b64 s[40:41], s[12:13], s[40:41]
	v_cndmask_b32_e64 v9, 0, 1, s[20:21]
	s_or_b64 s[20:21], s[30:31], s[34:35]
	v_readlane_b32 s55, v6, 40
	v_cndmask_b32_e64 v10, 0, 1, s[20:21]
	s_or_b64 s[20:21], s[36:37], s[40:41]
	v_cndmask_b32_e64 v11, 0, 1, s[20:21]
	v_cmp_eq_f32_e64 s[20:21], s55, v6
	v_cmp_gt_f32_e32 vcc, s55, v6
	s_and_b64 s[20:21], s[14:15], s[20:21]
	s_or_b64 s[20:21], vcc, s[20:21]
	v_readlane_b32 s5, v6, 48
	v_cndmask_b32_e64 v12, 0, 1, s[20:21]
	s_nop 0
	v_cmp_eq_f32_e64 s[20:21], s5, v6
	v_cmp_gt_f32_e32 vcc, s5, v6
	s_and_b64 s[20:21], s[16:17], s[20:21]
	v_readlane_b32 s5, v6, 56
	s_or_b64 s[20:21], vcc, s[20:21]
	v_cndmask_b32_e64 v13, 0, 1, s[20:21]
	v_cmp_gt_f32_e32 vcc, s5, v6
	s_nop 1
	v_cndmask_b32_e64 v6, 0, 1, vcc
	v_add_u32_e32 v6, v8, v6
	v_add3_u32 v6, v6, v7, v9
	v_add3_u32 v6, v6, v10, v11
	v_add3_u32 v6, v6, v12, v13
	v_cmp_eq_u32_e32 vcc, 0, v6
	s_ff1_i32_b64 s98, vcc
	v_cmp_eq_u32_e32 vcc, 1, v6
	s_ff1_i32_b64 s99, vcc
	v_cmp_eq_u32_e32 vcc, 2, v6
	s_ff1_i32_b64 s100, vcc
	v_cmp_eq_u32_e32 vcc, 3, v6
	s_ff1_i32_b64 s101, vcc
	v_cmp_gt_u32_e32 vcc, 4, v6
	s_nop 1
	v_cndmask_b32_e32 v6, v245, v2, vcc
	v_mov_b32_e32 v2, 0
	v_ashrrev_i32_e32 v9, 31, v6
	v_sub_u32_e32 v8, 63, v230
	v_and_b32_e32 v9, 0x7fffffff, v9
	v_xor_b32_e32 v9, v6, v9
	s_nop 0
	v_readlane_b32 s23, v9, s98
	s_sub_i32 s22, 63, s98
	s_add_i32 s98, s98, 1
	v_readlane_b32 s21, v9, s98
	s_sub_i32 s20, 63, s98
	s_add_i32 s98, s98, 1
	v_cmp_gt_i64_e32 vcc, s[22:23], v[8:9]
	v_readlane_b32 s23, v9, s98
	s_sub_i32 s22, 63, s98
	s_add_i32 s98, s98, 1
	v_addc_co_u32_e32 v2, vcc, 0, v2, vcc
	v_cmp_gt_i64_e32 vcc, s[20:21], v[8:9]
	v_readlane_b32 s21, v9, s98
	s_sub_i32 s20, 63, s98
	s_add_i32 s98, s98, 1
	v_addc_co_u32_e32 v2, vcc, 0, v2, vcc
	v_cmp_gt_i64_e32 vcc, s[22:23], v[8:9]
	v_readlane_b32 s23, v9, s98
	s_sub_i32 s22, 63, s98
	s_add_i32 s98, s98, 1
	v_addc_co_u32_e32 v2, vcc, 0, v2, vcc
	v_cmp_gt_i64_e32 vcc, s[20:21], v[8:9]
	v_readlane_b32 s21, v9, s98
	s_sub_i32 s20, 63, s98
	s_add_i32 s98, s98, 1
	v_addc_co_u32_e32 v2, vcc, 0, v2, vcc
	v_cmp_gt_i64_e32 vcc, s[22:23], v[8:9]
	v_readlane_b32 s23, v9, s98
	s_sub_i32 s22, 63, s98
	s_add_i32 s98, s98, 1
	v_addc_co_u32_e32 v2, vcc, 0, v2, vcc
	v_cmp_gt_i64_e32 vcc, s[20:21], v[8:9]
	v_readlane_b32 s21, v9, s98
	s_sub_i32 s20, 63, s98
	s_nop 0
	v_addc_co_u32_e32 v2, vcc, 0, v2, vcc
	v_cmp_gt_i64_e32 vcc, s[22:23], v[8:9]
	v_readlane_b32 s23, v9, s99
	s_sub_i32 s22, 63, s99
	s_add_i32 s99, s99, 1
	v_addc_co_u32_e32 v2, vcc, 0, v2, vcc
	v_cmp_gt_i64_e32 vcc, s[20:21], v[8:9]
	v_readlane_b32 s21, v9, s99
	s_sub_i32 s20, 63, s99
	s_add_i32 s99, s99, 1
	v_addc_co_u32_e32 v2, vcc, 0, v2, vcc
	v_cmp_gt_i64_e32 vcc, s[22:23], v[8:9]
	v_readlane_b32 s23, v9, s99
	s_sub_i32 s22, 63, s99
	s_add_i32 s99, s99, 1
	v_addc_co_u32_e32 v2, vcc, 0, v2, vcc
	v_cmp_gt_i64_e32 vcc, s[20:21], v[8:9]
	v_readlane_b32 s21, v9, s99
	s_sub_i32 s20, 63, s99
	s_add_i32 s99, s99, 1
	v_addc_co_u32_e32 v2, vcc, 0, v2, vcc
	v_cmp_gt_i64_e32 vcc, s[22:23], v[8:9]
	v_readlane_b32 s23, v9, s99
	s_sub_i32 s22, 63, s99
	s_add_i32 s99, s99, 1
	v_addc_co_u32_e32 v2, vcc, 0, v2, vcc
	v_cmp_gt_i64_e32 vcc, s[20:21], v[8:9]
	v_readlane_b32 s21, v9, s99
	s_sub_i32 s20, 63, s99
	s_add_i32 s99, s99, 1
; __device__ __forceinline__ void phase_nrr(const Frame& F, const Args& a, int l, const bf16_t* XA, const float* g, const float* modl, unsigned char* XN8) {
;     ...
;             int rank = 0;
; #pragma unroll 8
;             for (int e2 = 0; e2 < 64; ++e2) { const float v = __int_as_float(__builtin_amdgcn_readlane(__float_as_int(val), e2)); rank += (v > val || (v == val && e2 < lane)) ? 1 : 0; }
;             const bool sel = rank < TOPK;
;             const float ssum = wave_sum(sel ? sc : 0.f);
;             if (sel) { const int p = atomicAdd((int*)(hist + lane), 1); top_e[t * TOPK + rank] = lane; gate[t * TOPK + rank] = sc / ssum * 2.5f; lpos[t * TOPK + rank] = p; }
	v_addc_co_u32_e32 v2, vcc, 0, v2, vcc
	v_cmp_gt_i64_e32 vcc, s[22:23], v[8:9]
	v_readlane_b32 s23, v9, s99
	s_sub_i32 s22, 63, s99
	s_add_i32 s99, s99, 1
	v_addc_co_u32_e32 v2, vcc, 0, v2, vcc
	v_cmp_gt_i64_e32 vcc, s[20:21], v[8:9]
	v_readlane_b32 s21, v9, s99
	s_sub_i32 s20, 63, s99
	s_nop 0
	v_addc_co_u32_e32 v2, vcc, 0, v2, vcc
	v_cmp_gt_i64_e32 vcc, s[22:23], v[8:9]
	v_readlane_b32 s23, v9, s100
	s_sub_i32 s22, 63, s100
	s_add_i32 s100, s100, 1
	v_addc_co_u32_e32 v2, vcc, 0, v2, vcc
	v_cmp_gt_i64_e32 vcc, s[20:21], v[8:9]
	v_readlane_b32 s21, v9, s100
	s_sub_i32 s20, 63, s100
	s_add_i32 s100, s100, 1
	v_addc_co_u32_e32 v2, vcc, 0, v2, vcc
	v_cmp_gt_i64_e32 vcc, s[22:23], v[8:9]
	v_readlane_b32 s23, v9, s100
	s_sub_i32 s22, 63, s100
	s_add_i32 s100, s100, 1
	v_addc_co_u32_e32 v2, vcc, 0, v2, vcc
	v_cmp_gt_i64_e32 vcc, s[20:21], v[8:9]
	v_readlane_b32 s21, v9, s100
	s_sub_i32 s20, 63, s100
	s_add_i32 s100, s100, 1
	v_addc_co_u32_e32 v2, vcc, 0, v2, vcc
	v_cmp_gt_i64_e32 vcc, s[22:23], v[8:9]
	v_readlane_b32 s23, v9, s100
	s_sub_i32 s22, 63, s100
	s_add_i32 s100, s100, 1
	v_addc_co_u32_e32 v2, vcc, 0, v2, vcc
	v_cmp_gt_i64_e32 vcc, s[20:21], v[8:9]
	v_readlane_b32 s21, v9, s100
	s_sub_i32 s20, 63, s100
	s_add_i32 s100, s100, 1
	v_addc_co_u32_e32 v2, vcc, 0, v2, vcc
	v_cmp_gt_i64_e32 vcc, s[22:23], v[8:9]
	v_readlane_b32 s23, v9, s100
	s_sub_i32 s22, 63, s100
	s_add_i32 s100, s100, 1
	v_addc_co_u32_e32 v2, vcc, 0, v2, vcc
	v_cmp_gt_i64_e32 vcc, s[20:21], v[8:9]
	v_readlane_b32 s21, v9, s100
	s_sub_i32 s20, 63, s100
	s_nop 0
	v_addc_co_u32_e32 v2, vcc, 0, v2, vcc
	v_cmp_gt_i64_e32 vcc, s[22:23], v[8:9]
	v_readlane_b32 s23, v9, s101
	s_sub_i32 s22, 63, s101
	s_add_i32 s101, s101, 1
	v_addc_co_u32_e32 v2, vcc, 0, v2, vcc
	v_cmp_gt_i64_e32 vcc, s[20:21], v[8:9]
	v_readlane_b32 s21, v9, s101
	s_sub_i32 s20, 63, s101
	s_add_i32 s101, s101, 1
	v_addc_co_u32_e32 v2, vcc, 0, v2, vcc
	v_cmp_gt_i64_e32 vcc, s[22:23], v[8:9]
	v_readlane_b32 s23, v9, s101
	s_sub_i32 s22, 63, s101
	s_add_i32 s101, s101, 1
	v_addc_co_u32_e32 v2, vcc, 0, v2, vcc
	v_cmp_gt_i64_e32 vcc, s[20:21], v[8:9]
	v_readlane_b32 s21, v9, s101
	s_sub_i32 s20, 63, s101
	s_add_i32 s101, s101, 1
	v_addc_co_u32_e32 v2, vcc, 0, v2, vcc
	v_cmp_gt_i64_e32 vcc, s[22:23], v[8:9]
	v_readlane_b32 s23, v9, s101
	s_sub_i32 s22, 63, s101
	s_add_i32 s101, s101, 1
	v_addc_co_u32_e32 v2, vcc, 0, v2, vcc
	v_cmp_gt_i64_e32 vcc, s[20:21], v[8:9]
	v_readlane_b32 s21, v9, s101
	s_sub_i32 s20, 63, s101
	s_add_i32 s101, s101, 1
	v_addc_co_u32_e32 v2, vcc, 0, v2, vcc
	v_cmp_gt_i64_e32 vcc, s[22:23], v[8:9]
	v_readlane_b32 s23, v9, s101
	s_sub_i32 s22, 63, s101
	s_add_i32 s101, s101, 1
	v_addc_co_u32_e32 v2, vcc, 0, v2, vcc
	v_cmp_gt_i64_e32 vcc, s[20:21], v[8:9]
	v_readlane_b32 s21, v9, s101
	s_sub_i32 s20, 63, s101
	s_nop 0
	v_addc_co_u32_e32 v2, vcc, 0, v2, vcc
	v_cmp_gt_i64_e32 vcc, s[22:23], v[8:9]
	s_nop 1
	v_addc_co_u32_e32 v2, vcc, 0, v2, vcc
	v_cmp_gt_i64_e32 vcc, s[20:21], v[8:9]
	s_nop 1
	v_addc_co_u32_e32 v2, vcc, 0, v2, vcc
	v_cmp_gt_u32_e32 vcc, 6, v2
	s_nop 1
	v_cndmask_b32_e32 v6, 0, v5, vcc
	s_nop 1
	v_add_f32_dpp v6, v6, v6 quad_perm:[1,0,3,2] row_mask:0xf bank_mask:0xf
	s_nop 1
	v_add_f32_dpp v6, v6, v6 quad_perm:[2,3,0,1] row_mask:0xf bank_mask:0xf
	s_nop 1
	v_add_f32_dpp v6, v6, v6 row_half_mirror row_mask:0xf bank_mask:0xf
	s_nop 1
	v_add_f32_dpp v6, v6, v6 row_mirror row_mask:0xf bank_mask:0xf
	s_nop 0
	ds_bpermute_b32 v7, v222, v6
	s_waitcnt lgkmcnt(0)
	v_add_f32_e32 v6, v6, v7
	v_mov_b32_e32 v7, v6
	s_nop 1
	v_permlane32_swap_b32_e32 v7, v6
	s_and_saveexec_b64 s[20:21], vcc
	s_cbranch_execz .LBB0_1320
	s_waitcnt lgkmcnt(0)
	v_add_f32_e32 v10, v6, v7
	v_mad_u64_u32 v[6:7], s[22:23], s54, 6, v[2:3]
	v_div_scale_f32 v2, s[22:23], v10, v10, v5
	v_rcp_f32_e32 v12, v2
	v_ashrrev_i32_e32 v7, 31, v6
	v_lshlrev_b64 v[6:7], 2, v[6:7]
	v_lshl_add_u64 v[8:9], s[42:43], 0, v[6:7]
	ds_add_rtn_u32 v11, v227, v243
	global_store_dword v[8:9], v230, off
	v_fma_f32 v8, -v2, v12, 1.0
	v_fmac_f32_e32 v12, v8, v12
	v_div_scale_f32 v8, vcc, v5, v10, v5
	v_mul_f32_e32 v9, v8, v12
	v_fma_f32 v13, -v2, v9, v8
	v_fmac_f32_e32 v9, v13, v12
	v_fma_f32 v2, -v2, v9, v8
	v_div_fmas_f32 v2, v2, v12, v9
	v_div_fixup_f32 v2, v2, v10, v5
	v_mul_f32_e32 v2, 0x40200000, v2
	v_lshl_add_u64 v[8:9], s[44:45], 0, v[6:7]
	v_lshl_add_u64 v[6:7], s[46:47], 0, v[6:7]
	global_store_dword v[8:9], v2, off
	s_waitcnt lgkmcnt(0)
	global_store_dword v[6:7], v11, off
; __device__ __forceinline__ void phase_nrr(const Frame& F, const Args& a, int l, const bf16_t* XA, const float* g, const float* modl, unsigned char* XN8) {
;     ...
;         for (int i = 0; i < 8; ++i) { const int t = tb + i;
;             const float lg = Pl[(w * 8 + i) * NE + lane] + Pl[(64 + w * 8 + i) * NE + lane]; const float sc = 1.f / (1.f + __expf(-lg)); const float bb = sc + bias;
;             float m1 = bb; m1 = fmaxf(m1, __shfl_xor(m1, 1)); m1 = fmaxf(m1, __shfl_xor(m1, 2)); m1 = fmaxf(m1, __shfl_xor(m1, 4));
;             const unsigned long long eq = __ballot(bb == m1); const int gbase = lane & ~7; const unsigned grpmask = (unsigned)((eq >> gbase) & 0xffull);
;             const int first = gbase + __builtin_ctz(grpmask);
;             float m2 = (lane == first) ? -INFINITY : bb; m2 = fmaxf(m2, __shfl_xor(m2, 1)); m2 = fmaxf(m2, __shfl_xor(m2, 2)); m2 = fmaxf(m2, __shfl_xor(m2, 4));
;             const float gsum = m1 + m2; const int gq = lane >> 3;
;             int grank = 0;
; #pragma unroll
;             for (int g2 = 0; g2 < 8; ++g2) { const float v = __int_as_float(__builtin_amdgcn_readlane(__float_as_int(gsum), g2 * 8)); grank += (v > gsum || (v == gsum && g2 < gq)) ? 1 : 0; }
;             const bool keep = grank < 4; const float val = keep ? bb : -INFINITY;
;             int rank = 0;
; #pragma unroll 8
;             for (int e2 = 0; e2 < 64; ++e2) { const float v = __int_as_float(__builtin_amdgcn_readlane(__float_as_int(val), e2)); rank += (v > val || (v == val && e2 < lane)) ? 1 : 0; }
.LBB0_1320:
	s_or_b64 exec, exec, s[20:21]
	v_add_u32_e32 v2, s78, v226
	ds_read_b32 v2, v2
	ds_read_b32 v5, v4 offset:17152
	s_mov_b32 s3, 0
	s_waitcnt lgkmcnt(0)
	v_add_f32_e32 v2, v2, v5
	v_mul_f32_e32 v2, 0xbfb8aa3b, v2
	v_exp_f32_e32 v2, v2
	s_nop 0
	v_add_f32_e32 v2, 1.0, v2
	v_div_scale_f32 v5, s[20:21], v2, v2, 1.0
	v_rcp_f32_e32 v6, v5
	v_div_scale_f32 v7, vcc, 1.0, v2, 1.0
	v_fma_f32 v8, -v5, v6, 1.0
	v_fmac_f32_e32 v6, v8, v6
	v_mul_f32_e32 v8, v7, v6
	v_fma_f32 v9, -v5, v8, v7
	v_fmac_f32_e32 v8, v9, v6
	v_fma_f32 v5, -v5, v8, v7
	v_div_fmas_f32 v5, v5, v6, v8
	v_div_fixup_f32 v5, v5, v2, 1.0
	v_add_f32_e32 v2, v3, v5
	s_nop 1
	s_waitcnt lgkmcnt(0)
	v_max_f32_dpp v6, v2, v2 quad_perm:[1,0,3,2] row_mask:0xf bank_mask:0xf
	s_nop 1
	s_waitcnt lgkmcnt(0)
	v_max_f32_dpp v6, v6, v6 quad_perm:[2,3,0,1] row_mask:0xf bank_mask:0xf
	s_nop 1
	s_waitcnt lgkmcnt(0)
	v_max_f32_dpp v8, v6, v6 row_half_mirror row_mask:0xf bank_mask:0xf
	v_cmp_eq_f32_e32 vcc, v2, v8
	s_nop 1
	v_lshrrev_b64 v[6:7], v200, vcc
	v_ffbl_b32_sdwa v6, v6 dst_sel:DWORD dst_unused:UNUSED_PAD src0_sel:BYTE_0
	v_add_u32_e32 v6, v6, v200
	v_cmp_ne_u32_e32 vcc, v230, v6
	s_nop 1
	v_cndmask_b32_e32 v6, v245, v2, vcc
	s_nop 1
	s_waitcnt lgkmcnt(0)
	v_max_f32_dpp v6, v6, v6 quad_perm:[1,0,3,2] row_mask:0xf bank_mask:0xf
	s_nop 1
	s_waitcnt lgkmcnt(0)
	v_max_f32_dpp v6, v6, v6 quad_perm:[2,3,0,1] row_mask:0xf bank_mask:0xf
	s_nop 1
	s_waitcnt lgkmcnt(0)
	v_max_f32_dpp v6, v6, v6 row_half_mirror row_mask:0xf bank_mask:0xf
	v_add_f32_e32 v6, v8, v6
	s_nop 0
	v_readlane_b32 s5, v6, 0
	v_readlane_b32 s24, v6, 8
	v_readlane_b32 s28, v6, 16
	v_cmp_eq_f32_e64 s[20:21], s5, v6
	v_cmp_gt_f32_e32 vcc, s5, v6
	v_cmp_gt_f32_e64 s[22:23], s24, v6
	v_cmp_eq_f32_e64 s[24:25], s24, v6
	s_and_b64 s[20:21], s[0:1], s[20:21]
	v_readlane_b32 s34, v6, 24
	v_cmp_gt_f32_e64 s[26:27], s28, v6
	v_cmp_eq_f32_e64 s[28:29], s28, v6
	s_and_b64 s[24:25], s[6:7], s[24:25]
	s_or_b64 s[20:21], vcc, s[20:21]
	v_readlane_b32 s40, v6, 32
	v_cmp_gt_f32_e64 s[30:31], s34, v6
	v_cmp_eq_f32_e64 s[34:35], s34, v6
	s_and_b64 s[28:29], s[8:9], s[28:29]
	v_cndmask_b32_e64 v7, 0, 1, s[20:21]
	s_or_b64 s[20:21], s[22:23], s[24:25]
	v_cmp_gt_f32_e64 s[36:37], s40, v6
	v_cmp_eq_f32_e64 s[40:41], s40, v6
	s_and_b64 s[34:35], s[10:11], s[34:35]
	v_cndmask_b32_e64 v8, 0, 1, s[20:21]
	s_or_b64 s[20:21], s[26:27], s[28:29]
	s_and_b64 s[40:41], s[12:13], s[40:41]
	v_cndmask_b32_e64 v9, 0, 1, s[20:21]
	s_or_b64 s[20:21], s[30:31], s[34:35]
	v_readlane_b32 s54, v6, 40
	v_cndmask_b32_e64 v10, 0, 1, s[20:21]
	s_or_b64 s[20:21], s[36:37], s[40:41]
	v_cndmask_b32_e64 v11, 0, 1, s[20:21]
	v_cmp_eq_f32_e64 s[20:21], s54, v6
	v_cmp_gt_f32_e32 vcc, s54, v6
	s_and_b64 s[20:21], s[14:15], s[20:21]
	s_or_b64 s[20:21], vcc, s[20:21]
	v_readlane_b32 s5, v6, 48
	v_cndmask_b32_e64 v12, 0, 1, s[20:21]
	s_nop 0
	v_cmp_eq_f32_e64 s[20:21], s5, v6
	v_cmp_gt_f32_e32 vcc, s5, v6
	s_and_b64 s[20:21], s[16:17], s[20:21]
	v_readlane_b32 s5, v6, 56
	s_or_b64 s[20:21], vcc, s[20:21]
	v_cndmask_b32_e64 v13, 0, 1, s[20:21]
	v_cmp_gt_f32_e32 vcc, s5, v6
	s_nop 1
	v_cndmask_b32_e64 v6, 0, 1, vcc
	v_add_u32_e32 v6, v8, v6
	v_add3_u32 v6, v6, v7, v9
	v_add3_u32 v6, v6, v10, v11
	v_add3_u32 v6, v6, v12, v13
	v_cmp_eq_u32_e32 vcc, 0, v6
	s_ff1_i32_b64 s98, vcc
	v_cmp_eq_u32_e32 vcc, 1, v6
	s_ff1_i32_b64 s99, vcc
	v_cmp_eq_u32_e32 vcc, 2, v6
	s_ff1_i32_b64 s100, vcc
	v_cmp_eq_u32_e32 vcc, 3, v6
	s_ff1_i32_b64 s101, vcc
	v_cmp_gt_u32_e32 vcc, 4, v6
	s_nop 1
	v_cndmask_b32_e32 v6, v245, v2, vcc
	v_mov_b32_e32 v2, 0
	v_ashrrev_i32_e32 v9, 31, v6
	v_sub_u32_e32 v8, 63, v230
	v_and_b32_e32 v9, 0x7fffffff, v9
	v_xor_b32_e32 v9, v6, v9
	s_nop 0
	v_readlane_b32 s23, v9, s98
	s_sub_i32 s22, 63, s98
	s_add_i32 s98, s98, 1
	v_readlane_b32 s21, v9, s98
	s_sub_i32 s20, 63, s98
	s_add_i32 s98, s98, 1
	v_cmp_gt_i64_e32 vcc, s[22:23], v[8:9]
	v_readlane_b32 s23, v9, s98
	s_sub_i32 s22, 63, s98
	s_add_i32 s98, s98, 1
	v_addc_co_u32_e32 v2, vcc, 0, v2, vcc
	v_cmp_gt_i64_e32 vcc, s[20:21], v[8:9]
	v_readlane_b32 s21, v9, s98
	s_sub_i32 s20, 63, s98
	s_add_i32 s98, s98, 1
	v_addc_co_u32_e32 v2, vcc, 0, v2, vcc
	v_cmp_gt_i64_e32 vcc, s[22:23], v[8:9]
	v_readlane_b32 s23, v9, s98
	s_sub_i32 s22, 63, s98
	s_add_i32 s98, s98, 1
	v_addc_co_u32_e32 v2, vcc, 0, v2, vcc
	v_cmp_gt_i64_e32 vcc, s[20:21], v[8:9]
	v_readlane_b32 s21, v9, s98
	s_sub_i32 s20, 63, s98
	s_add_i32 s98, s98, 1
	v_addc_co_u32_e32 v2, vcc, 0, v2, vcc
	v_cmp_gt_i64_e32 vcc, s[22:23], v[8:9]
	v_readlane_b32 s23, v9, s98
	s_sub_i32 s22, 63, s98
	s_add_i32 s98, s98, 1
	v_addc_co_u32_e32 v2, vcc, 0, v2, vcc
	v_cmp_gt_i64_e32 vcc, s[20:21], v[8:9]
	v_readlane_b32 s21, v9, s98
	s_sub_i32 s20, 63, s98
	s_nop 0
	v_addc_co_u32_e32 v2, vcc, 0, v2, vcc
	v_cmp_gt_i64_e32 vcc, s[22:23], v[8:9]
	v_readlane_b32 s23, v9, s99
	s_sub_i32 s22, 63, s99
	s_add_i32 s99, s99, 1
	v_addc_co_u32_e32 v2, vcc, 0, v2, vcc
	v_cmp_gt_i64_e32 vcc, s[20:21], v[8:9]
	v_readlane_b32 s21, v9, s99
	s_sub_i32 s20, 63, s99
	s_add_i32 s99, s99, 1
	v_addc_co_u32_e32 v2, vcc, 0, v2, vcc
	v_cmp_gt_i64_e32 vcc, s[22:23], v[8:9]
	v_readlane_b32 s23, v9, s99
	s_sub_i32 s22, 63, s99
	s_add_i32 s99, s99, 1
	v_addc_co_u32_e32 v2, vcc, 0, v2, vcc
	v_cmp_gt_i64_e32 vcc, s[20:21], v[8:9]
	v_readlane_b32 s21, v9, s99
	s_sub_i32 s20, 63, s99
	s_add_i32 s99, s99, 1
	v_addc_co_u32_e32 v2, vcc, 0, v2, vcc
	v_cmp_gt_i64_e32 vcc, s[22:23], v[8:9]
	v_readlane_b32 s23, v9, s99
	s_sub_i32 s22, 63, s99
	s_add_i32 s99, s99, 1
	v_addc_co_u32_e32 v2, vcc, 0, v2, vcc
	v_cmp_gt_i64_e32 vcc, s[20:21], v[8:9]
	v_readlane_b32 s21, v9, s99
	s_sub_i32 s20, 63, s99
	s_add_i32 s99, s99, 1
; __device__ __forceinline__ void phase_nrr(const Frame& F, const Args& a, int l, const bf16_t* XA, const float* g, const float* modl, unsigned char* XN8) {
;     ...
;             int rank = 0;
; #pragma unroll 8
;             for (int e2 = 0; e2 < 64; ++e2) { const float v = __int_as_float(__builtin_amdgcn_readlane(__float_as_int(val), e2)); rank += (v > val || (v == val && e2 < lane)) ? 1 : 0; }
;             const bool sel = rank < TOPK;
;             const float ssum = wave_sum(sel ? sc : 0.f);
;             if (sel) { const int p = atomicAdd((int*)(hist + lane), 1); top_e[t * TOPK + rank] = lane; gate[t * TOPK + rank] = sc / ssum * 2.5f; lpos[t * TOPK + rank] = p; }
	v_addc_co_u32_e32 v2, vcc, 0, v2, vcc
	v_cmp_gt_i64_e32 vcc, s[22:23], v[8:9]
	v_readlane_b32 s23, v9, s99
	s_sub_i32 s22, 63, s99
	s_add_i32 s99, s99, 1
	v_addc_co_u32_e32 v2, vcc, 0, v2, vcc
	v_cmp_gt_i64_e32 vcc, s[20:21], v[8:9]
	v_readlane_b32 s21, v9, s99
	s_sub_i32 s20, 63, s99
	s_nop 0
	v_addc_co_u32_e32 v2, vcc, 0, v2, vcc
	v_cmp_gt_i64_e32 vcc, s[22:23], v[8:9]
	v_readlane_b32 s23, v9, s100
	s_sub_i32 s22, 63, s100
	s_add_i32 s100, s100, 1
	v_addc_co_u32_e32 v2, vcc, 0, v2, vcc
	v_cmp_gt_i64_e32 vcc, s[20:21], v[8:9]
	v_readlane_b32 s21, v9, s100
	s_sub_i32 s20, 63, s100
	s_add_i32 s100, s100, 1
	v_addc_co_u32_e32 v2, vcc, 0, v2, vcc
	v_cmp_gt_i64_e32 vcc, s[22:23], v[8:9]
	v_readlane_b32 s23, v9, s100
	s_sub_i32 s22, 63, s100
	s_add_i32 s100, s100, 1
	v_addc_co_u32_e32 v2, vcc, 0, v2, vcc
	v_cmp_gt_i64_e32 vcc, s[20:21], v[8:9]
	v_readlane_b32 s21, v9, s100
	s_sub_i32 s20, 63, s100
	s_add_i32 s100, s100, 1
	v_addc_co_u32_e32 v2, vcc, 0, v2, vcc
	v_cmp_gt_i64_e32 vcc, s[22:23], v[8:9]
	v_readlane_b32 s23, v9, s100
	s_sub_i32 s22, 63, s100
	s_add_i32 s100, s100, 1
	v_addc_co_u32_e32 v2, vcc, 0, v2, vcc
	v_cmp_gt_i64_e32 vcc, s[20:21], v[8:9]
	v_readlane_b32 s21, v9, s100
	s_sub_i32 s20, 63, s100
	s_add_i32 s100, s100, 1
	v_addc_co_u32_e32 v2, vcc, 0, v2, vcc
	v_cmp_gt_i64_e32 vcc, s[22:23], v[8:9]
	v_readlane_b32 s23, v9, s100
	s_sub_i32 s22, 63, s100
	s_add_i32 s100, s100, 1
	v_addc_co_u32_e32 v2, vcc, 0, v2, vcc
	v_cmp_gt_i64_e32 vcc, s[20:21], v[8:9]
	v_readlane_b32 s21, v9, s100
	s_sub_i32 s20, 63, s100
	s_nop 0
	v_addc_co_u32_e32 v2, vcc, 0, v2, vcc
	v_cmp_gt_i64_e32 vcc, s[22:23], v[8:9]
	v_readlane_b32 s23, v9, s101
	s_sub_i32 s22, 63, s101
	s_add_i32 s101, s101, 1
	v_addc_co_u32_e32 v2, vcc, 0, v2, vcc
	v_cmp_gt_i64_e32 vcc, s[20:21], v[8:9]
	v_readlane_b32 s21, v9, s101
	s_sub_i32 s20, 63, s101
	s_add_i32 s101, s101, 1
	v_addc_co_u32_e32 v2, vcc, 0, v2, vcc
	v_cmp_gt_i64_e32 vcc, s[22:23], v[8:9]
	v_readlane_b32 s23, v9, s101
	s_sub_i32 s22, 63, s101
	s_add_i32 s101, s101, 1
	v_addc_co_u32_e32 v2, vcc, 0, v2, vcc
	v_cmp_gt_i64_e32 vcc, s[20:21], v[8:9]
	v_readlane_b32 s21, v9, s101
	s_sub_i32 s20, 63, s101
	s_add_i32 s101, s101, 1
	v_addc_co_u32_e32 v2, vcc, 0, v2, vcc
	v_cmp_gt_i64_e32 vcc, s[22:23], v[8:9]
	v_readlane_b32 s23, v9, s101
	s_sub_i32 s22, 63, s101
	s_add_i32 s101, s101, 1
	v_addc_co_u32_e32 v2, vcc, 0, v2, vcc
	v_cmp_gt_i64_e32 vcc, s[20:21], v[8:9]
	v_readlane_b32 s21, v9, s101
	s_sub_i32 s20, 63, s101
	s_add_i32 s101, s101, 1
	v_addc_co_u32_e32 v2, vcc, 0, v2, vcc
	v_cmp_gt_i64_e32 vcc, s[22:23], v[8:9]
	v_readlane_b32 s23, v9, s101
	s_sub_i32 s22, 63, s101
	s_add_i32 s101, s101, 1
	v_addc_co_u32_e32 v2, vcc, 0, v2, vcc
	v_cmp_gt_i64_e32 vcc, s[20:21], v[8:9]
	v_readlane_b32 s21, v9, s101
	s_sub_i32 s20, 63, s101
	s_nop 0
	v_addc_co_u32_e32 v2, vcc, 0, v2, vcc
	v_cmp_gt_i64_e32 vcc, s[22:23], v[8:9]
	s_nop 1
	v_addc_co_u32_e32 v2, vcc, 0, v2, vcc
	v_cmp_gt_i64_e32 vcc, s[20:21], v[8:9]
	s_nop 1
	v_addc_co_u32_e32 v2, vcc, 0, v2, vcc
	v_cmp_gt_u32_e32 vcc, 6, v2
	s_nop 1
	v_cndmask_b32_e32 v6, 0, v5, vcc
	s_nop 1
	v_add_f32_dpp v6, v6, v6 quad_perm:[1,0,3,2] row_mask:0xf bank_mask:0xf
	s_nop 1
	v_add_f32_dpp v6, v6, v6 quad_perm:[2,3,0,1] row_mask:0xf bank_mask:0xf
	s_nop 1
	v_add_f32_dpp v6, v6, v6 row_half_mirror row_mask:0xf bank_mask:0xf
	s_nop 1
	v_add_f32_dpp v6, v6, v6 row_mirror row_mask:0xf bank_mask:0xf
	s_nop 0
	ds_bpermute_b32 v7, v222, v6
	s_waitcnt lgkmcnt(0)
	v_add_f32_e32 v6, v6, v7
	v_mov_b32_e32 v7, v6
	s_nop 1
	v_permlane32_swap_b32_e32 v7, v6
	s_and_saveexec_b64 s[20:21], vcc
	s_cbranch_execz .LBB0_1324
	s_waitcnt lgkmcnt(0)
	v_add_f32_e32 v10, v6, v7
	v_mad_u64_u32 v[6:7], s[4:5], s4, 6, v[2:3]
	v_div_scale_f32 v2, s[4:5], v10, v10, v5
	v_rcp_f32_e32 v12, v2
	v_ashrrev_i32_e32 v7, 31, v6
	v_lshlrev_b64 v[6:7], 2, v[6:7]
	v_lshl_add_u64 v[8:9], s[42:43], 0, v[6:7]
	ds_add_rtn_u32 v11, v227, v243
	global_store_dword v[8:9], v230, off
	v_fma_f32 v8, -v2, v12, 1.0
	v_fmac_f32_e32 v12, v8, v12
	v_div_scale_f32 v8, vcc, v5, v10, v5
	v_mul_f32_e32 v9, v8, v12
	v_fma_f32 v13, -v2, v9, v8
	v_fmac_f32_e32 v9, v13, v12
	v_fma_f32 v2, -v2, v9, v8
	v_div_fmas_f32 v2, v2, v12, v9
	v_div_fixup_f32 v2, v2, v10, v5
	v_mul_f32_e32 v2, 0x40200000, v2
	v_lshl_add_u64 v[8:9], s[44:45], 0, v[6:7]
	v_lshl_add_u64 v[6:7], s[46:47], 0, v[6:7]
	global_store_dword v[8:9], v2, off
	s_waitcnt lgkmcnt(0)
	global_store_dword v[6:7], v11, off
; __device__ __forceinline__ void phase_nrr(const Frame& F, const Args& a, int l, const bf16_t* XA, const float* g, const float* modl, unsigned char* XN8) {
;     ...
;         for (int i = 0; i < 8; ++i) { const int t = tb + i;
;             const float lg = Pl[(w * 8 + i) * NE + lane] + Pl[(64 + w * 8 + i) * NE + lane]; const float sc = 1.f / (1.f + __expf(-lg)); const float bb = sc + bias;
;             float m1 = bb; m1 = fmaxf(m1, __shfl_xor(m1, 1)); m1 = fmaxf(m1, __shfl_xor(m1, 2)); m1 = fmaxf(m1, __shfl_xor(m1, 4));
;             const unsigned long long eq = __ballot(bb == m1); const int gbase = lane & ~7; const unsigned grpmask = (unsigned)((eq >> gbase) & 0xffull);
;             const int first = gbase + __builtin_ctz(grpmask);
;             float m2 = (lane == first) ? -INFINITY : bb; m2 = fmaxf(m2, __shfl_xor(m2, 1)); m2 = fmaxf(m2, __shfl_xor(m2, 2)); m2 = fmaxf(m2, __shfl_xor(m2, 4));
;             const float gsum = m1 + m2; const int gq = lane >> 3;
;             int grank = 0;
; #pragma unroll
;             for (int g2 = 0; g2 < 8; ++g2) { const float v = __int_as_float(__builtin_amdgcn_readlane(__float_as_int(gsum), g2 * 8)); grank += (v > gsum || (v == gsum && g2 < gq)) ? 1 : 0; }
;             const bool keep = grank < 4; const float val = keep ? bb : -INFINITY;
;             int rank = 0;
; #pragma unroll 8
;             for (int e2 = 0; e2 < 64; ++e2) { const float v = __int_as_float(__builtin_amdgcn_readlane(__float_as_int(val), e2)); rank += (v > val || (v == val && e2 < lane)) ? 1 : 0; }
.LBB0_1324:
	s_or_b64 exec, exec, s[20:21]
	v_add_u32_e32 v2, s79, v226
	ds_read_b32 v2, v2
	ds_read_b32 v5, v4 offset:17408
	s_mov_b32 s3, 0
	s_waitcnt lgkmcnt(0)
	v_add_f32_e32 v2, v2, v5
	v_mul_f32_e32 v2, 0xbfb8aa3b, v2
	v_exp_f32_e32 v2, v2
	s_nop 0
	v_add_f32_e32 v2, 1.0, v2
	v_div_scale_f32 v5, s[4:5], v2, v2, 1.0
	v_rcp_f32_e32 v6, v5
	v_div_scale_f32 v7, vcc, 1.0, v2, 1.0
	v_fma_f32 v8, -v5, v6, 1.0
	v_fmac_f32_e32 v6, v8, v6
	v_mul_f32_e32 v8, v7, v6
	v_fma_f32 v9, -v5, v8, v7
	v_fmac_f32_e32 v8, v9, v6
	v_fma_f32 v5, -v5, v8, v7
	v_div_fmas_f32 v5, v5, v6, v8
	v_div_fixup_f32 v2, v5, v2, 1.0
	v_add_f32_e32 v5, v3, v2
	s_nop 1
	s_waitcnt lgkmcnt(0)
	v_max_f32_dpp v6, v5, v5 quad_perm:[1,0,3,2] row_mask:0xf bank_mask:0xf
	s_nop 1
	s_waitcnt lgkmcnt(0)
	v_max_f32_dpp v6, v6, v6 quad_perm:[2,3,0,1] row_mask:0xf bank_mask:0xf
	s_nop 1
	s_waitcnt lgkmcnt(0)
	v_max_f32_dpp v8, v6, v6 row_half_mirror row_mask:0xf bank_mask:0xf
	v_cmp_eq_f32_e32 vcc, v5, v8
	s_nop 1
	v_lshrrev_b64 v[6:7], v200, vcc
	v_ffbl_b32_sdwa v6, v6 dst_sel:DWORD dst_unused:UNUSED_PAD src0_sel:BYTE_0
	v_add_u32_e32 v6, v6, v200
	v_cmp_ne_u32_e32 vcc, v230, v6
	s_nop 1
	v_cndmask_b32_e32 v6, v245, v5, vcc
	s_nop 1
	s_waitcnt lgkmcnt(0)
	v_max_f32_dpp v6, v6, v6 quad_perm:[1,0,3,2] row_mask:0xf bank_mask:0xf
	s_nop 1
	s_waitcnt lgkmcnt(0)
	v_max_f32_dpp v6, v6, v6 quad_perm:[2,3,0,1] row_mask:0xf bank_mask:0xf
	s_nop 1
	s_waitcnt lgkmcnt(0)
	v_max_f32_dpp v6, v6, v6 row_half_mirror row_mask:0xf bank_mask:0xf
	v_add_f32_e32 v6, v8, v6
	s_nop 0
	v_readlane_b32 s4, v6, 0
	v_readlane_b32 s5, v6, 8
	v_readlane_b32 s28, v6, 16
	v_cmp_eq_f32_e64 s[20:21], s4, v6
	v_cmp_gt_f32_e32 vcc, s4, v6
	v_cmp_gt_f32_e64 s[22:23], s5, v6
	v_cmp_eq_f32_e64 s[24:25], s5, v6
	s_and_b64 s[4:5], s[0:1], s[20:21]
	v_readlane_b32 s34, v6, 24
	v_cmp_gt_f32_e64 s[26:27], s28, v6
	v_cmp_eq_f32_e64 s[28:29], s28, v6
	s_and_b64 s[20:21], s[6:7], s[24:25]
	s_or_b64 s[4:5], vcc, s[4:5]
	v_readlane_b32 s40, v6, 32
	v_cmp_gt_f32_e64 s[30:31], s34, v6
	v_cmp_eq_f32_e64 s[34:35], s34, v6
	s_and_b64 s[24:25], s[8:9], s[28:29]
	v_cndmask_b32_e64 v7, 0, 1, s[4:5]
	s_or_b64 s[4:5], s[22:23], s[20:21]
	v_cmp_gt_f32_e64 s[36:37], s40, v6
	v_cmp_eq_f32_e64 s[40:41], s40, v6
	s_and_b64 s[28:29], s[10:11], s[34:35]
	v_cndmask_b32_e64 v8, 0, 1, s[4:5]
	s_or_b64 s[4:5], s[26:27], s[24:25]
	v_readlane_b32 s54, v6, 40
	s_and_b64 s[34:35], s[12:13], s[40:41]
	v_cndmask_b32_e64 v9, 0, 1, s[4:5]
	s_or_b64 s[4:5], s[30:31], s[28:29]
	v_cndmask_b32_e64 v10, 0, 1, s[4:5]
	s_or_b64 s[4:5], s[36:37], s[34:35]
	v_cmp_eq_f32_e64 s[20:21], s54, v6
	v_cndmask_b32_e64 v11, 0, 1, s[4:5]
	v_cmp_gt_f32_e32 vcc, s54, v6
	s_and_b64 s[4:5], s[14:15], s[20:21]
	s_or_b64 s[4:5], vcc, s[4:5]
	v_cndmask_b32_e64 v12, 0, 1, s[4:5]
	v_readlane_b32 s4, v6, 48
	s_nop 1
	v_cmp_eq_f32_e64 s[20:21], s4, v6
	v_cmp_gt_f32_e32 vcc, s4, v6
	s_and_b64 s[4:5], s[16:17], s[20:21]
	s_or_b64 s[4:5], vcc, s[4:5]
	v_cndmask_b32_e64 v13, 0, 1, s[4:5]
	v_readlane_b32 s4, v6, 56
	s_nop 1
	v_cmp_gt_f32_e32 vcc, s4, v6
	s_nop 1
	v_cndmask_b32_e64 v6, 0, 1, vcc
	v_add_u32_e32 v6, v8, v6
	v_add3_u32 v6, v6, v7, v9
	v_add3_u32 v6, v6, v10, v11
	v_add3_u32 v6, v6, v12, v13
	v_cmp_eq_u32_e32 vcc, 0, v6
	s_ff1_i32_b64 s98, vcc
	v_cmp_eq_u32_e32 vcc, 1, v6
	s_ff1_i32_b64 s99, vcc
	v_cmp_eq_u32_e32 vcc, 2, v6
	s_ff1_i32_b64 s100, vcc
	v_cmp_eq_u32_e32 vcc, 3, v6
	s_ff1_i32_b64 s101, vcc
	v_cmp_gt_u32_e32 vcc, 4, v6
	v_mov_b32_e32 v6, 0
	s_nop 0
	v_cndmask_b32_e32 v5, v245, v5, vcc
	v_ashrrev_i32_e32 v9, 31, v5
	v_sub_u32_e32 v8, 63, v230
	v_and_b32_e32 v9, 0x7fffffff, v9
	v_xor_b32_e32 v9, v5, v9
	s_nop 0
	v_readlane_b32 s23, v9, s98
	s_sub_i32 s22, 63, s98
	s_add_i32 s98, s98, 1
	v_readlane_b32 s21, v9, s98
	s_sub_i32 s20, 63, s98
	s_add_i32 s98, s98, 1
	v_cmp_gt_i64_e32 vcc, s[22:23], v[8:9]
	v_readlane_b32 s23, v9, s98
	s_sub_i32 s22, 63, s98
	s_add_i32 s98, s98, 1
	v_addc_co_u32_e32 v6, vcc, 0, v6, vcc
	v_cmp_gt_i64_e32 vcc, s[20:21], v[8:9]
	v_readlane_b32 s21, v9, s98
	s_sub_i32 s20, 63, s98
	s_add_i32 s98, s98, 1
	v_addc_co_u32_e32 v6, vcc, 0, v6, vcc
	v_cmp_gt_i64_e32 vcc, s[22:23], v[8:9]
	v_readlane_b32 s23, v9, s98
	s_sub_i32 s22, 63, s98
	s_add_i32 s98, s98, 1
	v_addc_co_u32_e32 v6, vcc, 0, v6, vcc
	v_cmp_gt_i64_e32 vcc, s[20:21], v[8:9]
	v_readlane_b32 s21, v9, s98
	s_sub_i32 s20, 63, s98
	s_add_i32 s98, s98, 1
	v_addc_co_u32_e32 v6, vcc, 0, v6, vcc
	v_cmp_gt_i64_e32 vcc, s[22:23], v[8:9]
	v_readlane_b32 s23, v9, s98
	s_sub_i32 s22, 63, s98
	s_add_i32 s98, s98, 1
	v_addc_co_u32_e32 v6, vcc, 0, v6, vcc
	v_cmp_gt_i64_e32 vcc, s[20:21], v[8:9]
	v_readlane_b32 s21, v9, s98
	s_sub_i32 s20, 63, s98
	s_nop 0
	v_addc_co_u32_e32 v6, vcc, 0, v6, vcc
	v_cmp_gt_i64_e32 vcc, s[22:23], v[8:9]
	v_readlane_b32 s23, v9, s99
	s_sub_i32 s22, 63, s99
	s_add_i32 s99, s99, 1
	v_addc_co_u32_e32 v6, vcc, 0, v6, vcc
	v_cmp_gt_i64_e32 vcc, s[20:21], v[8:9]
	v_readlane_b32 s21, v9, s99
	s_sub_i32 s20, 63, s99
	s_add_i32 s99, s99, 1
	v_addc_co_u32_e32 v6, vcc, 0, v6, vcc
	v_cmp_gt_i64_e32 vcc, s[22:23], v[8:9]
	v_readlane_b32 s23, v9, s99
	s_sub_i32 s22, 63, s99
	s_add_i32 s99, s99, 1
	v_addc_co_u32_e32 v6, vcc, 0, v6, vcc
	v_cmp_gt_i64_e32 vcc, s[20:21], v[8:9]
	v_readlane_b32 s21, v9, s99
	s_sub_i32 s20, 63, s99
	s_add_i32 s99, s99, 1
	v_addc_co_u32_e32 v6, vcc, 0, v6, vcc
	v_cmp_gt_i64_e32 vcc, s[22:23], v[8:9]
	v_readlane_b32 s23, v9, s99
	s_sub_i32 s22, 63, s99
	s_add_i32 s99, s99, 1
	v_addc_co_u32_e32 v6, vcc, 0, v6, vcc
	v_cmp_gt_i64_e32 vcc, s[20:21], v[8:9]
	v_readlane_b32 s21, v9, s99
	s_sub_i32 s20, 63, s99
	s_add_i32 s99, s99, 1
	v_addc_co_u32_e32 v6, vcc, 0, v6, vcc
; __device__ __forceinline__ void phase_nrr(const Frame& F, const Args& a, int l, const bf16_t* XA, const float* g, const float* modl, unsigned char* XN8) {
;     ...
;             int rank = 0;
; #pragma unroll 8
;             for (int e2 = 0; e2 < 64; ++e2) { const float v = __int_as_float(__builtin_amdgcn_readlane(__float_as_int(val), e2)); rank += (v > val || (v == val && e2 < lane)) ? 1 : 0; }
;             const bool sel = rank < TOPK;
;             const float ssum = wave_sum(sel ? sc : 0.f);
;             if (sel) { const int p = atomicAdd((int*)(hist + lane), 1); top_e[t * TOPK + rank] = lane; gate[t * TOPK + rank] = sc / ssum * 2.5f; lpos[t * TOPK + rank] = p; }
	v_cmp_gt_i64_e32 vcc, s[22:23], v[8:9]
	v_readlane_b32 s23, v9, s99
	s_sub_i32 s22, 63, s99
	s_add_i32 s99, s99, 1
	v_addc_co_u32_e32 v6, vcc, 0, v6, vcc
	v_cmp_gt_i64_e32 vcc, s[20:21], v[8:9]
	v_readlane_b32 s21, v9, s99
	s_sub_i32 s20, 63, s99
	s_nop 0
	v_addc_co_u32_e32 v6, vcc, 0, v6, vcc
	v_cmp_gt_i64_e32 vcc, s[22:23], v[8:9]
	v_readlane_b32 s23, v9, s100
	s_sub_i32 s22, 63, s100
	s_add_i32 s100, s100, 1
	v_addc_co_u32_e32 v6, vcc, 0, v6, vcc
	v_cmp_gt_i64_e32 vcc, s[20:21], v[8:9]
	v_readlane_b32 s21, v9, s100
	s_sub_i32 s20, 63, s100
	s_add_i32 s100, s100, 1
	v_addc_co_u32_e32 v6, vcc, 0, v6, vcc
	v_cmp_gt_i64_e32 vcc, s[22:23], v[8:9]
	v_readlane_b32 s23, v9, s100
	s_sub_i32 s22, 63, s100
	s_add_i32 s100, s100, 1
	v_addc_co_u32_e32 v6, vcc, 0, v6, vcc
	v_cmp_gt_i64_e32 vcc, s[20:21], v[8:9]
	v_readlane_b32 s21, v9, s100
	s_sub_i32 s20, 63, s100
	s_add_i32 s100, s100, 1
	v_addc_co_u32_e32 v6, vcc, 0, v6, vcc
	v_cmp_gt_i64_e32 vcc, s[22:23], v[8:9]
	v_readlane_b32 s23, v9, s100
	s_sub_i32 s22, 63, s100
	s_add_i32 s100, s100, 1
	v_addc_co_u32_e32 v6, vcc, 0, v6, vcc
	v_cmp_gt_i64_e32 vcc, s[20:21], v[8:9]
	v_readlane_b32 s21, v9, s100
	s_sub_i32 s20, 63, s100
	s_add_i32 s100, s100, 1
	v_addc_co_u32_e32 v6, vcc, 0, v6, vcc
	v_cmp_gt_i64_e32 vcc, s[22:23], v[8:9]
	v_readlane_b32 s23, v9, s100
	s_sub_i32 s22, 63, s100
	s_add_i32 s100, s100, 1
	v_addc_co_u32_e32 v6, vcc, 0, v6, vcc
	v_cmp_gt_i64_e32 vcc, s[20:21], v[8:9]
	v_readlane_b32 s21, v9, s100
	s_sub_i32 s20, 63, s100
	s_nop 0
	v_addc_co_u32_e32 v6, vcc, 0, v6, vcc
	v_cmp_gt_i64_e32 vcc, s[22:23], v[8:9]
	v_readlane_b32 s23, v9, s101
	s_sub_i32 s22, 63, s101
	s_add_i32 s101, s101, 1
	v_addc_co_u32_e32 v6, vcc, 0, v6, vcc
	v_cmp_gt_i64_e32 vcc, s[20:21], v[8:9]
	v_readlane_b32 s21, v9, s101
	s_sub_i32 s20, 63, s101
	s_add_i32 s101, s101, 1
	v_addc_co_u32_e32 v6, vcc, 0, v6, vcc
	v_cmp_gt_i64_e32 vcc, s[22:23], v[8:9]
	v_readlane_b32 s23, v9, s101
	s_sub_i32 s22, 63, s101
	s_add_i32 s101, s101, 1
	v_addc_co_u32_e32 v6, vcc, 0, v6, vcc
	v_cmp_gt_i64_e32 vcc, s[20:21], v[8:9]
	v_readlane_b32 s21, v9, s101
	s_sub_i32 s20, 63, s101
	s_add_i32 s101, s101, 1
	v_addc_co_u32_e32 v6, vcc, 0, v6, vcc
	v_cmp_gt_i64_e32 vcc, s[22:23], v[8:9]
	v_readlane_b32 s23, v9, s101
	s_sub_i32 s22, 63, s101
	s_add_i32 s101, s101, 1
	v_addc_co_u32_e32 v6, vcc, 0, v6, vcc
	v_cmp_gt_i64_e32 vcc, s[20:21], v[8:9]
	v_readlane_b32 s21, v9, s101
	s_sub_i32 s20, 63, s101
	s_add_i32 s101, s101, 1
	v_addc_co_u32_e32 v6, vcc, 0, v6, vcc
	v_cmp_gt_i64_e32 vcc, s[22:23], v[8:9]
	v_readlane_b32 s23, v9, s101
	s_sub_i32 s22, 63, s101
	s_add_i32 s101, s101, 1
	v_addc_co_u32_e32 v6, vcc, 0, v6, vcc
	v_cmp_gt_i64_e32 vcc, s[20:21], v[8:9]
	v_readlane_b32 s21, v9, s101
	s_sub_i32 s20, 63, s101
	s_nop 0
	v_addc_co_u32_e32 v6, vcc, 0, v6, vcc
	v_cmp_gt_i64_e32 vcc, s[22:23], v[8:9]
	s_nop 1
	v_addc_co_u32_e32 v6, vcc, 0, v6, vcc
	v_cmp_gt_i64_e32 vcc, s[20:21], v[8:9]
	s_nop 1
	v_addc_co_u32_e32 v6, vcc, 0, v6, vcc
	v_cmp_gt_u32_e32 vcc, 6, v6
	s_nop 1
	v_cndmask_b32_e32 v5, 0, v2, vcc
	s_nop 1
	v_add_f32_dpp v5, v5, v5 quad_perm:[1,0,3,2] row_mask:0xf bank_mask:0xf
	s_nop 1
	v_add_f32_dpp v5, v5, v5 quad_perm:[2,3,0,1] row_mask:0xf bank_mask:0xf
	s_nop 1
	v_add_f32_dpp v5, v5, v5 row_half_mirror row_mask:0xf bank_mask:0xf
	s_nop 1
	v_add_f32_dpp v5, v5, v5 row_mirror row_mask:0xf bank_mask:0xf
	s_nop 0
	ds_bpermute_b32 v7, v222, v5
	s_waitcnt lgkmcnt(0)
	v_add_f32_e32 v5, v5, v7
	v_mov_b32_e32 v7, v5
	s_nop 1
	v_permlane32_swap_b32_e32 v7, v5
	s_and_saveexec_b64 s[4:5], vcc
	s_cbranch_execz .LBB0_1328
	s_waitcnt lgkmcnt(0)
	v_add_f32_e32 v5, v5, v7
	s_mul_i32 s2, s2, 6
	v_or_b32_e32 v6, s2, v6
	v_div_scale_f32 v11, s[2:3], v5, v5, v2
	v_rcp_f32_e32 v12, v11
	v_ashrrev_i32_e32 v7, 31, v6
	v_lshlrev_b64 v[6:7], 2, v[6:7]
	v_lshl_add_u64 v[8:9], s[42:43], 0, v[6:7]
	ds_add_rtn_u32 v10, v227, v243
	global_store_dword v[8:9], v230, off
	v_fma_f32 v8, -v11, v12, 1.0
	v_fmac_f32_e32 v12, v8, v12
	v_div_scale_f32 v8, vcc, v2, v5, v2
	v_mul_f32_e32 v9, v8, v12
	v_fma_f32 v13, -v11, v9, v8
	v_fmac_f32_e32 v9, v13, v12
	v_fma_f32 v8, -v11, v9, v8
	v_div_fmas_f32 v8, v8, v12, v9
	v_div_fixup_f32 v2, v8, v5, v2
	v_mul_f32_e32 v2, 0x40200000, v2
	v_lshl_add_u64 v[8:9], s[44:45], 0, v[6:7]
	v_lshl_add_u64 v[6:7], s[46:47], 0, v[6:7]
	global_store_dword v[8:9], v2, off
	s_waitcnt lgkmcnt(0)
	global_store_dword v[6:7], v10, off
; __device__ __forceinline__ void phase_nrr(const Frame& F, const Args& a, int l, const bf16_t* XA, const float* g, const float* modl, unsigned char* XN8) {
;     ...
;         for (int i = 0; i < 8; ++i) { const int t = tb + i;
;             const float lg = Pl[(w * 8 + i) * NE + lane] + Pl[(64 + w * 8 + i) * NE + lane]; const float sc = 1.f / (1.f + __expf(-lg)); const float bb = sc + bias;
;             float m1 = bb; m1 = fmaxf(m1, __shfl_xor(m1, 1)); m1 = fmaxf(m1, __shfl_xor(m1, 2)); m1 = fmaxf(m1, __shfl_xor(m1, 4));
;             const unsigned long long eq = __ballot(bb == m1); const int gbase = lane & ~7; const unsigned grpmask = (unsigned)((eq >> gbase) & 0xffull);
;             const int first = gbase + __builtin_ctz(grpmask);
;             float m2 = (lane == first) ? -INFINITY : bb; m2 = fmaxf(m2, __shfl_xor(m2, 1)); m2 = fmaxf(m2, __shfl_xor(m2, 2)); m2 = fmaxf(m2, __shfl_xor(m2, 4));
;             const float gsum = m1 + m2; const int gq = lane >> 3;
;             int grank = 0;
; #pragma unroll
;             for (int g2 = 0; g2 < 8; ++g2) { const float v = __int_as_float(__builtin_amdgcn_readlane(__float_as_int(gsum), g2 * 8)); grank += (v > gsum || (v == gsum && g2 < gq)) ? 1 : 0; }
;             const bool keep = grank < 4; const float val = keep ? bb : -INFINITY;
;             int rank = 0;
; #pragma unroll 8
;             for (int e2 = 0; e2 < 64; ++e2) { const float v = __int_as_float(__builtin_amdgcn_readlane(__float_as_int(val), e2)); rank += (v > val || (v == val && e2 < lane)) ? 1 : 0; }
.LBB0_1328:
	s_or_b64 exec, exec, s[4:5]
	v_add_u32_e32 v2, s80, v226
	ds_read_b32 v2, v2
	ds_read_b32 v5, v4 offset:17664
	s_waitcnt lgkmcnt(0)
	v_add_f32_e32 v2, v2, v5
	v_mul_f32_e32 v2, 0xbfb8aa3b, v2
	v_exp_f32_e32 v2, v2
	s_nop 0
	v_add_f32_e32 v2, 1.0, v2
	v_div_scale_f32 v5, s[2:3], v2, v2, 1.0
	v_rcp_f32_e32 v6, v5
	v_div_scale_f32 v7, vcc, 1.0, v2, 1.0
	s_mov_b32 s2, 0
	v_fma_f32 v8, -v5, v6, 1.0
	v_fmac_f32_e32 v6, v8, v6
	v_mul_f32_e32 v8, v7, v6
	v_fma_f32 v9, -v5, v8, v7
	v_fmac_f32_e32 v8, v9, v6
	v_fma_f32 v5, -v5, v8, v7
	v_div_fmas_f32 v5, v5, v6, v8
	v_div_fixup_f32 v2, v5, v2, 1.0
	v_add_f32_e32 v5, v3, v2
	s_nop 1
	s_waitcnt lgkmcnt(0)
	v_max_f32_dpp v6, v5, v5 quad_perm:[1,0,3,2] row_mask:0xf bank_mask:0xf
	s_nop 1
	s_waitcnt lgkmcnt(0)
	v_max_f32_dpp v6, v6, v6 quad_perm:[2,3,0,1] row_mask:0xf bank_mask:0xf
	s_nop 1
	s_waitcnt lgkmcnt(0)
	v_max_f32_dpp v8, v6, v6 row_half_mirror row_mask:0xf bank_mask:0xf
	v_cmp_eq_f32_e32 vcc, v5, v8
	s_nop 1
	v_lshrrev_b64 v[6:7], v200, vcc
	v_ffbl_b32_sdwa v6, v6 dst_sel:DWORD dst_unused:UNUSED_PAD src0_sel:BYTE_0
	v_add_u32_e32 v6, v6, v200
	v_cmp_ne_u32_e32 vcc, v230, v6
	s_nop 1
	v_cndmask_b32_e32 v6, v245, v5, vcc
	s_nop 1
	s_waitcnt lgkmcnt(0)
	v_max_f32_dpp v6, v6, v6 quad_perm:[1,0,3,2] row_mask:0xf bank_mask:0xf
	s_nop 1
	s_waitcnt lgkmcnt(0)
	v_max_f32_dpp v6, v6, v6 quad_perm:[2,3,0,1] row_mask:0xf bank_mask:0xf
	s_nop 1
	s_waitcnt lgkmcnt(0)
	v_max_f32_dpp v6, v6, v6 row_half_mirror row_mask:0xf bank_mask:0xf
	v_add_f32_e32 v6, v8, v6
	s_nop 0
	v_readlane_b32 s3, v6, 0
	v_readlane_b32 s4, v6, 8
	v_readlane_b32 s5, v6, 16
	v_cmp_eq_f32_e64 s[20:21], s3, v6
	v_cmp_gt_f32_e32 vcc, s3, v6
	v_cmp_gt_f32_e64 s[22:23], s4, v6
	v_cmp_eq_f32_e64 s[24:25], s4, v6
	v_cmp_gt_f32_e64 s[26:27], s5, v6
	v_cmp_eq_f32_e64 s[28:29], s5, v6
	s_and_b64 s[4:5], s[0:1], s[20:21]
	v_readlane_b32 s34, v6, 24
	s_and_b64 s[20:21], s[6:7], s[24:25]
	s_or_b64 s[4:5], vcc, s[4:5]
	v_readlane_b32 s40, v6, 32
	v_cmp_gt_f32_e64 s[30:31], s34, v6
	v_cmp_eq_f32_e64 s[34:35], s34, v6
	s_and_b64 s[24:25], s[8:9], s[28:29]
	v_cndmask_b32_e64 v7, 0, 1, s[4:5]
	s_or_b64 s[4:5], s[22:23], s[20:21]
	v_cmp_gt_f32_e64 s[36:37], s40, v6
	v_cmp_eq_f32_e64 s[40:41], s40, v6
	s_and_b64 s[28:29], s[10:11], s[34:35]
	v_cndmask_b32_e64 v8, 0, 1, s[4:5]
	s_or_b64 s[4:5], s[26:27], s[24:25]
	v_readlane_b32 s54, v6, 40
	s_and_b64 s[34:35], s[12:13], s[40:41]
	v_cndmask_b32_e64 v9, 0, 1, s[4:5]
	s_or_b64 s[4:5], s[30:31], s[28:29]
	v_cndmask_b32_e64 v10, 0, 1, s[4:5]
	s_or_b64 s[4:5], s[36:37], s[34:35]
	v_cmp_eq_f32_e64 s[20:21], s54, v6
	v_cndmask_b32_e64 v11, 0, 1, s[4:5]
	v_cmp_gt_f32_e32 vcc, s54, v6
	s_and_b64 s[4:5], s[14:15], s[20:21]
	v_readlane_b32 s3, v6, 48
	s_or_b64 s[4:5], vcc, s[4:5]
	v_cndmask_b32_e64 v12, 0, 1, s[4:5]
	v_cmp_eq_f32_e64 s[20:21], s3, v6
	v_cmp_gt_f32_e32 vcc, s3, v6
	s_and_b64 s[4:5], s[16:17], s[20:21]
	v_readlane_b32 s3, v6, 56
	s_or_b64 s[4:5], vcc, s[4:5]
	v_cndmask_b32_e64 v13, 0, 1, s[4:5]
	v_cmp_gt_f32_e32 vcc, s3, v6
	s_nop 1
	v_cndmask_b32_e64 v6, 0, 1, vcc
	v_add_u32_e32 v6, v8, v6
	v_add3_u32 v6, v6, v7, v9
	v_add3_u32 v6, v6, v10, v11
	v_add3_u32 v6, v6, v12, v13
	v_cmp_eq_u32_e32 vcc, 0, v6
	s_ff1_i32_b64 s98, vcc
	v_cmp_eq_u32_e32 vcc, 1, v6
	s_ff1_i32_b64 s99, vcc
	v_cmp_eq_u32_e32 vcc, 2, v6
	s_ff1_i32_b64 s100, vcc
	v_cmp_eq_u32_e32 vcc, 3, v6
	s_ff1_i32_b64 s101, vcc
	v_cmp_gt_u32_e32 vcc, 4, v6
	v_mov_b32_e32 v6, 0
	s_nop 0
	v_cndmask_b32_e32 v5, v245, v5, vcc
	v_ashrrev_i32_e32 v9, 31, v5
	v_sub_u32_e32 v8, 63, v230
	v_and_b32_e32 v9, 0x7fffffff, v9
	v_xor_b32_e32 v9, v5, v9
	s_nop 0
	v_readlane_b32 s23, v9, s98
	s_sub_i32 s22, 63, s98
	s_add_i32 s98, s98, 1
	v_readlane_b32 s21, v9, s98
	s_sub_i32 s20, 63, s98
	s_add_i32 s98, s98, 1
	v_cmp_gt_i64_e32 vcc, s[22:23], v[8:9]
	v_readlane_b32 s23, v9, s98
	s_sub_i32 s22, 63, s98
	s_add_i32 s98, s98, 1
	v_addc_co_u32_e32 v6, vcc, 0, v6, vcc
	v_cmp_gt_i64_e32 vcc, s[20:21], v[8:9]
	v_readlane_b32 s21, v9, s98
	s_sub_i32 s20, 63, s98
	s_add_i32 s98, s98, 1
	v_addc_co_u32_e32 v6, vcc, 0, v6, vcc
	v_cmp_gt_i64_e32 vcc, s[22:23], v[8:9]
	v_readlane_b32 s23, v9, s98
	s_sub_i32 s22, 63, s98
	s_add_i32 s98, s98, 1
	v_addc_co_u32_e32 v6, vcc, 0, v6, vcc
	v_cmp_gt_i64_e32 vcc, s[20:21], v[8:9]
	v_readlane_b32 s21, v9, s98
	s_sub_i32 s20, 63, s98
	s_add_i32 s98, s98, 1
	v_addc_co_u32_e32 v6, vcc, 0, v6, vcc
	v_cmp_gt_i64_e32 vcc, s[22:23], v[8:9]
	v_readlane_b32 s23, v9, s98
	s_sub_i32 s22, 63, s98
	s_add_i32 s98, s98, 1
	v_addc_co_u32_e32 v6, vcc, 0, v6, vcc
	v_cmp_gt_i64_e32 vcc, s[20:21], v[8:9]
	v_readlane_b32 s21, v9, s98
	s_sub_i32 s20, 63, s98
	s_nop 0
	v_addc_co_u32_e32 v6, vcc, 0, v6, vcc
	v_cmp_gt_i64_e32 vcc, s[22:23], v[8:9]
	v_readlane_b32 s23, v9, s99
	s_sub_i32 s22, 63, s99
	s_add_i32 s99, s99, 1
	v_addc_co_u32_e32 v6, vcc, 0, v6, vcc
	v_cmp_gt_i64_e32 vcc, s[20:21], v[8:9]
	v_readlane_b32 s21, v9, s99
	s_sub_i32 s20, 63, s99
	s_add_i32 s99, s99, 1
	v_addc_co_u32_e32 v6, vcc, 0, v6, vcc
	v_cmp_gt_i64_e32 vcc, s[22:23], v[8:9]
	v_readlane_b32 s23, v9, s99
	s_sub_i32 s22, 63, s99
	s_add_i32 s99, s99, 1
	v_addc_co_u32_e32 v6, vcc, 0, v6, vcc
	v_cmp_gt_i64_e32 vcc, s[20:21], v[8:9]
	v_readlane_b32 s21, v9, s99
	s_sub_i32 s20, 63, s99
	s_add_i32 s99, s99, 1
	v_addc_co_u32_e32 v6, vcc, 0, v6, vcc
	v_cmp_gt_i64_e32 vcc, s[22:23], v[8:9]
	v_readlane_b32 s23, v9, s99
	s_sub_i32 s22, 63, s99
	s_add_i32 s99, s99, 1
	v_addc_co_u32_e32 v6, vcc, 0, v6, vcc
	v_cmp_gt_i64_e32 vcc, s[20:21], v[8:9]
	v_readlane_b32 s21, v9, s99
	s_sub_i32 s20, 63, s99
	s_add_i32 s99, s99, 1
	v_addc_co_u32_e32 v6, vcc, 0, v6, vcc
	v_cmp_gt_i64_e32 vcc, s[22:23], v[8:9]
; __device__ __forceinline__ void phase_nrr(const Frame& F, const Args& a, int l, const bf16_t* XA, const float* g, const float* modl, unsigned char* XN8) {
;     ...
;             int rank = 0;
; #pragma unroll 8
;             for (int e2 = 0; e2 < 64; ++e2) { const float v = __int_as_float(__builtin_amdgcn_readlane(__float_as_int(val), e2)); rank += (v > val || (v == val && e2 < lane)) ? 1 : 0; }
;             const bool sel = rank < TOPK;
;             const float ssum = wave_sum(sel ? sc : 0.f);
;             if (sel) { const int p = atomicAdd((int*)(hist + lane), 1); top_e[t * TOPK + rank] = lane; gate[t * TOPK + rank] = sc / ssum * 2.5f; lpos[t * TOPK + rank] = p; }
	v_readlane_b32 s23, v9, s99
	s_sub_i32 s22, 63, s99
	s_add_i32 s99, s99, 1
	v_addc_co_u32_e32 v6, vcc, 0, v6, vcc
	v_cmp_gt_i64_e32 vcc, s[20:21], v[8:9]
	v_readlane_b32 s21, v9, s99
	s_sub_i32 s20, 63, s99
	s_nop 0
	v_addc_co_u32_e32 v6, vcc, 0, v6, vcc
	v_cmp_gt_i64_e32 vcc, s[22:23], v[8:9]
	v_readlane_b32 s23, v9, s100
	s_sub_i32 s22, 63, s100
	s_add_i32 s100, s100, 1
	v_addc_co_u32_e32 v6, vcc, 0, v6, vcc
	v_cmp_gt_i64_e32 vcc, s[20:21], v[8:9]
	v_readlane_b32 s21, v9, s100
	s_sub_i32 s20, 63, s100
	s_add_i32 s100, s100, 1
	v_addc_co_u32_e32 v6, vcc, 0, v6, vcc
	v_cmp_gt_i64_e32 vcc, s[22:23], v[8:9]
	v_readlane_b32 s23, v9, s100
	s_sub_i32 s22, 63, s100
	s_add_i32 s100, s100, 1
	v_addc_co_u32_e32 v6, vcc, 0, v6, vcc
	v_cmp_gt_i64_e32 vcc, s[20:21], v[8:9]
	v_readlane_b32 s21, v9, s100
	s_sub_i32 s20, 63, s100
	s_add_i32 s100, s100, 1
	v_addc_co_u32_e32 v6, vcc, 0, v6, vcc
	v_cmp_gt_i64_e32 vcc, s[22:23], v[8:9]
	v_readlane_b32 s23, v9, s100
	s_sub_i32 s22, 63, s100
	s_add_i32 s100, s100, 1
	v_addc_co_u32_e32 v6, vcc, 0, v6, vcc
	v_cmp_gt_i64_e32 vcc, s[20:21], v[8:9]
	v_readlane_b32 s21, v9, s100
	s_sub_i32 s20, 63, s100
	s_add_i32 s100, s100, 1
	v_addc_co_u32_e32 v6, vcc, 0, v6, vcc
	v_cmp_gt_i64_e32 vcc, s[22:23], v[8:9]
	v_readlane_b32 s23, v9, s100
	s_sub_i32 s22, 63, s100
	s_add_i32 s100, s100, 1
	v_addc_co_u32_e32 v6, vcc, 0, v6, vcc
	v_cmp_gt_i64_e32 vcc, s[20:21], v[8:9]
	v_readlane_b32 s21, v9, s100
	s_sub_i32 s20, 63, s100
	s_nop 0
	v_addc_co_u32_e32 v6, vcc, 0, v6, vcc
	v_cmp_gt_i64_e32 vcc, s[22:23], v[8:9]
	v_readlane_b32 s23, v9, s101
	s_sub_i32 s22, 63, s101
	s_add_i32 s101, s101, 1
	v_addc_co_u32_e32 v6, vcc, 0, v6, vcc
	v_cmp_gt_i64_e32 vcc, s[20:21], v[8:9]
	v_readlane_b32 s21, v9, s101
	s_sub_i32 s20, 63, s101
	s_add_i32 s101, s101, 1
	v_addc_co_u32_e32 v6, vcc, 0, v6, vcc
	v_cmp_gt_i64_e32 vcc, s[22:23], v[8:9]
	v_readlane_b32 s23, v9, s101
	s_sub_i32 s22, 63, s101
	s_add_i32 s101, s101, 1
	v_addc_co_u32_e32 v6, vcc, 0, v6, vcc
	v_cmp_gt_i64_e32 vcc, s[20:21], v[8:9]
	v_readlane_b32 s21, v9, s101
	s_sub_i32 s20, 63, s101
	s_add_i32 s101, s101, 1
	v_addc_co_u32_e32 v6, vcc, 0, v6, vcc
	v_cmp_gt_i64_e32 vcc, s[22:23], v[8:9]
	v_readlane_b32 s23, v9, s101
	s_sub_i32 s22, 63, s101
	s_add_i32 s101, s101, 1
	v_addc_co_u32_e32 v6, vcc, 0, v6, vcc
	v_cmp_gt_i64_e32 vcc, s[20:21], v[8:9]
	v_readlane_b32 s21, v9, s101
	s_sub_i32 s20, 63, s101
	s_add_i32 s101, s101, 1
	v_addc_co_u32_e32 v6, vcc, 0, v6, vcc
	v_cmp_gt_i64_e32 vcc, s[22:23], v[8:9]
	v_readlane_b32 s23, v9, s101
	s_sub_i32 s22, 63, s101
	s_add_i32 s101, s101, 1
	v_addc_co_u32_e32 v6, vcc, 0, v6, vcc
	v_cmp_gt_i64_e32 vcc, s[20:21], v[8:9]
	v_readlane_b32 s21, v9, s101
	s_sub_i32 s20, 63, s101
	s_nop 0
	v_addc_co_u32_e32 v6, vcc, 0, v6, vcc
	v_cmp_gt_i64_e32 vcc, s[22:23], v[8:9]
	s_nop 1
	v_addc_co_u32_e32 v6, vcc, 0, v6, vcc
	v_cmp_gt_i64_e32 vcc, s[20:21], v[8:9]
	s_nop 1
	v_addc_co_u32_e32 v6, vcc, 0, v6, vcc
	v_cmp_gt_u32_e32 vcc, 6, v6
	s_nop 1
	v_cndmask_b32_e32 v5, 0, v2, vcc
	s_nop 1
	v_add_f32_dpp v5, v5, v5 quad_perm:[1,0,3,2] row_mask:0xf bank_mask:0xf
	s_nop 1
	v_add_f32_dpp v5, v5, v5 quad_perm:[2,3,0,1] row_mask:0xf bank_mask:0xf
	s_nop 1
	v_add_f32_dpp v5, v5, v5 row_half_mirror row_mask:0xf bank_mask:0xf
	s_nop 1
	v_add_f32_dpp v5, v5, v5 row_mirror row_mask:0xf bank_mask:0xf
	s_nop 0
	ds_bpermute_b32 v7, v222, v5
	s_waitcnt lgkmcnt(0)
	v_add_f32_e32 v5, v5, v7
	v_mov_b32_e32 v7, v5
	s_nop 1
	v_permlane32_swap_b32_e32 v7, v5
	s_and_saveexec_b64 s[2:3], vcc
	s_cbranch_execz .LBB0_1332
	s_waitcnt lgkmcnt(0)
	v_add_f32_e32 v5, v5, v7
	v_div_scale_f32 v11, s[4:5], v5, v5, v2
	v_add3_u32 v6, s50, 30, v6
	v_rcp_f32_e32 v12, v11
	v_ashrrev_i32_e32 v7, 31, v6
	v_lshlrev_b64 v[6:7], 2, v[6:7]
	v_lshl_add_u64 v[8:9], s[42:43], 0, v[6:7]
	ds_add_rtn_u32 v10, v227, v243
	global_store_dword v[8:9], v230, off
	v_fma_f32 v8, -v11, v12, 1.0
	v_fmac_f32_e32 v12, v8, v12
	v_div_scale_f32 v8, vcc, v2, v5, v2
	v_mul_f32_e32 v9, v8, v12
	v_fma_f32 v13, -v11, v9, v8
	v_fmac_f32_e32 v9, v13, v12
	v_fma_f32 v8, -v11, v9, v8
	v_div_fmas_f32 v8, v8, v12, v9
	v_div_fixup_f32 v2, v8, v5, v2
	v_mul_f32_e32 v2, 0x40200000, v2
	v_lshl_add_u64 v[8:9], s[44:45], 0, v[6:7]
	v_lshl_add_u64 v[6:7], s[46:47], 0, v[6:7]
	global_store_dword v[8:9], v2, off
	s_waitcnt lgkmcnt(0)
	global_store_dword v[6:7], v10, off
; __device__ __forceinline__ void phase_nrr(const Frame& F, const Args& a, int l, const bf16_t* XA, const float* g, const float* modl, unsigned char* XN8) {
;     ...
;         for (int i = 0; i < 8; ++i) { const int t = tb + i;
;             const float lg = Pl[(w * 8 + i) * NE + lane] + Pl[(64 + w * 8 + i) * NE + lane]; const float sc = 1.f / (1.f + __expf(-lg)); const float bb = sc + bias;
;             float m1 = bb; m1 = fmaxf(m1, __shfl_xor(m1, 1)); m1 = fmaxf(m1, __shfl_xor(m1, 2)); m1 = fmaxf(m1, __shfl_xor(m1, 4));
;             const unsigned long long eq = __ballot(bb == m1); const int gbase = lane & ~7; const unsigned grpmask = (unsigned)((eq >> gbase) & 0xffull);
;             const int first = gbase + __builtin_ctz(grpmask);
;             float m2 = (lane == first) ? -INFINITY : bb; m2 = fmaxf(m2, __shfl_xor(m2, 1)); m2 = fmaxf(m2, __shfl_xor(m2, 2)); m2 = fmaxf(m2, __shfl_xor(m2, 4));
;             const float gsum = m1 + m2; const int gq = lane >> 3;
;             int grank = 0;
; #pragma unroll
;             for (int g2 = 0; g2 < 8; ++g2) { const float v = __int_as_float(__builtin_amdgcn_readlane(__float_as_int(gsum), g2 * 8)); grank += (v > gsum || (v == gsum && g2 < gq)) ? 1 : 0; }
;             const bool keep = grank < 4; const float val = keep ? bb : -INFINITY;
;             int rank = 0;
; #pragma unroll 8
;             for (int e2 = 0; e2 < 64; ++e2) { const float v = __int_as_float(__builtin_amdgcn_readlane(__float_as_int(val), e2)); rank += (v > val || (v == val && e2 < lane)) ? 1 : 0; }
.LBB0_1332:
	s_or_b64 exec, exec, s[2:3]
	v_add_u32_e32 v2, s81, v226
	ds_read_b32 v2, v2
	ds_read_b32 v5, v4 offset:17920
	s_waitcnt lgkmcnt(0)
	v_add_f32_e32 v2, v2, v5
	v_mul_f32_e32 v2, 0xbfb8aa3b, v2
	v_exp_f32_e32 v2, v2
	s_nop 0
	v_add_f32_e32 v2, 1.0, v2
	v_div_scale_f32 v5, s[2:3], v2, v2, 1.0
	v_rcp_f32_e32 v6, v5
	v_div_scale_f32 v7, vcc, 1.0, v2, 1.0
	s_mov_b32 s2, 0
	v_fma_f32 v8, -v5, v6, 1.0
	v_fmac_f32_e32 v6, v8, v6
	v_mul_f32_e32 v8, v7, v6
	v_fma_f32 v9, -v5, v8, v7
	v_fmac_f32_e32 v8, v9, v6
	v_fma_f32 v5, -v5, v8, v7
	v_div_fmas_f32 v5, v5, v6, v8
	v_div_fixup_f32 v2, v5, v2, 1.0
	v_add_f32_e32 v5, v3, v2
	s_nop 1
	s_waitcnt lgkmcnt(0)
	v_max_f32_dpp v6, v5, v5 quad_perm:[1,0,3,2] row_mask:0xf bank_mask:0xf
	s_nop 1
	s_waitcnt lgkmcnt(0)
	v_max_f32_dpp v6, v6, v6 quad_perm:[2,3,0,1] row_mask:0xf bank_mask:0xf
	s_nop 1
	s_waitcnt lgkmcnt(0)
	v_max_f32_dpp v8, v6, v6 row_half_mirror row_mask:0xf bank_mask:0xf
	v_cmp_eq_f32_e32 vcc, v5, v8
	s_nop 1
	v_lshrrev_b64 v[6:7], v200, vcc
	v_ffbl_b32_sdwa v6, v6 dst_sel:DWORD dst_unused:UNUSED_PAD src0_sel:BYTE_0
	v_add_u32_e32 v6, v6, v200
	v_cmp_ne_u32_e32 vcc, v230, v6
	s_nop 1
	v_cndmask_b32_e32 v6, v245, v5, vcc
	s_nop 1
	s_waitcnt lgkmcnt(0)
	v_max_f32_dpp v6, v6, v6 quad_perm:[1,0,3,2] row_mask:0xf bank_mask:0xf
	s_nop 1
	s_waitcnt lgkmcnt(0)
	v_max_f32_dpp v6, v6, v6 quad_perm:[2,3,0,1] row_mask:0xf bank_mask:0xf
	s_nop 1
	s_waitcnt lgkmcnt(0)
	v_max_f32_dpp v6, v6, v6 row_half_mirror row_mask:0xf bank_mask:0xf
	v_add_f32_e32 v6, v8, v6
	s_nop 0
	v_readlane_b32 s3, v6, 0
	v_readlane_b32 s4, v6, 8
	v_readlane_b32 s5, v6, 16
	v_cmp_eq_f32_e64 s[20:21], s3, v6
	v_cmp_gt_f32_e32 vcc, s3, v6
	v_cmp_gt_f32_e64 s[22:23], s4, v6
	v_cmp_eq_f32_e64 s[24:25], s4, v6
	v_cmp_gt_f32_e64 s[26:27], s5, v6
	v_cmp_eq_f32_e64 s[28:29], s5, v6
	s_and_b64 s[4:5], s[0:1], s[20:21]
	v_readlane_b32 s34, v6, 24
	s_and_b64 s[20:21], s[6:7], s[24:25]
	s_or_b64 s[4:5], vcc, s[4:5]
	v_readlane_b32 s40, v6, 32
	v_cmp_gt_f32_e64 s[30:31], s34, v6
	v_cmp_eq_f32_e64 s[34:35], s34, v6
	s_and_b64 s[24:25], s[8:9], s[28:29]
	v_cndmask_b32_e64 v7, 0, 1, s[4:5]
	s_or_b64 s[4:5], s[22:23], s[20:21]
	v_cmp_gt_f32_e64 s[36:37], s40, v6
	v_cmp_eq_f32_e64 s[40:41], s40, v6
	s_and_b64 s[28:29], s[10:11], s[34:35]
	v_cndmask_b32_e64 v8, 0, 1, s[4:5]
	s_or_b64 s[4:5], s[26:27], s[24:25]
	v_readlane_b32 s54, v6, 40
	s_and_b64 s[34:35], s[12:13], s[40:41]
	v_cndmask_b32_e64 v9, 0, 1, s[4:5]
	s_or_b64 s[4:5], s[30:31], s[28:29]
	v_cndmask_b32_e64 v10, 0, 1, s[4:5]
	s_or_b64 s[4:5], s[36:37], s[34:35]
	v_cmp_eq_f32_e64 s[20:21], s54, v6
	v_cndmask_b32_e64 v11, 0, 1, s[4:5]
	v_cmp_gt_f32_e32 vcc, s54, v6
	s_and_b64 s[4:5], s[14:15], s[20:21]
	v_readlane_b32 s3, v6, 48
	s_or_b64 s[4:5], vcc, s[4:5]
	v_cndmask_b32_e64 v12, 0, 1, s[4:5]
	v_cmp_eq_f32_e64 s[20:21], s3, v6
	v_cmp_gt_f32_e32 vcc, s3, v6
	s_and_b64 s[4:5], s[16:17], s[20:21]
	v_readlane_b32 s3, v6, 56
	s_or_b64 s[4:5], vcc, s[4:5]
	v_cndmask_b32_e64 v13, 0, 1, s[4:5]
	v_cmp_gt_f32_e32 vcc, s3, v6
	s_nop 1
	v_cndmask_b32_e64 v6, 0, 1, vcc
	v_add_u32_e32 v6, v8, v6
	v_add3_u32 v6, v6, v7, v9
	v_add3_u32 v6, v6, v10, v11
	v_add3_u32 v6, v6, v12, v13
	v_cmp_eq_u32_e32 vcc, 0, v6
	s_ff1_i32_b64 s98, vcc
	v_cmp_eq_u32_e32 vcc, 1, v6
	s_ff1_i32_b64 s99, vcc
	v_cmp_eq_u32_e32 vcc, 2, v6
	s_ff1_i32_b64 s100, vcc
	v_cmp_eq_u32_e32 vcc, 3, v6
	s_ff1_i32_b64 s101, vcc
	v_cmp_gt_u32_e32 vcc, 4, v6
	v_mov_b32_e32 v6, 0
	s_nop 0
	v_cndmask_b32_e32 v5, v245, v5, vcc
	v_ashrrev_i32_e32 v9, 31, v5
	v_sub_u32_e32 v8, 63, v230
	v_and_b32_e32 v9, 0x7fffffff, v9
	v_xor_b32_e32 v9, v5, v9
	s_nop 0
	v_readlane_b32 s23, v9, s98
	s_sub_i32 s22, 63, s98
	s_add_i32 s98, s98, 1
	v_readlane_b32 s21, v9, s98
	s_sub_i32 s20, 63, s98
	s_add_i32 s98, s98, 1
	v_cmp_gt_i64_e32 vcc, s[22:23], v[8:9]
	v_readlane_b32 s23, v9, s98
	s_sub_i32 s22, 63, s98
	s_add_i32 s98, s98, 1
	v_addc_co_u32_e32 v6, vcc, 0, v6, vcc
	v_cmp_gt_i64_e32 vcc, s[20:21], v[8:9]
	v_readlane_b32 s21, v9, s98
	s_sub_i32 s20, 63, s98
	s_add_i32 s98, s98, 1
	v_addc_co_u32_e32 v6, vcc, 0, v6, vcc
	v_cmp_gt_i64_e32 vcc, s[22:23], v[8:9]
	v_readlane_b32 s23, v9, s98
	s_sub_i32 s22, 63, s98
	s_add_i32 s98, s98, 1
	v_addc_co_u32_e32 v6, vcc, 0, v6, vcc
	v_cmp_gt_i64_e32 vcc, s[20:21], v[8:9]
	v_readlane_b32 s21, v9, s98
	s_sub_i32 s20, 63, s98
	s_add_i32 s98, s98, 1
	v_addc_co_u32_e32 v6, vcc, 0, v6, vcc
	v_cmp_gt_i64_e32 vcc, s[22:23], v[8:9]
	v_readlane_b32 s23, v9, s98
	s_sub_i32 s22, 63, s98
	s_add_i32 s98, s98, 1
	v_addc_co_u32_e32 v6, vcc, 0, v6, vcc
	v_cmp_gt_i64_e32 vcc, s[20:21], v[8:9]
	v_readlane_b32 s21, v9, s98
	s_sub_i32 s20, 63, s98
	s_nop 0
	v_addc_co_u32_e32 v6, vcc, 0, v6, vcc
	v_cmp_gt_i64_e32 vcc, s[22:23], v[8:9]
	v_readlane_b32 s23, v9, s99
	s_sub_i32 s22, 63, s99
	s_add_i32 s99, s99, 1
	v_addc_co_u32_e32 v6, vcc, 0, v6, vcc
	v_cmp_gt_i64_e32 vcc, s[20:21], v[8:9]
	v_readlane_b32 s21, v9, s99
	s_sub_i32 s20, 63, s99
	s_add_i32 s99, s99, 1
	v_addc_co_u32_e32 v6, vcc, 0, v6, vcc
	v_cmp_gt_i64_e32 vcc, s[22:23], v[8:9]
	v_readlane_b32 s23, v9, s99
	s_sub_i32 s22, 63, s99
	s_add_i32 s99, s99, 1
	v_addc_co_u32_e32 v6, vcc, 0, v6, vcc
	v_cmp_gt_i64_e32 vcc, s[20:21], v[8:9]
	v_readlane_b32 s21, v9, s99
	s_sub_i32 s20, 63, s99
	s_add_i32 s99, s99, 1
	v_addc_co_u32_e32 v6, vcc, 0, v6, vcc
	v_cmp_gt_i64_e32 vcc, s[22:23], v[8:9]
	v_readlane_b32 s23, v9, s99
	s_sub_i32 s22, 63, s99
	s_add_i32 s99, s99, 1
	v_addc_co_u32_e32 v6, vcc, 0, v6, vcc
	v_cmp_gt_i64_e32 vcc, s[20:21], v[8:9]
	v_readlane_b32 s21, v9, s99
	s_sub_i32 s20, 63, s99
	s_add_i32 s99, s99, 1
	v_addc_co_u32_e32 v6, vcc, 0, v6, vcc
	v_cmp_gt_i64_e32 vcc, s[22:23], v[8:9]
; __device__ __forceinline__ void phase_nrr(const Frame& F, const Args& a, int l, const bf16_t* XA, const float* g, const float* modl, unsigned char* XN8) {
;     ...
;             int rank = 0;
; #pragma unroll 8
;             for (int e2 = 0; e2 < 64; ++e2) { const float v = __int_as_float(__builtin_amdgcn_readlane(__float_as_int(val), e2)); rank += (v > val || (v == val && e2 < lane)) ? 1 : 0; }
;             const bool sel = rank < TOPK;
;             const float ssum = wave_sum(sel ? sc : 0.f);
;             if (sel) { const int p = atomicAdd((int*)(hist + lane), 1); top_e[t * TOPK + rank] = lane; gate[t * TOPK + rank] = sc / ssum * 2.5f; lpos[t * TOPK + rank] = p; }
	v_readlane_b32 s23, v9, s99
	s_sub_i32 s22, 63, s99
	s_add_i32 s99, s99, 1
	v_addc_co_u32_e32 v6, vcc, 0, v6, vcc
	v_cmp_gt_i64_e32 vcc, s[20:21], v[8:9]
	v_readlane_b32 s21, v9, s99
	s_sub_i32 s20, 63, s99
	s_nop 0
	v_addc_co_u32_e32 v6, vcc, 0, v6, vcc
	v_cmp_gt_i64_e32 vcc, s[22:23], v[8:9]
	v_readlane_b32 s23, v9, s100
	s_sub_i32 s22, 63, s100
	s_add_i32 s100, s100, 1
	v_addc_co_u32_e32 v6, vcc, 0, v6, vcc
	v_cmp_gt_i64_e32 vcc, s[20:21], v[8:9]
	v_readlane_b32 s21, v9, s100
	s_sub_i32 s20, 63, s100
	s_add_i32 s100, s100, 1
	v_addc_co_u32_e32 v6, vcc, 0, v6, vcc
	v_cmp_gt_i64_e32 vcc, s[22:23], v[8:9]
	v_readlane_b32 s23, v9, s100
	s_sub_i32 s22, 63, s100
	s_add_i32 s100, s100, 1
	v_addc_co_u32_e32 v6, vcc, 0, v6, vcc
	v_cmp_gt_i64_e32 vcc, s[20:21], v[8:9]
	v_readlane_b32 s21, v9, s100
	s_sub_i32 s20, 63, s100
	s_add_i32 s100, s100, 1
	v_addc_co_u32_e32 v6, vcc, 0, v6, vcc
	v_cmp_gt_i64_e32 vcc, s[22:23], v[8:9]
	v_readlane_b32 s23, v9, s100
	s_sub_i32 s22, 63, s100
	s_add_i32 s100, s100, 1
	v_addc_co_u32_e32 v6, vcc, 0, v6, vcc
	v_cmp_gt_i64_e32 vcc, s[20:21], v[8:9]
	v_readlane_b32 s21, v9, s100
	s_sub_i32 s20, 63, s100
	s_add_i32 s100, s100, 1
	v_addc_co_u32_e32 v6, vcc, 0, v6, vcc
	v_cmp_gt_i64_e32 vcc, s[22:23], v[8:9]
	v_readlane_b32 s23, v9, s100
	s_sub_i32 s22, 63, s100
	s_add_i32 s100, s100, 1
	v_addc_co_u32_e32 v6, vcc, 0, v6, vcc
	v_cmp_gt_i64_e32 vcc, s[20:21], v[8:9]
	v_readlane_b32 s21, v9, s100
	s_sub_i32 s20, 63, s100
	s_nop 0
	v_addc_co_u32_e32 v6, vcc, 0, v6, vcc
	v_cmp_gt_i64_e32 vcc, s[22:23], v[8:9]
	v_readlane_b32 s23, v9, s101
	s_sub_i32 s22, 63, s101
	s_add_i32 s101, s101, 1
	v_addc_co_u32_e32 v6, vcc, 0, v6, vcc
	v_cmp_gt_i64_e32 vcc, s[20:21], v[8:9]
	v_readlane_b32 s21, v9, s101
	s_sub_i32 s20, 63, s101
	s_add_i32 s101, s101, 1
	v_addc_co_u32_e32 v6, vcc, 0, v6, vcc
	v_cmp_gt_i64_e32 vcc, s[22:23], v[8:9]
	v_readlane_b32 s23, v9, s101
	s_sub_i32 s22, 63, s101
	s_add_i32 s101, s101, 1
	v_addc_co_u32_e32 v6, vcc, 0, v6, vcc
	v_cmp_gt_i64_e32 vcc, s[20:21], v[8:9]
	v_readlane_b32 s21, v9, s101
	s_sub_i32 s20, 63, s101
	s_add_i32 s101, s101, 1
	v_addc_co_u32_e32 v6, vcc, 0, v6, vcc
	v_cmp_gt_i64_e32 vcc, s[22:23], v[8:9]
	v_readlane_b32 s23, v9, s101
	s_sub_i32 s22, 63, s101
	s_add_i32 s101, s101, 1
	v_addc_co_u32_e32 v6, vcc, 0, v6, vcc
	v_cmp_gt_i64_e32 vcc, s[20:21], v[8:9]
	v_readlane_b32 s21, v9, s101
	s_sub_i32 s20, 63, s101
	s_add_i32 s101, s101, 1
	v_addc_co_u32_e32 v6, vcc, 0, v6, vcc
	v_cmp_gt_i64_e32 vcc, s[22:23], v[8:9]
	v_readlane_b32 s23, v9, s101
	s_sub_i32 s22, 63, s101
	s_add_i32 s101, s101, 1
	v_addc_co_u32_e32 v6, vcc, 0, v6, vcc
	v_cmp_gt_i64_e32 vcc, s[20:21], v[8:9]
	v_readlane_b32 s21, v9, s101
	s_sub_i32 s20, 63, s101
	s_nop 0
	v_addc_co_u32_e32 v6, vcc, 0, v6, vcc
	v_cmp_gt_i64_e32 vcc, s[22:23], v[8:9]
	s_nop 1
	v_addc_co_u32_e32 v6, vcc, 0, v6, vcc
	v_cmp_gt_i64_e32 vcc, s[20:21], v[8:9]
	s_nop 1
	v_addc_co_u32_e32 v6, vcc, 0, v6, vcc
	v_cmp_gt_u32_e32 vcc, 6, v6
	s_nop 1
	v_cndmask_b32_e32 v5, 0, v2, vcc
	s_nop 1
	v_add_f32_dpp v5, v5, v5 quad_perm:[1,0,3,2] row_mask:0xf bank_mask:0xf
	s_nop 1
	v_add_f32_dpp v5, v5, v5 quad_perm:[2,3,0,1] row_mask:0xf bank_mask:0xf
	s_nop 1
	v_add_f32_dpp v5, v5, v5 row_half_mirror row_mask:0xf bank_mask:0xf
	s_nop 1
	v_add_f32_dpp v5, v5, v5 row_mirror row_mask:0xf bank_mask:0xf
	s_nop 0
	ds_bpermute_b32 v7, v222, v5
	s_waitcnt lgkmcnt(0)
	v_add_f32_e32 v5, v5, v7
	v_mov_b32_e32 v7, v5
	s_nop 1
	v_permlane32_swap_b32_e32 v7, v5
	s_and_saveexec_b64 s[2:3], vcc
	s_cbranch_execz .LBB0_1336
	s_waitcnt lgkmcnt(0)
	v_add_f32_e32 v5, v5, v7
	v_div_scale_f32 v11, s[4:5], v5, v5, v2
	v_add3_u32 v6, s50, 36, v6
	v_rcp_f32_e32 v12, v11
	v_ashrrev_i32_e32 v7, 31, v6
	v_lshlrev_b64 v[6:7], 2, v[6:7]
	v_lshl_add_u64 v[8:9], s[42:43], 0, v[6:7]
	ds_add_rtn_u32 v10, v227, v243
	global_store_dword v[8:9], v230, off
	v_fma_f32 v8, -v11, v12, 1.0
	v_fmac_f32_e32 v12, v8, v12
	v_div_scale_f32 v8, vcc, v2, v5, v2
	v_mul_f32_e32 v9, v8, v12
	v_fma_f32 v13, -v11, v9, v8
	v_fmac_f32_e32 v9, v13, v12
	v_fma_f32 v8, -v11, v9, v8
	v_div_fmas_f32 v8, v8, v12, v9
	v_div_fixup_f32 v2, v8, v5, v2
	v_mul_f32_e32 v2, 0x40200000, v2
	v_lshl_add_u64 v[8:9], s[44:45], 0, v[6:7]
	v_lshl_add_u64 v[6:7], s[46:47], 0, v[6:7]
	global_store_dword v[8:9], v2, off
	s_waitcnt lgkmcnt(0)
	global_store_dword v[6:7], v10, off
; __device__ __forceinline__ void phase_nrr(const Frame& F, const Args& a, int l, const bf16_t* XA, const float* g, const float* modl, unsigned char* XN8) {
;     ...
;         for (int i = 0; i < 8; ++i) { const int t = tb + i;
;             const float lg = Pl[(w * 8 + i) * NE + lane] + Pl[(64 + w * 8 + i) * NE + lane]; const float sc = 1.f / (1.f + __expf(-lg)); const float bb = sc + bias;
;             float m1 = bb; m1 = fmaxf(m1, __shfl_xor(m1, 1)); m1 = fmaxf(m1, __shfl_xor(m1, 2)); m1 = fmaxf(m1, __shfl_xor(m1, 4));
;             const unsigned long long eq = __ballot(bb == m1); const int gbase = lane & ~7; const unsigned grpmask = (unsigned)((eq >> gbase) & 0xffull);
;             const int first = gbase + __builtin_ctz(grpmask);
;             float m2 = (lane == first) ? -INFINITY : bb; m2 = fmaxf(m2, __shfl_xor(m2, 1)); m2 = fmaxf(m2, __shfl_xor(m2, 2)); m2 = fmaxf(m2, __shfl_xor(m2, 4));
;             const float gsum = m1 + m2; const int gq = lane >> 3;
;             int grank = 0;
; #pragma unroll
;             for (int g2 = 0; g2 < 8; ++g2) { const float v = __int_as_float(__builtin_amdgcn_readlane(__float_as_int(gsum), g2 * 8)); grank += (v > gsum || (v == gsum && g2 < gq)) ? 1 : 0; }
;             const bool keep = grank < 4; const float val = keep ? bb : -INFINITY;
;             int rank = 0;
; #pragma unroll 8
;             for (int e2 = 0; e2 < 64; ++e2) { const float v = __int_as_float(__builtin_amdgcn_readlane(__float_as_int(val), e2)); rank += (v > val || (v == val && e2 < lane)) ? 1 : 0; }
.LBB0_1336:
	s_or_b64 exec, exec, s[2:3]
	v_add_u32_e32 v2, s82, v226
	ds_read_b32 v2, v2
	ds_read_b32 v4, v4 offset:18176
	s_waitcnt lgkmcnt(0)
	v_add_f32_e32 v2, v2, v4
	v_mul_f32_e32 v2, 0xbfb8aa3b, v2
	v_exp_f32_e32 v2, v2
	s_nop 0
	v_add_f32_e32 v2, 1.0, v2
	v_div_scale_f32 v4, s[2:3], v2, v2, 1.0
	v_rcp_f32_e32 v5, v4
	v_div_scale_f32 v6, vcc, 1.0, v2, 1.0
	s_mov_b32 s2, 0
	v_fma_f32 v7, -v4, v5, 1.0
	v_fmac_f32_e32 v5, v7, v5
	v_mul_f32_e32 v7, v6, v5
	v_fma_f32 v8, -v4, v7, v6
	v_fmac_f32_e32 v7, v8, v5
	v_fma_f32 v4, -v4, v7, v6
	v_div_fmas_f32 v4, v4, v5, v7
	v_div_fixup_f32 v2, v4, v2, 1.0
	v_add_f32_e32 v3, v3, v2
	s_nop 1
	s_waitcnt lgkmcnt(0)
	v_max_f32_dpp v4, v3, v3 quad_perm:[1,0,3,2] row_mask:0xf bank_mask:0xf
	s_nop 1
	s_waitcnt lgkmcnt(0)
	v_max_f32_dpp v4, v4, v4 quad_perm:[2,3,0,1] row_mask:0xf bank_mask:0xf
	s_nop 1
	s_waitcnt lgkmcnt(0)
	v_max_f32_dpp v6, v4, v4 row_half_mirror row_mask:0xf bank_mask:0xf
	v_cmp_eq_f32_e32 vcc, v3, v6
	s_nop 1
	v_lshrrev_b64 v[4:5], v200, vcc
	v_ffbl_b32_sdwa v4, v4 dst_sel:DWORD dst_unused:UNUSED_PAD src0_sel:BYTE_0
	v_add_u32_e32 v4, v4, v200
	v_cmp_ne_u32_e32 vcc, v230, v4
	s_nop 1
	v_cndmask_b32_e32 v4, v245, v3, vcc
	s_nop 1
	s_waitcnt lgkmcnt(0)
	v_max_f32_dpp v4, v4, v4 quad_perm:[1,0,3,2] row_mask:0xf bank_mask:0xf
	s_nop 1
	s_waitcnt lgkmcnt(0)
	v_max_f32_dpp v4, v4, v4 quad_perm:[2,3,0,1] row_mask:0xf bank_mask:0xf
	s_nop 1
	s_waitcnt lgkmcnt(0)
	v_max_f32_dpp v4, v4, v4 row_half_mirror row_mask:0xf bank_mask:0xf
	v_add_f32_e32 v4, v6, v4
	s_nop 0
	v_readlane_b32 s3, v4, 0
	v_readlane_b32 s4, v4, 8
	v_readlane_b32 s5, v4, 16
	v_cmp_eq_f32_e64 s[20:21], s3, v4
	v_cmp_gt_f32_e32 vcc, s3, v4
	v_cmp_gt_f32_e64 s[22:23], s4, v4
	v_cmp_eq_f32_e64 s[24:25], s4, v4
	v_cmp_gt_f32_e64 s[26:27], s5, v4
	v_cmp_eq_f32_e64 s[28:29], s5, v4
	s_and_b64 s[4:5], s[0:1], s[20:21]
	v_readlane_b32 s34, v4, 24
	s_and_b64 s[20:21], s[6:7], s[24:25]
	s_or_b64 s[4:5], vcc, s[4:5]
	v_readlane_b32 s40, v4, 32
	v_cmp_gt_f32_e64 s[30:31], s34, v4
	v_cmp_eq_f32_e64 s[34:35], s34, v4
	s_and_b64 s[24:25], s[8:9], s[28:29]
	v_cndmask_b32_e64 v5, 0, 1, s[4:5]
	s_or_b64 s[4:5], s[22:23], s[20:21]
	v_cmp_gt_f32_e64 s[36:37], s40, v4
	v_cmp_eq_f32_e64 s[40:41], s40, v4
	s_and_b64 s[28:29], s[10:11], s[34:35]
	v_cndmask_b32_e64 v6, 0, 1, s[4:5]
	s_or_b64 s[4:5], s[26:27], s[24:25]
	v_readlane_b32 s54, v4, 40
	s_and_b64 s[34:35], s[12:13], s[40:41]
	v_cndmask_b32_e64 v7, 0, 1, s[4:5]
	s_or_b64 s[4:5], s[30:31], s[28:29]
	v_cndmask_b32_e64 v8, 0, 1, s[4:5]
	s_or_b64 s[4:5], s[36:37], s[34:35]
	v_cmp_eq_f32_e64 s[20:21], s54, v4
	v_cndmask_b32_e64 v9, 0, 1, s[4:5]
	v_cmp_gt_f32_e32 vcc, s54, v4
	s_and_b64 s[4:5], s[14:15], s[20:21]
	v_readlane_b32 s3, v4, 48
	s_or_b64 s[4:5], vcc, s[4:5]
	v_cndmask_b32_e64 v10, 0, 1, s[4:5]
	v_cmp_eq_f32_e64 s[20:21], s3, v4
	v_cmp_gt_f32_e32 vcc, s3, v4
	s_and_b64 s[4:5], s[16:17], s[20:21]
	v_readlane_b32 s3, v4, 56
	s_or_b64 s[4:5], vcc, s[4:5]
	v_cndmask_b32_e64 v11, 0, 1, s[4:5]
	v_cmp_gt_f32_e32 vcc, s3, v4
	s_nop 1
	v_cndmask_b32_e64 v4, 0, 1, vcc
	v_add_u32_e32 v4, v6, v4
	v_add3_u32 v4, v4, v5, v7
	v_add3_u32 v4, v4, v8, v9
	v_add3_u32 v4, v4, v10, v11
	v_cmp_eq_u32_e32 vcc, 0, v4
	s_ff1_i32_b64 s98, vcc
	v_cmp_eq_u32_e32 vcc, 1, v4
	s_ff1_i32_b64 s99, vcc
	v_cmp_eq_u32_e32 vcc, 2, v4
	s_ff1_i32_b64 s100, vcc
	v_cmp_eq_u32_e32 vcc, 3, v4
	s_ff1_i32_b64 s101, vcc
	v_cmp_gt_u32_e32 vcc, 4, v4
	v_mov_b32_e32 v4, 0
	s_nop 0
	v_cndmask_b32_e32 v3, v245, v3, vcc
	v_ashrrev_i32_e32 v9, 31, v3
	v_sub_u32_e32 v8, 63, v230
	v_and_b32_e32 v9, 0x7fffffff, v9
	v_xor_b32_e32 v9, v3, v9
	s_nop 0
	v_readlane_b32 s23, v9, s98
	s_sub_i32 s22, 63, s98
	s_add_i32 s98, s98, 1
	v_readlane_b32 s21, v9, s98
	s_sub_i32 s20, 63, s98
	s_add_i32 s98, s98, 1
	v_cmp_gt_i64_e32 vcc, s[22:23], v[8:9]
	v_readlane_b32 s23, v9, s98
	s_sub_i32 s22, 63, s98
	s_add_i32 s98, s98, 1
	v_addc_co_u32_e32 v4, vcc, 0, v4, vcc
	v_cmp_gt_i64_e32 vcc, s[20:21], v[8:9]
	v_readlane_b32 s21, v9, s98
	s_sub_i32 s20, 63, s98
	s_add_i32 s98, s98, 1
	v_addc_co_u32_e32 v4, vcc, 0, v4, vcc
	v_cmp_gt_i64_e32 vcc, s[22:23], v[8:9]
	v_readlane_b32 s23, v9, s98
	s_sub_i32 s22, 63, s98
	s_add_i32 s98, s98, 1
	v_addc_co_u32_e32 v4, vcc, 0, v4, vcc
	v_cmp_gt_i64_e32 vcc, s[20:21], v[8:9]
	v_readlane_b32 s21, v9, s98
	s_sub_i32 s20, 63, s98
	s_add_i32 s98, s98, 1
	v_addc_co_u32_e32 v4, vcc, 0, v4, vcc
	v_cmp_gt_i64_e32 vcc, s[22:23], v[8:9]
	v_readlane_b32 s23, v9, s98
	s_sub_i32 s22, 63, s98
	s_add_i32 s98, s98, 1
	v_addc_co_u32_e32 v4, vcc, 0, v4, vcc
	v_cmp_gt_i64_e32 vcc, s[20:21], v[8:9]
	v_readlane_b32 s21, v9, s98
	s_sub_i32 s20, 63, s98
	s_nop 0
	v_addc_co_u32_e32 v4, vcc, 0, v4, vcc
	v_cmp_gt_i64_e32 vcc, s[22:23], v[8:9]
	v_readlane_b32 s23, v9, s99
	s_sub_i32 s22, 63, s99
	s_add_i32 s99, s99, 1
	v_addc_co_u32_e32 v4, vcc, 0, v4, vcc
	v_cmp_gt_i64_e32 vcc, s[20:21], v[8:9]
	v_readlane_b32 s21, v9, s99
	s_sub_i32 s20, 63, s99
	s_add_i32 s99, s99, 1
	v_addc_co_u32_e32 v4, vcc, 0, v4, vcc
; __device__ __forceinline__ void phase_nrr(const Frame& F, const Args& a, int l, const bf16_t* XA, const float* g, const float* modl, unsigned char* XN8) {
;     ...
;             int rank = 0;
; #pragma unroll 8
;             for (int e2 = 0; e2 < 64; ++e2) { const float v = __int_as_float(__builtin_amdgcn_readlane(__float_as_int(val), e2)); rank += (v > val || (v == val && e2 < lane)) ? 1 : 0; }
;             const bool sel = rank < TOPK;
;             const float ssum = wave_sum(sel ? sc : 0.f);
;             if (sel) { const int p = atomicAdd((int*)(hist + lane), 1); top_e[t * TOPK + rank] = lane; gate[t * TOPK + rank] = sc / ssum * 2.5f; lpos[t * TOPK + rank] = p; }
	v_cmp_gt_i64_e32 vcc, s[22:23], v[8:9]
	v_readlane_b32 s23, v9, s99
	s_sub_i32 s22, 63, s99
	s_add_i32 s99, s99, 1
	v_addc_co_u32_e32 v4, vcc, 0, v4, vcc
	v_cmp_gt_i64_e32 vcc, s[20:21], v[8:9]
	v_readlane_b32 s21, v9, s99
	s_sub_i32 s20, 63, s99
	s_add_i32 s99, s99, 1
	v_addc_co_u32_e32 v4, vcc, 0, v4, vcc
	v_cmp_gt_i64_e32 vcc, s[22:23], v[8:9]
	v_readlane_b32 s23, v9, s99
	s_sub_i32 s22, 63, s99
	s_add_i32 s99, s99, 1
	v_addc_co_u32_e32 v4, vcc, 0, v4, vcc
	v_cmp_gt_i64_e32 vcc, s[20:21], v[8:9]
	v_readlane_b32 s21, v9, s99
	s_sub_i32 s20, 63, s99
	s_add_i32 s99, s99, 1
	v_addc_co_u32_e32 v4, vcc, 0, v4, vcc
	v_cmp_gt_i64_e32 vcc, s[22:23], v[8:9]
	v_readlane_b32 s23, v9, s99
	s_sub_i32 s22, 63, s99
	s_add_i32 s99, s99, 1
	v_addc_co_u32_e32 v4, vcc, 0, v4, vcc
	v_cmp_gt_i64_e32 vcc, s[20:21], v[8:9]
	v_readlane_b32 s21, v9, s99
	s_sub_i32 s20, 63, s99
	s_nop 0
	v_addc_co_u32_e32 v4, vcc, 0, v4, vcc
	v_cmp_gt_i64_e32 vcc, s[22:23], v[8:9]
	v_readlane_b32 s23, v9, s100
	s_sub_i32 s22, 63, s100
	s_add_i32 s100, s100, 1
	v_addc_co_u32_e32 v4, vcc, 0, v4, vcc
	v_cmp_gt_i64_e32 vcc, s[20:21], v[8:9]
	v_readlane_b32 s21, v9, s100
	s_sub_i32 s20, 63, s100
	s_add_i32 s100, s100, 1
	v_addc_co_u32_e32 v4, vcc, 0, v4, vcc
	v_cmp_gt_i64_e32 vcc, s[22:23], v[8:9]
	v_readlane_b32 s23, v9, s100
	s_sub_i32 s22, 63, s100
	s_add_i32 s100, s100, 1
	v_addc_co_u32_e32 v4, vcc, 0, v4, vcc
	v_cmp_gt_i64_e32 vcc, s[20:21], v[8:9]
	v_readlane_b32 s21, v9, s100
	s_sub_i32 s20, 63, s100
	s_add_i32 s100, s100, 1
	v_addc_co_u32_e32 v4, vcc, 0, v4, vcc
	v_cmp_gt_i64_e32 vcc, s[22:23], v[8:9]
	v_readlane_b32 s23, v9, s100
	s_sub_i32 s22, 63, s100
	s_add_i32 s100, s100, 1
	v_addc_co_u32_e32 v4, vcc, 0, v4, vcc
	v_cmp_gt_i64_e32 vcc, s[20:21], v[8:9]
	v_readlane_b32 s21, v9, s100
	s_sub_i32 s20, 63, s100
	s_add_i32 s100, s100, 1
	v_addc_co_u32_e32 v4, vcc, 0, v4, vcc
	v_cmp_gt_i64_e32 vcc, s[22:23], v[8:9]
	v_readlane_b32 s23, v9, s100
	s_sub_i32 s22, 63, s100
	s_add_i32 s100, s100, 1
	v_addc_co_u32_e32 v4, vcc, 0, v4, vcc
	v_cmp_gt_i64_e32 vcc, s[20:21], v[8:9]
	v_readlane_b32 s21, v9, s100
	s_sub_i32 s20, 63, s100
	s_nop 0
	v_addc_co_u32_e32 v4, vcc, 0, v4, vcc
	v_cmp_gt_i64_e32 vcc, s[22:23], v[8:9]
	v_readlane_b32 s23, v9, s101
	s_sub_i32 s22, 63, s101
	s_add_i32 s101, s101, 1
	v_addc_co_u32_e32 v4, vcc, 0, v4, vcc
	v_cmp_gt_i64_e32 vcc, s[20:21], v[8:9]
	v_readlane_b32 s21, v9, s101
	s_sub_i32 s20, 63, s101
	s_add_i32 s101, s101, 1
	v_addc_co_u32_e32 v4, vcc, 0, v4, vcc
	v_cmp_gt_i64_e32 vcc, s[22:23], v[8:9]
	v_readlane_b32 s23, v9, s101
	s_sub_i32 s22, 63, s101
	s_add_i32 s101, s101, 1
	v_addc_co_u32_e32 v4, vcc, 0, v4, vcc
	v_cmp_gt_i64_e32 vcc, s[20:21], v[8:9]
	v_readlane_b32 s21, v9, s101
	s_sub_i32 s20, 63, s101
	s_add_i32 s101, s101, 1
	v_addc_co_u32_e32 v4, vcc, 0, v4, vcc
	v_cmp_gt_i64_e32 vcc, s[22:23], v[8:9]
	v_readlane_b32 s23, v9, s101
	s_sub_i32 s22, 63, s101
	s_add_i32 s101, s101, 1
	v_addc_co_u32_e32 v4, vcc, 0, v4, vcc
	v_cmp_gt_i64_e32 vcc, s[20:21], v[8:9]
	v_readlane_b32 s21, v9, s101
	s_sub_i32 s20, 63, s101
	s_add_i32 s101, s101, 1
	v_addc_co_u32_e32 v4, vcc, 0, v4, vcc
	v_cmp_gt_i64_e32 vcc, s[22:23], v[8:9]
	v_readlane_b32 s23, v9, s101
	s_sub_i32 s22, 63, s101
	s_add_i32 s101, s101, 1
	v_addc_co_u32_e32 v4, vcc, 0, v4, vcc
	v_cmp_gt_i64_e32 vcc, s[20:21], v[8:9]
	v_readlane_b32 s21, v9, s101
	s_sub_i32 s20, 63, s101
	s_nop 0
	v_addc_co_u32_e32 v4, vcc, 0, v4, vcc
	v_cmp_gt_i64_e32 vcc, s[22:23], v[8:9]
	s_nop 1
	v_addc_co_u32_e32 v4, vcc, 0, v4, vcc
	v_cmp_gt_i64_e32 vcc, s[20:21], v[8:9]
	s_nop 1
	v_addc_co_u32_e32 v4, vcc, 0, v4, vcc
	v_cmp_gt_u32_e32 vcc, 6, v4
	s_nop 1
	v_cndmask_b32_e32 v3, 0, v2, vcc
	s_nop 1
	v_add_f32_dpp v3, v3, v3 quad_perm:[1,0,3,2] row_mask:0xf bank_mask:0xf
	s_nop 1
	v_add_f32_dpp v3, v3, v3 quad_perm:[2,3,0,1] row_mask:0xf bank_mask:0xf
	s_nop 1
	v_add_f32_dpp v3, v3, v3 row_half_mirror row_mask:0xf bank_mask:0xf
	s_nop 1
	v_add_f32_dpp v3, v3, v3 row_mirror row_mask:0xf bank_mask:0xf
	s_nop 0
	ds_bpermute_b32 v5, v222, v3
	s_waitcnt lgkmcnt(0)
	v_add_f32_e32 v3, v3, v5
	v_mov_b32_e32 v5, v3
	s_nop 1
	v_permlane32_swap_b32_e32 v5, v3
	s_and_saveexec_b64 s[2:3], vcc
	s_cbranch_execz .LBB0_1340
	s_waitcnt lgkmcnt(0)
	v_add_f32_e32 v3, v3, v5
	v_div_scale_f32 v9, s[4:5], v3, v3, v2
	v_add3_u32 v4, s50, 42, v4
	v_rcp_f32_e32 v10, v9
	v_ashrrev_i32_e32 v5, 31, v4
	v_lshlrev_b64 v[4:5], 2, v[4:5]
	v_lshl_add_u64 v[6:7], s[42:43], 0, v[4:5]
	ds_add_rtn_u32 v8, v227, v243
	global_store_dword v[6:7], v230, off
	v_fma_f32 v6, -v9, v10, 1.0
	v_fmac_f32_e32 v10, v6, v10
	v_div_scale_f32 v6, vcc, v2, v3, v2
	v_mul_f32_e32 v7, v6, v10
	v_fma_f32 v11, -v9, v7, v6
	v_fmac_f32_e32 v7, v11, v10
	v_fma_f32 v6, -v9, v7, v6
	v_div_fmas_f32 v6, v6, v10, v7
	v_div_fixup_f32 v2, v6, v3, v2
	v_mul_f32_e32 v6, 0x40200000, v2
	v_lshl_add_u64 v[2:3], s[44:45], 0, v[4:5]
	global_store_dword v[2:3], v6, off
	v_lshl_add_u64 v[2:3], s[46:47], 0, v[4:5]
	s_waitcnt lgkmcnt(0)
	global_store_dword v[2:3], v8, off
